# conversion units: 16-item groups software-pipelined 4 deep in registers (DN and gate-up expert weights); diff epilogue scale and lambda loads hoisted
# speedup vs baseline: 1.0452x; 1.0019x over previous
; __device__ __forceinline__ int crow(int r, int hi) { return (r & 3) + 8 * (r >> 2) + 4 * hi; }
; __device__ __forceinline__ void diff_unit(KP Pk, Frame& F, int l, int b, int h, int qrow0, int nkt) {
;     ...
;     if (m == 0) {
;         const float* dl = Pk->in[I_DLAM] + l * 256; const float lam_init = __builtin_bit_cast(float, __builtin_amdgcn_readfirstlane(__builtin_bit_cast(int, l == 0 ? 0.2f : (0.8f - 0.6f * 0.74081822068f))));
;         const float lam = expf(wave_sum(dl[ln_] * dl[64 + ln_])) - expf(wave_sum(dl[128 + ln_] * dl[192 + ln_])) + lam_init;
;         float ssq[16];
; #pragma unroll
;         for (int r = 0; r < 16; ++r) { float a = 0.f;
; #pragma unroll
;             for (int nb = 0; nb < 4; ++nb) { const float v = O[nb][r] * rlr[r] - lam * ex[crow(r, hi) * 128 + nb * 32 + r32]; O[nb][r] = v; a += v * v; }
;             a += __shfl_xor(a, 1); a += __shfl_xor(a, 2); a += __shfl_xor(a, 4); a += __shfl_xor(a, 8); a += __shfl_xor(a, 16);
;             ssq[r] = rsqrtf(a * (1.f / 128.f) + NORM_EPS) * (1.f - lam_init); }
.LBB0_622:
	v_readlane_b32 s26, v253, 17
	v_readlane_b32 s27, v253, 18
	s_andn2_b64 vcc, exec, s[26:27]
	s_waitcnt lgkmcnt(0)
	s_barrier
	s_cbranch_vccnz .LBB0_624
	s_load_dwordx4 s[44:47], s[8:9], 0xd8
	s_lshl_b32 s8, s4, 8
	s_ashr_i32 s9, s8, 31
	s_lshl_b64 s[8:9], s[8:9], 2
	v_ashrrev_i32_e32 v101, 31, v100
	s_waitcnt lgkmcnt(0)
	s_add_u32 s8, s44, s8
	s_addc_u32 s9, s45, s9
	v_lshl_add_u64 v[100:101], v[100:101], 2, s[8:9]
	global_load_dword v69, v[100:101], off
	global_load_dword v71, v[100:101], off offset:256
	global_load_dword v250, v[100:101], off offset:512
	global_load_dword v251, v[100:101], off offset:768
	s_cmp_eq_u32 s4, 0
	s_mov_b32 s5, 0x3e4ccccd
	s_cselect_b32 s5, s5, 0x3eb60549
	v_mov_b32_e32 v102, v2
	v_mov_b32_e32 v103, v18
	v_mov_b32_e32 v146, v50
	v_mov_b32_e32 v147, v34
	v_mov_b32_e32 v18, v3
	v_mov_b32_e32 v50, v35
	s_mov_b32 s8, 0x358637bd
	v_mov_b32_e32 v106, s46
	v_mov_b32_e32 v107, s47
	s_mov_b32 s41, s61
	v_mov_b32_e32 v105, v0
	v_ashrrev_i32_e32 v93, 31, v92
	v_lshlrev_b64 v[92:93], 11, v[92:93]
	v_ashrrev_i32_e32 v91, 31, v90
	v_lshlrev_b64 v[90:91], 11, v[90:91]
	v_ashrrev_i32_e32 v89, 31, v88
	v_lshlrev_b64 v[88:89], 11, v[88:89]
	v_ashrrev_i32_e32 v87, 31, v86
	v_lshlrev_b64 v[86:87], 11, v[86:87]
	v_ashrrev_i32_e32 v85, 31, v84
	v_lshlrev_b64 v[84:85], 11, v[84:85]
	v_ashrrev_i32_e32 v83, 31, v82
	v_lshlrev_b64 v[82:83], 11, v[82:83]
	v_ashrrev_i32_e32 v81, 31, v80
	v_lshlrev_b64 v[80:81], 11, v[80:81]
	v_ashrrev_i32_e32 v79, 31, v78
	v_lshlrev_b64 v[78:79], 11, v[78:79]
	v_ashrrev_i32_e32 v99, 31, v98
	v_ashrrev_i32_e32 v97, 31, v96
	v_ashrrev_i32_e32 v95, 31, v94
	v_lshlrev_b64 v[94:95], 11, v[94:95]
	s_waitcnt vmcnt(0)
	v_mul_f32_e32 v73, v69, v71
	ds_bpermute_b32 v73, v142, v73
	s_waitcnt lgkmcnt(0)
	v_fmac_f32_e32 v73, v69, v71
	ds_bpermute_b32 v69, v141, v73
	s_waitcnt lgkmcnt(0)
	v_add_f32_e32 v69, v73, v69
	ds_bpermute_b32 v71, v140, v69
	s_waitcnt lgkmcnt(0)
	v_add_f32_e32 v69, v69, v71
	ds_bpermute_b32 v71, v139, v69
	s_waitcnt lgkmcnt(0)
	v_add_f32_e32 v69, v69, v71
	ds_bpermute_b32 v71, v1, v69
	s_waitcnt lgkmcnt(0)
	v_add_f32_e32 v69, v69, v71
	ds_bpermute_b32 v71, v143, v69
	s_waitcnt lgkmcnt(0)
	v_add_f32_e32 v69, v69, v71
	v_mul_f32_e32 v71, 0x3fb8aa3b, v69
	v_fma_f32 v73, v69, s10, -v71
	v_rndne_f32_e32 v75, v71
	v_fmac_f32_e32 v73, 0x32a5705f, v69
	v_sub_f32_e32 v71, v71, v75
	v_add_f32_e32 v71, v71, v73
	v_exp_f32_e32 v71, v71
	v_cvt_i32_f32_e32 v73, v75
	v_cmp_ngt_f32_e32 vcc, s11, v69
	v_ldexp_f32 v71, v71, v73
	s_nop 0
	v_cndmask_b32_e32 v71, 0, v71, vcc
	v_cmp_nlt_f32_e32 vcc, s12, v69
	s_nop 1
	v_cndmask_b32_e32 v69, v237, v71, vcc
	v_mov_b32_e32 v71, v250
	v_mov_b32_e32 v73, v251
	ds_read2_b32 v[100:101], v67 offset1:32
	v_mul_f32_e32 v75, v71, v73
	ds_bpermute_b32 v75, v142, v75
	s_waitcnt lgkmcnt(0)
	v_fmac_f32_e32 v75, v71, v73
	ds_bpermute_b32 v71, v141, v75
	s_waitcnt lgkmcnt(0)
	v_add_f32_e32 v71, v75, v71
	ds_bpermute_b32 v73, v140, v71
	s_waitcnt lgkmcnt(0)
	v_add_f32_e32 v71, v71, v73
	ds_bpermute_b32 v73, v139, v71
	s_waitcnt lgkmcnt(0)
	v_add_f32_e32 v71, v71, v73
	ds_bpermute_b32 v73, v1, v71
	s_waitcnt lgkmcnt(0)
	v_add_f32_e32 v71, v71, v73
	ds_bpermute_b32 v73, v143, v71
	s_waitcnt lgkmcnt(0)
	v_add_f32_e32 v71, v71, v73
	v_mul_f32_e32 v73, 0x3fb8aa3b, v71
	v_fma_f32 v75, v71, s10, -v73
	v_rndne_f32_e32 v77, v73
	v_fmac_f32_e32 v75, 0x32a5705f, v71
	v_sub_f32_e32 v73, v73, v77
	v_add_f32_e32 v73, v73, v75
	v_exp_f32_e32 v73, v73
	v_cvt_i32_f32_e32 v75, v77
	v_cmp_ngt_f32_e32 vcc, s11, v71
	v_ldexp_f32 v73, v73, v75
	s_nop 0
	v_cndmask_b32_e32 v73, 0, v73, vcc
	v_cmp_nlt_f32_e32 vcc, s12, v71
	v_ashrrev_i32_e32 v75, 31, v74
	v_lshlrev_b64 v[74:75], 11, v[74:75]
	v_cndmask_b32_e32 v71, v237, v73, vcc
	v_sub_f32_e32 v69, v69, v71
	v_add_f32_e32 v116, s5, v69
	v_pk_mul_f32 v[100:101], v[100:101], v[116:117] op_sel_hi:[1,0]
	v_sub_f32_e64 v69, 1.0, s5
	v_pk_fma_f32 v[100:101], v[102:103], v[76:77], v[100:101] op_sel_hi:[1,0,1] neg_lo:[0,0,1] neg_hi:[0,0,1]
	ds_read2_b32 v[102:103], v67 offset0:64 offset1:96
	v_pk_mul_f32 v[144:145], v[100:101], v[100:101]
	v_add_u32_e32 v71, 0x400, v67
	v_readlane_b32 s5, v254, 61
	v_ashrrev_i32_e32 v73, 31, v72
	s_waitcnt lgkmcnt(0)
	v_mov_b32_e32 v148, v103
	v_mov_b32_e32 v149, v102
	v_pk_mul_f32 v[102:103], v[116:117], v[148:149] op_sel_hi:[0,1]
	v_pk_fma_f32 v[76:77], v[146:147], v[76:77], v[102:103] op_sel_hi:[1,0,1] neg_lo:[0,0,1] neg_hi:[0,0,1]
	ds_read2_b32 v[102:103], v67 offset0:128 offset1:160
	v_pk_mul_f32 v[146:147], v[76:77], v[76:77]
	v_lshlrev_b64 v[72:73], 11, v[72:73]
	s_waitcnt lgkmcnt(0)
	v_pk_mul_f32 v[2:3], v[116:117], v[102:103] op_sel_hi:[0,1]
	v_pk_fma_f32 v[102:103], v[18:19], v[122:123], v[2:3] op_sel_hi:[1,0,1] neg_lo:[0,0,1] neg_hi:[0,0,1]
	ds_read2_b32 v[2:3], v67 offset0:192 offset1:224
	v_pk_mul_f32 v[18:19], v[102:103], v[102:103]
	s_waitcnt lgkmcnt(0)
	v_pk_mul_f32 v[2:3], v[116:117], v[2:3] op_sel_hi:[0,1]
	v_pk_fma_f32 v[2:3], v[50:51], v[122:123], v[2:3] op_sel_hi:[1,0,1] neg_lo:[0,0,1] neg_hi:[0,0,1]
	v_mov_b32_e32 v50, v18
	v_pk_mul_f32 v[34:35], v[2:3], v[2:3]
	v_mov_b32_e32 v51, v144
	v_mov_b32_e32 v144, v19
	v_pk_add_f32 v[18:19], v[50:51], v[144:145]
	v_mov_b32_e32 v50, v34
	v_mov_b32_e32 v51, v147
	v_pk_add_f32 v[18:19], v[18:19], v[50:51]
	v_pk_mov_b32 v[34:35], v[34:35], v[146:147] op_sel:[1,0]
	v_mov_b64_e32 v[122:123], s[8:9]
	v_pk_add_f32 v[18:19], v[18:19], v[34:35]
	ds_bpermute_b32 v35, v142, v19
	ds_bpermute_b32 v34, v142, v18
	s_brev_b32 s8, 60
	ds_read2_b32 v[146:147], v71 offset0:128 offset1:160
	v_mov_b32_e32 v144, v36
	v_mov_b32_e32 v145, v52
	s_waitcnt lgkmcnt(1)
; __device__ __forceinline__ int crow(int r, int hi) { return (r & 3) + 8 * (r >> 2) + 4 * hi; }
; __device__ __forceinline__ void diff_unit(KP Pk, Frame& F, int l, int b, int h, int qrow0, int nkt) {
;     ...
;         for (int r = 0; r < 16; ++r) { float a = 0.f;
; #pragma unroll
;             for (int nb = 0; nb < 4; ++nb) { const float v = O[nb][r] * rlr[r] - lam * ex[crow(r, hi) * 128 + nb * 32 + r32]; O[nb][r] = v; a += v * v; }
;             a += __shfl_xor(a, 1); a += __shfl_xor(a, 2); a += __shfl_xor(a, 4); a += __shfl_xor(a, 8); a += __shfl_xor(a, 16);
;             ssq[r] = rsqrtf(a * (1.f / 128.f) + NORM_EPS) * (1.f - lam_init); }
	v_pk_add_f32 v[18:19], v[18:19], v[34:35]
	ds_bpermute_b32 v35, v141, v19
	ds_bpermute_b32 v34, v141, v18
	v_mov_b32_e32 v52, v37
	s_waitcnt lgkmcnt(0)
	v_pk_add_f32 v[18:19], v[18:19], v[34:35]
	ds_bpermute_b32 v35, v140, v19
	ds_bpermute_b32 v34, v140, v18
	s_waitcnt lgkmcnt(0)
	v_pk_add_f32 v[18:19], v[18:19], v[34:35]
	ds_bpermute_b32 v35, v139, v19
	ds_bpermute_b32 v34, v139, v18
	s_waitcnt lgkmcnt(0)
	v_pk_add_f32 v[18:19], v[18:19], v[34:35]
	ds_bpermute_b32 v35, v1, v19
	ds_bpermute_b32 v34, v1, v18
	s_waitcnt lgkmcnt(0)
	v_pk_add_f32 v[18:19], v[18:19], v[34:35]
	s_nop 0
	v_pk_fma_f32 v[18:19], v[18:19], s[8:9], v[122:123] op_sel_hi:[1,0,0]
	v_mov_b32_e32 v35, v20
	v_mul_f32_e32 v34, 0x4b800000, v19
	v_cmp_gt_f32_e64 s[38:39], s66, v19
	v_cmp_gt_f32_e32 vcc, s66, v18
	v_mov_b32_e32 v20, v5
	v_cndmask_b32_e64 v19, v19, v34, s[38:39]
	v_rsq_f32_e32 v19, v19
	s_nop 0
	v_mul_f32_e32 v34, 0x45800000, v19
	v_cndmask_b32_e64 v19, v19, v34, s[38:39]
	v_mul_f32_e32 v111, v69, v19
	v_mul_f32_e32 v19, 0x4b800000, v18
	v_cndmask_b32_e32 v18, v18, v19, vcc
	v_rsq_f32_e32 v18, v18
	v_mov_b32_e32 v34, v4
	v_pk_mul_f32 v[4:5], v[116:117], v[146:147] op_sel_hi:[0,1]
	v_pk_fma_f32 v[20:21], v[20:21], v[136:137], v[4:5] op_sel_hi:[1,0,1] neg_lo:[0,0,1] neg_hi:[0,0,1]
	v_mul_f32_e32 v19, 0x45800000, v18
	v_cndmask_b32_e32 v18, v18, v19, vcc
	v_mul_f32_e32 v109, v69, v18
	ds_read2_b32 v[18:19], v71 offset1:32
	ds_read2_b32 v[4:5], v71 offset0:192 offset1:224
	v_pk_mul_f32 v[146:147], v[20:21], v[20:21]
	v_mul_f32_e32 v2, v2, v109
	v_mul_f32_e32 v3, v3, v109
	s_waitcnt lgkmcnt(1)
	v_pk_mul_f32 v[18:19], v[116:117], v[18:19] op_sel_hi:[0,1]
	v_pk_fma_f32 v[34:35], v[34:35], v[138:139], v[18:19] op_sel_hi:[1,0,1] neg_lo:[0,0,1] neg_hi:[0,0,1]
	ds_read2_b32 v[18:19], v71 offset0:64 offset1:96
	s_waitcnt lgkmcnt(1)
	v_pk_mul_f32 v[4:5], v[116:117], v[4:5] op_sel_hi:[0,1]
	v_pk_mul_f32 v[50:51], v[34:35], v[34:35]
	v_pk_fma_f32 v[4:5], v[52:53], v[136:137], v[4:5] op_sel_hi:[1,0,1] neg_lo:[0,0,1] neg_hi:[0,0,1]
	v_mov_b32_e32 v52, v146
	s_waitcnt lgkmcnt(0)
	v_pk_mul_f32 v[18:19], v[116:117], v[18:19] op_sel_hi:[0,1]
	v_pk_fma_f32 v[18:19], v[144:145], v[138:139], v[18:19] op_sel_hi:[1,0,1] neg_lo:[0,0,1] neg_hi:[0,0,1]
	v_pk_mul_f32 v[36:37], v[4:5], v[4:5]
	v_pk_mul_f32 v[144:145], v[18:19], v[18:19]
	v_mov_b32_e32 v53, v50
	v_mov_b32_e32 v50, v147
	v_pk_add_f32 v[50:51], v[52:53], v[50:51]
	v_mov_b32_e32 v52, v36
	v_mov_b32_e32 v53, v144
	v_pk_add_f32 v[50:51], v[50:51], v[52:53]
	v_mov_b32_e32 v144, v37
	v_pk_add_f32 v[36:37], v[50:51], v[144:145]
	ds_bpermute_b32 v51, v142, v37
	ds_bpermute_b32 v50, v142, v36
	v_add_u32_e32 v71, 0x1000, v67
	v_mov_b32_e32 v52, v38
	v_mov_b32_e32 v53, v54
	v_mov_b32_e32 v54, v39
	s_waitcnt lgkmcnt(0)
	v_pk_add_f32 v[36:37], v[36:37], v[50:51]
	ds_bpermute_b32 v51, v141, v37
	ds_bpermute_b32 v50, v141, v36
	s_waitcnt lgkmcnt(0)
	v_pk_add_f32 v[36:37], v[36:37], v[50:51]
	ds_bpermute_b32 v51, v140, v37
	ds_bpermute_b32 v50, v140, v36
	s_waitcnt lgkmcnt(0)
	v_pk_add_f32 v[36:37], v[36:37], v[50:51]
	ds_bpermute_b32 v51, v139, v37
	ds_bpermute_b32 v50, v139, v36
	s_waitcnt lgkmcnt(0)
	v_pk_add_f32 v[36:37], v[36:37], v[50:51]
	ds_bpermute_b32 v51, v1, v37
	ds_bpermute_b32 v50, v1, v36
	s_waitcnt lgkmcnt(0)
	v_pk_add_f32 v[36:37], v[36:37], v[50:51]
	s_nop 0
	v_pk_fma_f32 v[36:37], v[36:37], s[8:9], v[122:123] op_sel_hi:[1,0,0]
	v_mov_b32_e32 v51, v22
	v_mul_f32_e32 v50, 0x4b800000, v37
	v_cmp_gt_f32_e64 s[38:39], s66, v37
	v_cmp_gt_f32_e32 vcc, s66, v36
	v_mov_b32_e32 v22, v7
	v_cndmask_b32_e64 v37, v37, v50, s[38:39]
	v_rsq_f32_e32 v37, v37
	s_nop 0
	v_mul_f32_e32 v50, 0x45800000, v37
	v_cndmask_b32_e64 v37, v37, v50, s[38:39]
	v_mul_f32_e32 v115, v69, v37
	v_mul_f32_e32 v37, 0x4b800000, v36
	v_cndmask_b32_e32 v36, v36, v37, vcc
	v_rsq_f32_e32 v36, v36
	v_mov_b32_e32 v50, v6
	v_mul_f32_e32 v34, v34, v115
	v_mul_f32_e32 v37, 0x45800000, v36
	v_cndmask_b32_e32 v36, v36, v37, vcc
	v_mul_f32_e32 v113, v69, v36
	ds_read2_b32 v[36:37], v71 offset1:32
	v_mul_f32_e32 v20, v20, v113
	v_mul_f32_e32 v21, v21, v113
	s_waitcnt lgkmcnt(0)
	v_pk_mul_f32 v[36:37], v[116:117], v[36:37] op_sel_hi:[0,1]
	v_pk_fma_f32 v[36:37], v[50:51], v[134:135], v[36:37] op_sel_hi:[1,0,1] neg_lo:[0,0,1] neg_hi:[0,0,1]
	ds_read2_b32 v[50:51], v71 offset0:64 offset1:96
	v_pk_mul_f32 v[136:137], v[36:37], v[36:37]
	s_waitcnt lgkmcnt(0)
	v_pk_mul_f32 v[50:51], v[116:117], v[50:51] op_sel_hi:[0,1]
	v_pk_fma_f32 v[50:51], v[52:53], v[134:135], v[50:51] op_sel_hi:[1,0,1] neg_lo:[0,0,1] neg_hi:[0,0,1]
	ds_read2_b32 v[52:53], v71 offset0:128 offset1:160
	v_pk_mul_f32 v[134:135], v[50:51], v[50:51]
	s_waitcnt lgkmcnt(0)
	v_pk_mul_f32 v[6:7], v[116:117], v[52:53] op_sel_hi:[0,1]
	v_pk_fma_f32 v[52:53], v[22:23], v[132:133], v[6:7] op_sel_hi:[1,0,1] neg_lo:[0,0,1] neg_hi:[0,0,1]
	ds_read2_b32 v[6:7], v71 offset0:192 offset1:224
	v_pk_mul_f32 v[22:23], v[52:53], v[52:53]
	v_add_u32_e32 v71, 0x1400, v67
	s_waitcnt lgkmcnt(0)
	v_pk_mul_f32 v[6:7], v[116:117], v[6:7] op_sel_hi:[0,1]
	v_pk_fma_f32 v[6:7], v[54:55], v[132:133], v[6:7] op_sel_hi:[1,0,1] neg_lo:[0,0,1] neg_hi:[0,0,1]
	v_mov_b32_e32 v54, v22
	v_pk_mul_f32 v[38:39], v[6:7], v[6:7]
	v_mov_b32_e32 v55, v136
	v_mov_b32_e32 v136, v23
	v_pk_add_f32 v[22:23], v[54:55], v[136:137]
	v_mov_b32_e32 v54, v38
	v_mov_b32_e32 v55, v134
	v_pk_add_f32 v[22:23], v[22:23], v[54:55]
	v_mov_b32_e32 v134, v39
	v_pk_add_f32 v[22:23], v[22:23], v[134:135]
	ds_bpermute_b32 v39, v142, v23
	ds_bpermute_b32 v38, v142, v22
	v_mov_b32_e32 v54, v40
	v_mov_b32_e32 v55, v56
	v_mov_b32_e32 v56, v41
	s_waitcnt lgkmcnt(0)
; __device__ __forceinline__ int crow(int r, int hi) { return (r & 3) + 8 * (r >> 2) + 4 * hi; }
; __device__ __forceinline__ void diff_unit(KP Pk, Frame& F, int l, int b, int h, int qrow0, int nkt) {
;     ...
;         for (int r = 0; r < 16; ++r) { float a = 0.f;
; #pragma unroll
;             for (int nb = 0; nb < 4; ++nb) { const float v = O[nb][r] * rlr[r] - lam * ex[crow(r, hi) * 128 + nb * 32 + r32]; O[nb][r] = v; a += v * v; }
;             a += __shfl_xor(a, 1); a += __shfl_xor(a, 2); a += __shfl_xor(a, 4); a += __shfl_xor(a, 8); a += __shfl_xor(a, 16);
;             ssq[r] = rsqrtf(a * (1.f / 128.f) + NORM_EPS) * (1.f - lam_init); }
	v_pk_add_f32 v[22:23], v[22:23], v[38:39]
	ds_bpermute_b32 v39, v141, v23
	ds_bpermute_b32 v38, v141, v22
	s_waitcnt lgkmcnt(0)
	v_pk_add_f32 v[22:23], v[22:23], v[38:39]
	ds_bpermute_b32 v39, v140, v23
	ds_bpermute_b32 v38, v140, v22
	s_waitcnt lgkmcnt(0)
	v_pk_add_f32 v[22:23], v[22:23], v[38:39]
	ds_bpermute_b32 v39, v139, v23
	ds_bpermute_b32 v38, v139, v22
	s_waitcnt lgkmcnt(0)
	v_pk_add_f32 v[22:23], v[22:23], v[38:39]
	ds_bpermute_b32 v39, v1, v23
	ds_bpermute_b32 v38, v1, v22
	s_waitcnt lgkmcnt(0)
	v_pk_add_f32 v[22:23], v[22:23], v[38:39]
	s_nop 0
	v_pk_fma_f32 v[22:23], v[22:23], s[8:9], v[122:123] op_sel_hi:[1,0,0]
	v_mov_b32_e32 v39, v24
	v_mul_f32_e32 v38, 0x4b800000, v23
	v_cmp_gt_f32_e64 s[38:39], s66, v23
	v_cmp_gt_f32_e32 vcc, s66, v22
	v_mov_b32_e32 v24, v9
	v_cndmask_b32_e64 v23, v23, v38, s[38:39]
	v_rsq_f32_e32 v23, v23
	s_nop 0
	v_mul_f32_e32 v38, 0x45800000, v23
	v_cndmask_b32_e64 v23, v23, v38, s[38:39]
	v_mul_f32_e32 v119, v69, v23
	v_mul_f32_e32 v23, 0x4b800000, v22
	v_cndmask_b32_e32 v22, v22, v23, vcc
	v_rsq_f32_e32 v22, v22
	v_mov_b32_e32 v38, v8
	v_mul_f32_e32 v23, 0x45800000, v22
	v_cndmask_b32_e32 v22, v22, v23, vcc
	v_mul_f32_e32 v117, v69, v22
	ds_read2_b32 v[22:23], v71 offset1:32
	s_waitcnt lgkmcnt(0)
	v_pk_mul_f32 v[22:23], v[116:117], v[22:23] op_sel_hi:[0,1]
	v_pk_fma_f32 v[38:39], v[38:39], v[130:131], v[22:23] op_sel_hi:[1,0,1] neg_lo:[0,0,1] neg_hi:[0,0,1]
	ds_read2_b32 v[22:23], v71 offset0:64 offset1:96
	v_pk_mul_f32 v[132:133], v[38:39], v[38:39]
	s_waitcnt lgkmcnt(0)
	v_pk_mul_f32 v[22:23], v[116:117], v[22:23] op_sel_hi:[0,1]
	v_pk_fma_f32 v[22:23], v[54:55], v[130:131], v[22:23] op_sel_hi:[1,0,1] neg_lo:[0,0,1] neg_hi:[0,0,1]
	ds_read2_b32 v[54:55], v71 offset0:128 offset1:160
	v_pk_mul_f32 v[130:131], v[22:23], v[22:23]
	s_waitcnt lgkmcnt(0)
	v_pk_mul_f32 v[8:9], v[116:117], v[54:55] op_sel_hi:[0,1]
	v_pk_fma_f32 v[54:55], v[24:25], v[128:129], v[8:9] op_sel_hi:[1,0,1] neg_lo:[0,0,1] neg_hi:[0,0,1]
	ds_read2_b32 v[8:9], v71 offset0:192 offset1:224
	v_pk_mul_f32 v[24:25], v[54:55], v[54:55]
	v_add_u32_e32 v71, 0x2000, v67
	s_waitcnt lgkmcnt(0)
	v_pk_mul_f32 v[8:9], v[116:117], v[8:9] op_sel_hi:[0,1]
	v_pk_fma_f32 v[8:9], v[56:57], v[128:129], v[8:9] op_sel_hi:[1,0,1] neg_lo:[0,0,1] neg_hi:[0,0,1]
	v_mov_b32_e32 v56, v24
	v_pk_mul_f32 v[40:41], v[8:9], v[8:9]
	v_mov_b32_e32 v57, v132
	v_mov_b32_e32 v132, v25
	v_pk_add_f32 v[24:25], v[56:57], v[132:133]
	v_mov_b32_e32 v56, v40
	v_mov_b32_e32 v57, v130
	v_pk_add_f32 v[24:25], v[24:25], v[56:57]
	v_mov_b32_e32 v130, v41
	v_pk_add_f32 v[24:25], v[24:25], v[130:131]
	ds_bpermute_b32 v41, v142, v25
	ds_bpermute_b32 v40, v142, v24
	v_mov_b32_e32 v56, v42
	v_mov_b32_e32 v57, v58
	v_mov_b32_e32 v58, v43
	s_waitcnt lgkmcnt(0)
	v_pk_add_f32 v[24:25], v[24:25], v[40:41]
	ds_bpermute_b32 v41, v141, v25
	ds_bpermute_b32 v40, v141, v24
	s_waitcnt lgkmcnt(0)
	v_pk_add_f32 v[24:25], v[24:25], v[40:41]
	ds_bpermute_b32 v41, v140, v25
	ds_bpermute_b32 v40, v140, v24
	s_waitcnt lgkmcnt(0)
	v_pk_add_f32 v[24:25], v[24:25], v[40:41]
	ds_bpermute_b32 v41, v139, v25
	ds_bpermute_b32 v40, v139, v24
	s_waitcnt lgkmcnt(0)
	v_pk_add_f32 v[24:25], v[24:25], v[40:41]
	ds_bpermute_b32 v41, v1, v25
	ds_bpermute_b32 v40, v1, v24
	s_waitcnt lgkmcnt(0)
	v_pk_add_f32 v[24:25], v[24:25], v[40:41]
	s_nop 0
	v_pk_fma_f32 v[24:25], v[24:25], s[8:9], v[122:123] op_sel_hi:[1,0,0]
	v_mov_b32_e32 v41, v26
	v_mul_f32_e32 v40, 0x4b800000, v25
	v_cmp_gt_f32_e64 s[38:39], s66, v25
	v_cmp_gt_f32_e32 vcc, s66, v24
	v_mov_b32_e32 v26, v11
	v_cndmask_b32_e64 v25, v25, v40, s[38:39]
	v_rsq_f32_e32 v25, v25
	s_nop 0
	v_mul_f32_e32 v40, 0x45800000, v25
	v_cndmask_b32_e64 v25, v25, v40, s[38:39]
	v_mul_f32_e32 v125, v69, v25
	v_mul_f32_e32 v25, 0x4b800000, v24
	v_cndmask_b32_e32 v24, v24, v25, vcc
	v_rsq_f32_e32 v24, v24
	v_mov_b32_e32 v40, v10
	v_mul_f32_e32 v25, 0x45800000, v24
	v_cndmask_b32_e32 v24, v24, v25, vcc
	v_mul_f32_e32 v121, v69, v24
	ds_read2_b32 v[24:25], v71 offset1:32
	s_waitcnt lgkmcnt(0)
	v_pk_mul_f32 v[24:25], v[116:117], v[24:25] op_sel_hi:[0,1]
	v_pk_fma_f32 v[40:41], v[40:41], v[126:127], v[24:25] op_sel_hi:[1,0,1] neg_lo:[0,0,1] neg_hi:[0,0,1]
	ds_read2_b32 v[24:25], v71 offset0:64 offset1:96
	v_pk_mul_f32 v[128:129], v[40:41], v[40:41]
	s_waitcnt lgkmcnt(0)
	v_pk_mul_f32 v[24:25], v[116:117], v[24:25] op_sel_hi:[0,1]
	v_pk_fma_f32 v[24:25], v[56:57], v[126:127], v[24:25] op_sel_hi:[1,0,1] neg_lo:[0,0,1] neg_hi:[0,0,1]
	ds_read2_b32 v[56:57], v71 offset0:128 offset1:160
	v_pk_mul_f32 v[126:127], v[24:25], v[24:25]
	s_waitcnt lgkmcnt(0)
	v_pk_mul_f32 v[10:11], v[116:117], v[56:57] op_sel_hi:[0,1]
	v_pk_fma_f32 v[56:57], v[26:27], v[124:125], v[10:11] op_sel_hi:[1,0,1] neg_lo:[0,0,1] neg_hi:[0,0,1]
	ds_read2_b32 v[10:11], v71 offset0:192 offset1:224
	v_pk_mul_f32 v[26:27], v[56:57], v[56:57]
	v_add_u32_e32 v71, 0x2400, v67
	s_waitcnt lgkmcnt(0)
	v_pk_mul_f32 v[10:11], v[116:117], v[10:11] op_sel_hi:[0,1]
	v_pk_fma_f32 v[10:11], v[58:59], v[124:125], v[10:11] op_sel_hi:[1,0,1] neg_lo:[0,0,1] neg_hi:[0,0,1]
	v_mov_b32_e32 v58, v26
	v_pk_mul_f32 v[42:43], v[10:11], v[10:11]
	v_mov_b32_e32 v59, v128
	v_mov_b32_e32 v128, v27
	v_pk_add_f32 v[26:27], v[58:59], v[128:129]
	v_mov_b32_e32 v58, v42
	v_mov_b32_e32 v59, v126
	v_pk_add_f32 v[26:27], v[26:27], v[58:59]
	v_mov_b32_e32 v126, v43
	v_pk_add_f32 v[26:27], v[26:27], v[126:127]
	ds_bpermute_b32 v43, v142, v27
	ds_bpermute_b32 v42, v142, v26
	v_mov_b32_e32 v58, v44
	v_mov_b32_e32 v59, v60
	v_mov_b32_e32 v60, v45
	s_waitcnt lgkmcnt(0)
	v_pk_add_f32 v[26:27], v[26:27], v[42:43]
	ds_bpermute_b32 v43, v141, v27
	ds_bpermute_b32 v42, v141, v26
	s_waitcnt lgkmcnt(0)
; __device__ __forceinline__ int crow(int r, int hi) { return (r & 3) + 8 * (r >> 2) + 4 * hi; }
; __device__ __forceinline__ void diff_unit(KP Pk, Frame& F, int l, int b, int h, int qrow0, int nkt) {
;     ...
;         for (int r = 0; r < 16; ++r) { float a = 0.f;
; #pragma unroll
;             for (int nb = 0; nb < 4; ++nb) { const float v = O[nb][r] * rlr[r] - lam * ex[crow(r, hi) * 128 + nb * 32 + r32]; O[nb][r] = v; a += v * v; }
;             a += __shfl_xor(a, 1); a += __shfl_xor(a, 2); a += __shfl_xor(a, 4); a += __shfl_xor(a, 8); a += __shfl_xor(a, 16);
;             ssq[r] = rsqrtf(a * (1.f / 128.f) + NORM_EPS) * (1.f - lam_init); }
	v_pk_add_f32 v[26:27], v[26:27], v[42:43]
	ds_bpermute_b32 v43, v140, v27
	ds_bpermute_b32 v42, v140, v26
	s_waitcnt lgkmcnt(0)
	v_pk_add_f32 v[26:27], v[26:27], v[42:43]
	ds_bpermute_b32 v43, v139, v27
	ds_bpermute_b32 v42, v139, v26
	s_waitcnt lgkmcnt(0)
	v_pk_add_f32 v[26:27], v[26:27], v[42:43]
	ds_bpermute_b32 v43, v1, v27
	ds_bpermute_b32 v42, v1, v26
	s_waitcnt lgkmcnt(0)
	v_pk_add_f32 v[26:27], v[26:27], v[42:43]
	s_nop 0
	v_pk_fma_f32 v[26:27], v[26:27], s[8:9], v[122:123] op_sel_hi:[1,0,0]
	v_mov_b32_e32 v43, v28
	v_mul_f32_e32 v42, 0x4b800000, v27
	v_cmp_gt_f32_e64 s[38:39], s66, v27
	v_cmp_gt_f32_e32 vcc, s66, v26
	v_mov_b32_e32 v28, v13
	v_cndmask_b32_e64 v27, v27, v42, s[38:39]
	v_rsq_f32_e32 v27, v27
	s_nop 0
	v_mul_f32_e32 v42, 0x45800000, v27
	v_cndmask_b32_e64 v27, v27, v42, s[38:39]
	v_mul_f32_e32 v126, v69, v27
	v_mul_f32_e32 v27, 0x4b800000, v26
	v_cndmask_b32_e32 v26, v26, v27, vcc
	v_rsq_f32_e32 v26, v26
	v_mov_b32_e32 v42, v12
	v_mul_f32_e32 v27, 0x45800000, v26
	v_cndmask_b32_e32 v26, v26, v27, vcc
	v_mul_f32_e32 v124, v69, v26
	ds_read2_b32 v[26:27], v71 offset1:32
	s_waitcnt lgkmcnt(0)
	v_pk_mul_f32 v[26:27], v[116:117], v[26:27] op_sel_hi:[0,1]
	v_pk_fma_f32 v[42:43], v[42:43], v[120:121], v[26:27] op_sel_hi:[1,0,1] neg_lo:[0,0,1] neg_hi:[0,0,1]
	ds_read2_b32 v[26:27], v71 offset0:64 offset1:96
	v_pk_mul_f32 v[128:129], v[42:43], v[42:43]
	s_waitcnt lgkmcnt(0)
	v_pk_mul_f32 v[26:27], v[116:117], v[26:27] op_sel_hi:[0,1]
	v_pk_fma_f32 v[26:27], v[58:59], v[120:121], v[26:27] op_sel_hi:[1,0,1] neg_lo:[0,0,1] neg_hi:[0,0,1]
	ds_read2_b32 v[58:59], v71 offset0:128 offset1:160
	v_pk_mul_f32 v[130:131], v[26:27], v[26:27]
	s_waitcnt lgkmcnt(0)
	v_pk_mul_f32 v[12:13], v[116:117], v[58:59] op_sel_hi:[0,1]
	v_pk_fma_f32 v[58:59], v[28:29], v[118:119], v[12:13] op_sel_hi:[1,0,1] neg_lo:[0,0,1] neg_hi:[0,0,1]
	ds_read2_b32 v[12:13], v71 offset0:192 offset1:224
	v_pk_mul_f32 v[28:29], v[58:59], v[58:59]
	v_add_u32_e32 v71, 0x3000, v67
	v_add_u32_e32 v67, 0x3400, v67
	s_waitcnt lgkmcnt(0)
	v_pk_mul_f32 v[12:13], v[116:117], v[12:13] op_sel_hi:[0,1]
	v_pk_fma_f32 v[12:13], v[60:61], v[118:119], v[12:13] op_sel_hi:[1,0,1] neg_lo:[0,0,1] neg_hi:[0,0,1]
	v_mov_b32_e32 v60, v28
	v_pk_mul_f32 v[44:45], v[12:13], v[12:13]
	v_mov_b32_e32 v61, v128
	v_mov_b32_e32 v128, v29
	v_pk_add_f32 v[28:29], v[60:61], v[128:129]
	v_mov_b32_e32 v60, v44
	v_mov_b32_e32 v61, v130
	v_pk_add_f32 v[28:29], v[28:29], v[60:61]
	v_mov_b32_e32 v130, v45
	v_pk_add_f32 v[28:29], v[28:29], v[130:131]
	ds_bpermute_b32 v45, v142, v29
	ds_bpermute_b32 v44, v142, v28
	v_mov_b32_e32 v60, v46
	v_mov_b32_e32 v61, v62
	v_mov_b32_e32 v62, v47
	s_waitcnt lgkmcnt(0)
	v_pk_add_f32 v[28:29], v[28:29], v[44:45]
	ds_bpermute_b32 v45, v141, v29
	ds_bpermute_b32 v44, v141, v28
	s_waitcnt lgkmcnt(0)
	v_pk_add_f32 v[28:29], v[28:29], v[44:45]
	ds_bpermute_b32 v45, v140, v29
	ds_bpermute_b32 v44, v140, v28
	s_waitcnt lgkmcnt(0)
	v_pk_add_f32 v[28:29], v[28:29], v[44:45]
	ds_bpermute_b32 v45, v139, v29
	ds_bpermute_b32 v44, v139, v28
	s_waitcnt lgkmcnt(0)
	v_pk_add_f32 v[28:29], v[28:29], v[44:45]
	ds_bpermute_b32 v45, v1, v29
	ds_bpermute_b32 v44, v1, v28
	s_waitcnt lgkmcnt(0)
	v_pk_add_f32 v[28:29], v[28:29], v[44:45]
	s_nop 0
	v_pk_fma_f32 v[28:29], v[28:29], s[8:9], v[122:123] op_sel_hi:[1,0,0]
	v_mov_b32_e32 v45, v30
	v_mul_f32_e32 v44, 0x4b800000, v29
	v_cmp_gt_f32_e64 s[38:39], s66, v29
	v_cmp_gt_f32_e32 vcc, s66, v28
	v_mov_b32_e32 v30, v15
	v_cndmask_b32_e64 v29, v29, v44, s[38:39]
	v_rsq_f32_e32 v29, v29
	s_nop 0
	v_mul_f32_e32 v44, 0x45800000, v29
	v_cndmask_b32_e64 v29, v29, v44, s[38:39]
	v_mul_f32_e32 v120, v69, v29
	v_mul_f32_e32 v29, 0x4b800000, v28
	v_cndmask_b32_e32 v28, v28, v29, vcc
	v_rsq_f32_e32 v28, v28
	v_mov_b32_e32 v44, v14
	v_mul_f32_e32 v29, 0x45800000, v28
	v_cndmask_b32_e32 v28, v28, v29, vcc
	v_mul_f32_e32 v118, v69, v28
	ds_read2_b32 v[28:29], v71 offset1:32
	s_waitcnt lgkmcnt(0)
	v_pk_mul_f32 v[28:29], v[116:117], v[28:29] op_sel_hi:[0,1]
	v_pk_fma_f32 v[44:45], v[44:45], v[114:115], v[28:29] op_sel_hi:[1,0,1] neg_lo:[0,0,1] neg_hi:[0,0,1]
	ds_read2_b32 v[28:29], v71 offset0:64 offset1:96
	v_pk_mul_f32 v[128:129], v[44:45], v[44:45]
	s_waitcnt lgkmcnt(0)
	v_pk_mul_f32 v[28:29], v[116:117], v[28:29] op_sel_hi:[0,1]
	v_pk_fma_f32 v[28:29], v[60:61], v[114:115], v[28:29] op_sel_hi:[1,0,1] neg_lo:[0,0,1] neg_hi:[0,0,1]
	ds_read2_b32 v[60:61], v71 offset0:128 offset1:160
	v_pk_mul_f32 v[130:131], v[28:29], v[28:29]
	s_waitcnt lgkmcnt(0)
	v_pk_mul_f32 v[14:15], v[116:117], v[60:61] op_sel_hi:[0,1]
	v_pk_fma_f32 v[60:61], v[30:31], v[112:113], v[14:15] op_sel_hi:[1,0,1] neg_lo:[0,0,1] neg_hi:[0,0,1]
	ds_read2_b32 v[14:15], v71 offset0:192 offset1:224
	v_pk_mul_f32 v[30:31], v[60:61], v[60:61]
	v_mov_b32_e32 v71, v0
	s_waitcnt lgkmcnt(0)
	v_pk_mul_f32 v[14:15], v[116:117], v[14:15] op_sel_hi:[0,1]
	v_pk_fma_f32 v[14:15], v[62:63], v[112:113], v[14:15] op_sel_hi:[1,0,1] neg_lo:[0,0,1] neg_hi:[0,0,1]
	v_mov_b32_e32 v62, v30
	v_pk_mul_f32 v[46:47], v[14:15], v[14:15]
	v_mov_b32_e32 v63, v128
	v_mov_b32_e32 v128, v31
	v_pk_add_f32 v[30:31], v[62:63], v[128:129]
	v_mov_b32_e32 v62, v46
	v_mov_b32_e32 v63, v130
	v_pk_add_f32 v[30:31], v[30:31], v[62:63]
	v_mov_b32_e32 v130, v47
	v_pk_add_f32 v[30:31], v[30:31], v[130:131]
	ds_bpermute_b32 v47, v142, v31
	ds_bpermute_b32 v46, v142, v30
	ds_read2_b32 v[130:131], v67 offset0:128 offset1:160
	v_mov_b32_e32 v128, v48
	v_mov_b32_e32 v129, v64
	v_mov_b32_e32 v64, v49
	s_waitcnt lgkmcnt(1)
	v_pk_add_f32 v[30:31], v[30:31], v[46:47]
	ds_bpermute_b32 v47, v141, v31
	ds_bpermute_b32 v46, v141, v30
	s_waitcnt lgkmcnt(0)
; __device__ __forceinline__ int crow(int r, int hi) { return (r & 3) + 8 * (r >> 2) + 4 * hi; }
; __device__ __forceinline__ void diff_unit(KP Pk, Frame& F, int l, int b, int h, int qrow0, int nkt) {
;     ...
;         for (int r = 0; r < 16; ++r) { float a = 0.f;
; #pragma unroll
;             for (int nb = 0; nb < 4; ++nb) { const float v = O[nb][r] * rlr[r] - lam * ex[crow(r, hi) * 128 + nb * 32 + r32]; O[nb][r] = v; a += v * v; }
;             a += __shfl_xor(a, 1); a += __shfl_xor(a, 2); a += __shfl_xor(a, 4); a += __shfl_xor(a, 8); a += __shfl_xor(a, 16);
;             ssq[r] = rsqrtf(a * (1.f / 128.f) + NORM_EPS) * (1.f - lam_init); }
;         unsigned char* mix = ws + WS_H + ((size_t)(qrow0 + 32 * rb) * D + 1536 + h * 128) * MIXB;
; #pragma unroll
;         for (int nb = 0; nb < 4; ++nb) { const float w = Pk->in[I_DSUB][l * 128 + nb * 32 + r32];
	v_pk_add_f32 v[30:31], v[30:31], v[46:47]
	ds_bpermute_b32 v47, v140, v31
	ds_bpermute_b32 v46, v140, v30
	s_waitcnt lgkmcnt(0)
	v_pk_add_f32 v[30:31], v[30:31], v[46:47]
	ds_bpermute_b32 v47, v139, v31
	ds_bpermute_b32 v46, v139, v30
	s_waitcnt lgkmcnt(0)
	v_pk_add_f32 v[30:31], v[30:31], v[46:47]
	ds_bpermute_b32 v47, v1, v31
	ds_bpermute_b32 v46, v1, v30
	s_waitcnt lgkmcnt(0)
	v_pk_add_f32 v[30:31], v[30:31], v[46:47]
	s_nop 0
	v_pk_fma_f32 v[30:31], v[30:31], s[8:9], v[122:123] op_sel_hi:[1,0,0]
	v_mov_b32_e32 v47, v32
	v_mul_f32_e32 v46, 0x4b800000, v31
	v_cmp_gt_f32_e64 s[38:39], s66, v31
	v_cmp_gt_f32_e32 vcc, s66, v30
	v_mov_b32_e32 v32, v17
	v_cndmask_b32_e64 v31, v31, v46, s[38:39]
	v_rsq_f32_e32 v31, v31
	s_nop 0
	v_mul_f32_e32 v46, 0x45800000, v31
	v_cndmask_b32_e64 v31, v31, v46, s[38:39]
	v_mul_f32_e32 v114, v69, v31
	v_mul_f32_e32 v31, 0x4b800000, v30
	v_cndmask_b32_e32 v30, v30, v31, vcc
	v_rsq_f32_e32 v30, v30
	v_mov_b32_e32 v46, v16
	v_pk_mul_f32 v[16:17], v[116:117], v[130:131] op_sel_hi:[0,1]
	v_pk_fma_f32 v[32:33], v[32:33], v[108:109], v[16:17] op_sel_hi:[1,0,1] neg_lo:[0,0,1] neg_hi:[0,0,1]
	v_mul_f32_e32 v31, 0x45800000, v30
	v_cndmask_b32_e32 v30, v30, v31, vcc
	v_mul_f32_e32 v112, v69, v30
	ds_read2_b32 v[30:31], v67 offset1:32
	ds_read2_b32 v[16:17], v67 offset0:192 offset1:224
	v_pk_mul_f32 v[130:131], v[32:33], v[32:33]
	s_waitcnt lgkmcnt(1)
	v_pk_mul_f32 v[30:31], v[116:117], v[30:31] op_sel_hi:[0,1]
	v_pk_fma_f32 v[46:47], v[46:47], v[110:111], v[30:31] op_sel_hi:[1,0,1] neg_lo:[0,0,1] neg_hi:[0,0,1]
	ds_read2_b32 v[30:31], v67 offset0:64 offset1:96
	s_waitcnt lgkmcnt(1)
	v_pk_mul_f32 v[16:17], v[116:117], v[16:17] op_sel_hi:[0,1]
	v_pk_mul_f32 v[62:63], v[46:47], v[46:47]
	v_pk_fma_f32 v[16:17], v[64:65], v[108:109], v[16:17] op_sel_hi:[1,0,1] neg_lo:[0,0,1] neg_hi:[0,0,1]
	v_mov_b32_e32 v64, v130
	s_waitcnt lgkmcnt(0)
	v_pk_mul_f32 v[30:31], v[116:117], v[30:31] op_sel_hi:[0,1]
	v_pk_fma_f32 v[30:31], v[128:129], v[110:111], v[30:31] op_sel_hi:[1,0,1] neg_lo:[0,0,1] neg_hi:[0,0,1]
	v_pk_mul_f32 v[48:49], v[16:17], v[16:17]
	v_pk_mul_f32 v[128:129], v[30:31], v[30:31]
	v_mov_b32_e32 v65, v62
	v_mov_b32_e32 v62, v131
	v_pk_add_f32 v[62:63], v[64:65], v[62:63]
	v_mov_b32_e32 v64, v48
	v_mov_b32_e32 v65, v128
	v_pk_add_f32 v[62:63], v[62:63], v[64:65]
	v_mov_b32_e32 v128, v49
	v_pk_add_f32 v[48:49], v[62:63], v[128:129]
	ds_bpermute_b32 v63, v142, v49
	ds_bpermute_b32 v62, v142, v48
	v_mov_b32_e32 v65, v0
	s_waitcnt lgkmcnt(0)
	v_pk_add_f32 v[48:49], v[48:49], v[62:63]
	ds_bpermute_b32 v63, v141, v49
	ds_bpermute_b32 v62, v141, v48
	s_waitcnt lgkmcnt(0)
	v_pk_add_f32 v[48:49], v[48:49], v[62:63]
	ds_bpermute_b32 v63, v140, v49
	ds_bpermute_b32 v62, v140, v48
	s_waitcnt lgkmcnt(0)
	v_pk_add_f32 v[48:49], v[48:49], v[62:63]
	ds_bpermute_b32 v63, v139, v49
	ds_bpermute_b32 v62, v139, v48
	s_waitcnt lgkmcnt(0)
	v_pk_add_f32 v[48:49], v[48:49], v[62:63]
	ds_bpermute_b32 v63, v1, v49
	ds_bpermute_b32 v62, v1, v48
	s_waitcnt lgkmcnt(0)
	v_pk_add_f32 v[48:49], v[48:49], v[62:63]
	s_nop 0
	v_pk_fma_f32 v[48:49], v[48:49], s[8:9], v[122:123] op_sel_hi:[1,0,0]
	v_mul_f32_e32 v62, v100, v111
	v_mul_f32_e32 v1, 0x4b800000, v49
	v_cmp_gt_f32_e64 s[38:39], s66, v49
	v_cmp_gt_f32_e32 vcc, s66, v48
	s_lshl_b64 s[8:9], s[40:41], 11
	v_cndmask_b32_e64 v1, v49, v1, s[38:39]
	v_rsq_f32_e32 v1, v1
	s_add_u32 s5, s5, s8
	v_readlane_b32 s8, v254, 62
	s_addc_u32 s9, s8, s9
	v_mul_f32_e32 v49, 0x45800000, v1
	v_cndmask_b32_e64 v1, v1, v49, s[38:39]
	v_mul_f32_e32 v108, v69, v1
	v_mul_f32_e32 v1, 0x4b800000, v48
	v_cndmask_b32_e32 v1, v48, v1, vcc
	v_rsq_f32_e32 v1, v1
	s_add_u32 s8, s5, s18
	s_addc_u32 s9, s9, 0
	v_mul_f32_e32 v48, 0x45800000, v1
	v_cndmask_b32_e32 v1, v1, v48, vcc
	v_lshl_or_b32 v48, s4, 7, v104
	v_ashrrev_i32_e32 v49, 31, v48
	v_lshl_add_u64 v[48:49], v[48:49], 2, v[106:107]
	global_load_dword v67, v[48:49], off
	global_load_dword v236, v[48:49], off offset:128
	global_load_dword v250, v[48:49], off offset:256
	global_load_dword v251, v[48:49], off offset:384
	v_mul_f32_e32 v1, v69, v1
	v_lshl_add_u64 v[104:105], s[8:9], 0, v[104:105]
	v_lshl_add_u64 v[92:93], v[104:105], 0, v[92:93]
	v_lshl_add_u64 v[90:91], v[104:105], 0, v[90:91]
	v_lshl_add_u64 v[88:89], v[104:105], 0, v[88:89]
	v_lshl_add_u64 v[86:87], v[104:105], 0, v[86:87]
	v_lshl_add_u64 v[84:85], v[104:105], 0, v[84:85]
	v_lshl_add_u64 v[82:83], v[104:105], 0, v[82:83]
	v_lshl_add_u64 v[80:81], v[104:105], 0, v[80:81]
	v_lshl_add_u64 v[78:79], v[104:105], 0, v[78:79]
	v_lshl_add_u64 v[74:75], v[104:105], 0, v[74:75]
	v_lshl_add_u64 v[72:73], v[104:105], 0, v[72:73]
	v_lshl_add_u64 v[94:95], v[104:105], 0, v[94:95]
	s_waitcnt vmcnt(0)
; __device__ __forceinline__ unsigned f2bf(float f) { unsigned u = __builtin_bit_cast(unsigned, f); return (u + 0x7fffu + ((u >> 16) & 1u)) >> 16; }
; __device__ __forceinline__ int crow(int r, int hi) { return (r & 3) + 8 * (r >> 2) + 4 * hi; }
; __device__ __forceinline__ unsigned char f8_1(float a) { a = fminf(fmaxf(a, -448.f), 448.f); return (unsigned char)(__builtin_amdgcn_cvt_pk_fp8_f32(a, a, 0, false) & 0xff); }
; __device__ __forceinline__ void diff_unit(KP Pk, Frame& F, int l, int b, int h, int qrow0, int nkt) {
;     ...
;         unsigned char* mix = ws + WS_H + ((size_t)(qrow0 + 32 * rb) * D + 1536 + h * 128) * MIXB;
; #pragma unroll
;         for (int nb = 0; nb < 4; ++nb) { const float w = Pk->in[I_DSUB][l * 128 + nb * 32 + r32];
; #pragma unroll
;             for (int r = 0; r < 16; ++r) { const float y = O[nb][r] * ssq[r] * w; const size_t e = (size_t)crow(r, hi) * D + nb * 32 + r32; if (WOUT_F8) mix[e] = f8_1(y); else ((bf16_t*)mix)[e] = (bf16_t)f2bf(y); } }
	v_mul_f32_e32 v64, v62, v67
	v_med3_f32 v64, v64, s83, v238
	v_cvt_pk_fp8_f32 v65, v64, v64
	v_mul_f32_e32 v64, v102, v109
	v_mul_f32_e32 v69, v64, v67
	v_med3_f32 v69, v69, s83, v238
	v_mul_f32_e32 v34, v34, v67
	v_cvt_pk_fp8_f32 v71, v69, v69
	v_med3_f32 v34, v34, s83, v238
	v_mov_b32_e32 v69, v0
	v_mul_f32_e32 v20, v20, v67
	v_cvt_pk_fp8_f32 v69, v34, v34
	v_med3_f32 v20, v20, s83, v238
	v_mov_b32_e32 v34, v0
	v_cvt_pk_fp8_f32 v34, v20, v20
	v_mul_f32_e32 v20, v36, v119
	v_mul_f32_e32 v20, v20, v67
	v_med3_f32 v20, v20, s83, v238
	global_store_byte v[92:93], v34, off
	v_mov_b32_e32 v34, v0
	v_cvt_pk_fp8_f32 v34, v20, v20
	v_mul_f32_e32 v20, v52, v117
	v_mul_f32_e32 v20, v20, v67
	v_med3_f32 v20, v20, s83, v238
	global_store_byte v[90:91], v34, off
	v_mov_b32_e32 v34, v0
	v_cvt_pk_fp8_f32 v34, v20, v20
	v_mul_f32_e32 v20, v38, v125
	v_mul_f32_e32 v20, v20, v67
	v_med3_f32 v20, v20, s83, v238
	global_store_byte v[88:89], v34, off
	v_mov_b32_e32 v34, v0
	v_cvt_pk_fp8_f32 v34, v20, v20
	v_mul_f32_e32 v20, v54, v121
	v_mul_f32_e32 v20, v20, v67
	v_med3_f32 v20, v20, s83, v238
	global_store_byte v[86:87], v34, off
	v_mov_b32_e32 v34, v0
	v_cvt_pk_fp8_f32 v34, v20, v20
	v_mul_f32_e32 v20, v40, v126
	v_mul_f32_e32 v20, v20, v67
	v_med3_f32 v20, v20, s83, v238
	global_store_byte v[84:85], v34, off
	v_mov_b32_e32 v34, v0
	v_cvt_pk_fp8_f32 v34, v20, v20
	v_mul_f32_e32 v20, v56, v124
	v_mul_f32_e32 v20, v20, v67
	v_med3_f32 v20, v20, s83, v238
	global_store_byte v[82:83], v34, off
	v_mov_b32_e32 v34, v0
	v_cvt_pk_fp8_f32 v34, v20, v20
	v_mul_f32_e32 v20, v42, v120
	v_mul_f32_e32 v20, v20, v67
	v_med3_f32 v20, v20, s83, v238
	global_store_byte v[80:81], v34, off
	v_mov_b32_e32 v34, v0
	v_cvt_pk_fp8_f32 v34, v20, v20
	v_mul_f32_e32 v20, v58, v118
	v_mul_f32_e32 v20, v20, v67
	v_med3_f32 v20, v20, s83, v238
	global_store_byte v[78:79], v34, off
	v_mov_b32_e32 v34, v0
	v_cvt_pk_fp8_f32 v34, v20, v20
	v_mul_f32_e32 v20, v44, v114
	v_mul_f32_e32 v20, v20, v67
	v_med3_f32 v20, v20, s83, v238
	global_store_byte v[74:75], v34, off
	v_mov_b32_e32 v34, v0
	v_cvt_pk_fp8_f32 v34, v20, v20
	v_lshlrev_b64 v[62:63], 11, v[98:99]
	v_mul_f32_e32 v20, v60, v112
	v_lshl_add_u64 v[62:63], v[104:105], 0, v[62:63]
	v_mul_f32_e32 v20, v20, v67
	global_store_byte v[62:63], v65, off
	v_lshlrev_b64 v[64:65], 11, v[96:97]
	global_store_byte v[72:73], v34, off
	v_med3_f32 v20, v20, s83, v238
	v_mov_b32_e32 v34, v0
	v_lshl_add_u64 v[64:65], v[104:105], 0, v[64:65]
	v_cvt_pk_fp8_f32 v34, v20, v20
	global_store_byte v[64:65], v71, off
	v_ashrrev_i32_e32 v71, 31, v70
	v_lshlrev_b64 v[70:71], 11, v[70:71]
	v_mul_f32_e32 v20, v46, v108
	v_lshl_add_u64 v[70:71], v[104:105], 0, v[70:71]
	v_mul_f32_e32 v20, v67, v20
	global_store_byte v[70:71], v34, off
	v_med3_f32 v20, v20, s83, v238
	v_mov_b32_e32 v34, v0
	v_cvt_pk_fp8_f32 v34, v20, v20
	v_mul_f32_e32 v20, v32, v1
	v_mul_f32_e32 v20, v67, v20
	v_med3_f32 v20, v20, s83, v238
	v_mov_b32_e32 v32, v0
	v_cvt_pk_fp8_f32 v32, v20, v20
	global_store_byte v[94:95], v69, off
	v_ashrrev_i32_e32 v69, 31, v68
	v_ashrrev_i32_e32 v67, 31, v66
	v_lshlrev_b64 v[68:69], 11, v[68:69]
	v_lshlrev_b64 v[66:67], 11, v[66:67]
	v_lshl_add_u64 v[68:69], v[104:105], 0, v[68:69]
	v_lshl_add_u64 v[66:67], v[104:105], 0, v[66:67]
	global_store_byte v[68:69], v34, off
	global_store_byte v[66:67], v32, off
	v_mov_b32_e32 v20, v236
	v_mul_f32_e32 v32, v101, v111
	v_mov_b32_e32 v34, v0
	v_mul_f32_e32 v32, v32, v20
	v_med3_f32 v32, v32, s83, v238
	v_cvt_pk_fp8_f32 v34, v32, v32
	v_mul_f32_e32 v32, v103, v109
	v_mul_f32_e32 v32, v32, v20
	v_med3_f32 v32, v32, s83, v238
	global_store_byte v[62:63], v34, off offset:32
	v_mov_b32_e32 v34, v0
	v_cvt_pk_fp8_f32 v34, v32, v32
	v_mul_f32_e32 v32, v35, v115
	v_mul_f32_e32 v32, v32, v20
	v_med3_f32 v32, v32, s83, v238
	global_store_byte v[64:65], v34, off offset:32
	v_mov_b32_e32 v34, v0
	v_mul_f32_e32 v21, v21, v20
	v_cvt_pk_fp8_f32 v34, v32, v32
	v_med3_f32 v21, v21, s83, v238
	v_mov_b32_e32 v32, v0
	v_cvt_pk_fp8_f32 v32, v21, v21
	v_mul_f32_e32 v21, v37, v119
	v_mul_f32_e32 v21, v21, v20
	v_med3_f32 v21, v21, s83, v238
	global_store_byte v[92:93], v32, off offset:32
	v_mov_b32_e32 v32, v0
	v_cvt_pk_fp8_f32 v32, v21, v21
	v_mul_f32_e32 v21, v53, v117
	v_mul_f32_e32 v21, v21, v20
	v_med3_f32 v21, v21, s83, v238
	global_store_byte v[90:91], v32, off offset:32
	v_mov_b32_e32 v32, v0
	v_cvt_pk_fp8_f32 v32, v21, v21
	v_mul_f32_e32 v21, v39, v125
	v_mul_f32_e32 v21, v21, v20
	v_med3_f32 v21, v21, s83, v238
	global_store_byte v[88:89], v32, off offset:32
	v_mov_b32_e32 v32, v0
	v_cvt_pk_fp8_f32 v32, v21, v21
	v_mul_f32_e32 v21, v55, v121
	v_mul_f32_e32 v21, v21, v20
	v_med3_f32 v21, v21, s83, v238
	global_store_byte v[86:87], v32, off offset:32
	v_mov_b32_e32 v32, v0
	v_cvt_pk_fp8_f32 v32, v21, v21
	v_mul_f32_e32 v21, v41, v126
	v_mul_f32_e32 v21, v21, v20
	v_med3_f32 v21, v21, s83, v238
	global_store_byte v[84:85], v32, off offset:32
	v_mov_b32_e32 v32, v0
	v_cvt_pk_fp8_f32 v32, v21, v21
	v_mul_f32_e32 v21, v57, v124
	v_mul_f32_e32 v21, v21, v20
	v_med3_f32 v21, v21, s83, v238
	global_store_byte v[82:83], v32, off offset:32
	v_mov_b32_e32 v32, v0
	v_cvt_pk_fp8_f32 v32, v21, v21
	v_mul_f32_e32 v21, v43, v120
	v_mul_f32_e32 v21, v21, v20
	v_med3_f32 v21, v21, s83, v238
	global_store_byte v[80:81], v32, off offset:32
	v_mov_b32_e32 v32, v0
	v_cvt_pk_fp8_f32 v32, v21, v21
	v_mul_f32_e32 v21, v59, v118
	v_mul_f32_e32 v21, v21, v20
	v_med3_f32 v21, v21, s83, v238
	global_store_byte v[78:79], v32, off offset:32
	v_mov_b32_e32 v32, v0
	v_cvt_pk_fp8_f32 v32, v21, v21
	v_mul_f32_e32 v21, v45, v114
	v_mul_f32_e32 v21, v21, v20
; __device__ __forceinline__ unsigned f2bf(float f) { unsigned u = __builtin_bit_cast(unsigned, f); return (u + 0x7fffu + ((u >> 16) & 1u)) >> 16; }
; __device__ __forceinline__ unsigned char f8_1(float a) { a = fminf(fmaxf(a, -448.f), 448.f); return (unsigned char)(__builtin_amdgcn_cvt_pk_fp8_f32(a, a, 0, false) & 0xff); }
; __device__ __forceinline__ int crow(int r, int hi) { return (r & 3) + 8 * (r >> 2) + 4 * hi; }
; __device__ __forceinline__ void diff_unit(KP Pk, Frame& F, int l, int b, int h, int qrow0, int nkt) {
;     ...
;         for (int nb = 0; nb < 4; ++nb) { const float w = Pk->in[I_DSUB][l * 128 + nb * 32 + r32];
; #pragma unroll
;             for (int r = 0; r < 16; ++r) { const float y = O[nb][r] * ssq[r] * w; const size_t e = (size_t)crow(r, hi) * D + nb * 32 + r32; if (WOUT_F8) mix[e] = f8_1(y); else ((bf16_t*)mix)[e] = (bf16_t)f2bf(y); } }
	v_med3_f32 v21, v21, s83, v238
	global_store_byte v[74:75], v32, off offset:32
	v_mov_b32_e32 v32, v0
	v_cvt_pk_fp8_f32 v32, v21, v21
	v_mul_f32_e32 v21, v61, v112
	v_mul_f32_e32 v21, v21, v20
	v_med3_f32 v21, v21, s83, v238
	global_store_byte v[72:73], v32, off offset:32
	v_mov_b32_e32 v32, v0
	v_cvt_pk_fp8_f32 v32, v21, v21
	v_mul_f32_e32 v21, v47, v108
	v_mul_f32_e32 v21, v21, v20
	v_med3_f32 v21, v21, s83, v238
	global_store_byte v[70:71], v32, off offset:32
	v_mov_b32_e32 v32, v0
	v_cvt_pk_fp8_f32 v32, v21, v21
	v_mul_f32_e32 v21, v33, v1
	v_mul_f32_e32 v20, v21, v20
	v_med3_f32 v20, v20, s83, v238
	v_mov_b32_e32 v21, v0
	v_cvt_pk_fp8_f32 v21, v20, v20
	global_store_byte v[94:95], v34, off offset:32
	global_store_byte v[68:69], v32, off offset:32
	v_mov_b32_e32 v32, v0
	global_store_byte v[66:67], v21, off offset:32
	v_mov_b32_e32 v20, v250
	v_mul_f32_e32 v21, v77, v111
	v_mul_f32_e32 v21, v21, v20
	v_med3_f32 v21, v21, s83, v238
	v_mul_f32_e32 v2, v2, v20
	v_cvt_pk_fp8_f32 v32, v21, v21
	v_med3_f32 v2, v2, s83, v238
	v_mov_b32_e32 v21, v0
	v_cvt_pk_fp8_f32 v21, v2, v2
	v_mul_f32_e32 v2, v18, v115
	v_mul_f32_e32 v2, v2, v20
	v_med3_f32 v2, v2, s83, v238
	v_mov_b32_e32 v18, v0
	v_cvt_pk_fp8_f32 v18, v2, v2
	v_mul_f32_e32 v2, v4, v113
	v_mul_f32_e32 v2, v2, v20
	v_med3_f32 v2, v2, s83, v238
	v_mov_b32_e32 v4, v0
	v_cvt_pk_fp8_f32 v4, v2, v2
	v_mul_f32_e32 v2, v50, v119
	v_mul_f32_e32 v2, v2, v20
	v_med3_f32 v2, v2, s83, v238
	global_store_byte v[92:93], v4, off offset:64
	v_mov_b32_e32 v4, v0
	v_cvt_pk_fp8_f32 v4, v2, v2
	v_mul_f32_e32 v2, v6, v117
	v_mul_f32_e32 v2, v2, v20
	v_med3_f32 v2, v2, s83, v238
	global_store_byte v[90:91], v4, off offset:64
	v_mov_b32_e32 v4, v0
	v_cvt_pk_fp8_f32 v4, v2, v2
	v_mul_f32_e32 v2, v22, v125
	v_mul_f32_e32 v2, v2, v20
	v_med3_f32 v2, v2, s83, v238
	global_store_byte v[88:89], v4, off offset:64
	v_mov_b32_e32 v4, v0
	v_cvt_pk_fp8_f32 v4, v2, v2
	v_mul_f32_e32 v2, v8, v121
	v_mul_f32_e32 v2, v2, v20
	v_med3_f32 v2, v2, s83, v238
	global_store_byte v[86:87], v4, off offset:64
	v_mov_b32_e32 v4, v0
	v_cvt_pk_fp8_f32 v4, v2, v2
	v_mul_f32_e32 v2, v24, v126
	v_mul_f32_e32 v2, v2, v20
	v_med3_f32 v2, v2, s83, v238
	global_store_byte v[84:85], v4, off offset:64
	v_mov_b32_e32 v4, v0
	v_cvt_pk_fp8_f32 v4, v2, v2
	v_mul_f32_e32 v2, v10, v124
	v_mul_f32_e32 v2, v2, v20
	v_med3_f32 v2, v2, s83, v238
	global_store_byte v[82:83], v4, off offset:64
	v_mov_b32_e32 v4, v0
	v_cvt_pk_fp8_f32 v4, v2, v2
	v_mul_f32_e32 v2, v26, v120
	v_mul_f32_e32 v2, v2, v20
	v_med3_f32 v2, v2, s83, v238
	global_store_byte v[80:81], v4, off offset:64
	v_mov_b32_e32 v4, v0
	v_cvt_pk_fp8_f32 v4, v2, v2
	v_mul_f32_e32 v2, v12, v118
	v_mul_f32_e32 v2, v2, v20
	v_med3_f32 v2, v2, s83, v238
	global_store_byte v[78:79], v4, off offset:64
	v_mov_b32_e32 v4, v0
	v_cvt_pk_fp8_f32 v4, v2, v2
	v_mul_f32_e32 v2, v28, v114
	v_mul_f32_e32 v2, v2, v20
	v_med3_f32 v2, v2, s83, v238
	global_store_byte v[74:75], v4, off offset:64
	v_mov_b32_e32 v4, v0
	v_cvt_pk_fp8_f32 v4, v2, v2
	v_mul_f32_e32 v2, v14, v112
	v_mul_f32_e32 v2, v2, v20
	v_med3_f32 v2, v2, s83, v238
	global_store_byte v[72:73], v4, off offset:64
	v_mov_b32_e32 v4, v0
	v_cvt_pk_fp8_f32 v4, v2, v2
	v_mul_f32_e32 v2, v30, v108
	v_mul_f32_e32 v2, v2, v20
	v_med3_f32 v2, v2, s83, v238
	global_store_byte v[70:71], v4, off offset:64
	v_mov_b32_e32 v4, v0
	v_cvt_pk_fp8_f32 v4, v2, v2
	v_mul_f32_e32 v2, v16, v1
	v_mul_f32_e32 v2, v2, v20
	v_med3_f32 v2, v2, s83, v238
	global_store_byte v[68:69], v4, off offset:64
	v_mov_b32_e32 v4, v0
	v_cvt_pk_fp8_f32 v4, v2, v2
	global_store_byte v[62:63], v32, off offset:64
	global_store_byte v[64:65], v21, off offset:64
	global_store_byte v[94:95], v18, off offset:64
	global_store_byte v[66:67], v4, off offset:64
	v_mov_b32_e32 v2, v251
	v_mul_f32_e32 v4, v76, v111
	v_mov_b32_e32 v6, v0
	v_mul_f32_e32 v1, v17, v1
	v_mul_f32_e32 v4, v4, v2
	v_med3_f32 v4, v4, s83, v238
	v_mul_f32_e32 v3, v3, v2
	v_cvt_pk_fp8_f32 v6, v4, v4
	v_med3_f32 v3, v3, s83, v238
	v_mov_b32_e32 v4, v0
	v_cvt_pk_fp8_f32 v4, v3, v3
	v_mul_f32_e32 v3, v19, v115
	v_mul_f32_e32 v3, v3, v2
	v_med3_f32 v3, v3, s83, v238
	global_store_byte v[64:65], v4, off offset:96
	v_mov_b32_e32 v4, v0
	v_cvt_pk_fp8_f32 v4, v3, v3
	v_mul_f32_e32 v3, v5, v113
	v_mul_f32_e32 v3, v3, v2
	v_med3_f32 v3, v3, s83, v238
	global_store_byte v[94:95], v4, off offset:96
	v_mov_b32_e32 v4, v0
	v_cvt_pk_fp8_f32 v4, v3, v3
	v_mul_f32_e32 v3, v51, v119
	v_mul_f32_e32 v3, v3, v2
	v_med3_f32 v3, v3, s83, v238
	global_store_byte v[92:93], v4, off offset:96
	v_mov_b32_e32 v4, v0
	v_cvt_pk_fp8_f32 v4, v3, v3
	v_mul_f32_e32 v3, v7, v117
	v_mul_f32_e32 v3, v3, v2
	v_med3_f32 v3, v3, s83, v238
	global_store_byte v[90:91], v4, off offset:96
	v_mov_b32_e32 v4, v0
	v_cvt_pk_fp8_f32 v4, v3, v3
	v_mul_f32_e32 v3, v23, v125
	v_mul_f32_e32 v3, v3, v2
	v_med3_f32 v3, v3, s83, v238
	global_store_byte v[88:89], v4, off offset:96
	v_mov_b32_e32 v4, v0
	v_cvt_pk_fp8_f32 v4, v3, v3
	v_mul_f32_e32 v3, v9, v121
	v_mul_f32_e32 v3, v3, v2
	v_med3_f32 v3, v3, s83, v238
	global_store_byte v[86:87], v4, off offset:96
	v_mov_b32_e32 v4, v0
	v_cvt_pk_fp8_f32 v4, v3, v3
	v_mul_f32_e32 v3, v25, v126
	v_mul_f32_e32 v3, v3, v2
	v_med3_f32 v3, v3, s83, v238
	global_store_byte v[84:85], v4, off offset:96
	v_mov_b32_e32 v4, v0
	v_cvt_pk_fp8_f32 v4, v3, v3
	v_mul_f32_e32 v3, v11, v124
	v_mul_f32_e32 v3, v3, v2
	v_med3_f32 v3, v3, s83, v238
	global_store_byte v[82:83], v4, off offset:96
	v_mov_b32_e32 v4, v0
	v_cvt_pk_fp8_f32 v4, v3, v3
	v_mul_f32_e32 v3, v27, v120
	v_mul_f32_e32 v3, v3, v2
	v_med3_f32 v3, v3, s83, v238
	global_store_byte v[80:81], v4, off offset:96
	v_mov_b32_e32 v4, v0
	v_cvt_pk_fp8_f32 v4, v3, v3
	v_mul_f32_e32 v3, v13, v118
	v_mul_f32_e32 v3, v3, v2
	v_med3_f32 v3, v3, s83, v238
	global_store_byte v[78:79], v4, off offset:96
	v_mov_b32_e32 v4, v0
	v_cvt_pk_fp8_f32 v4, v3, v3
	v_mul_f32_e32 v3, v29, v114
	v_mul_f32_e32 v3, v3, v2
	v_med3_f32 v3, v3, s83, v238
	global_store_byte v[74:75], v4, off offset:96
	v_mov_b32_e32 v4, v0
	v_cvt_pk_fp8_f32 v4, v3, v3
	v_mul_f32_e32 v3, v15, v112
	v_mul_f32_e32 v3, v3, v2
	v_med3_f32 v3, v3, s83, v238
	global_store_byte v[72:73], v4, off offset:96
	v_mov_b32_e32 v4, v0
	v_cvt_pk_fp8_f32 v4, v3, v3
	v_mul_f32_e32 v3, v31, v108
	v_mul_f32_e32 v3, v3, v2
	v_mul_f32_e32 v1, v1, v2
	global_store_byte v[70:71], v4, off offset:96
	v_med3_f32 v3, v3, s83, v238
	v_mov_b32_e32 v4, v0
	v_med3_f32 v1, v1, s83, v238
	v_mov_b32_e32 v2, v0
	v_cvt_pk_fp8_f32 v4, v3, v3
	v_cvt_pk_fp8_f32 v2, v1, v1
	global_store_byte v[62:63], v6, off offset:96
	global_store_byte v[68:69], v4, off offset:96
	global_store_byte v[66:67], v2, off offset:96

; __device__ __forceinline__ int crow(int r, int hi) { return (r & 3) + 8 * (r >> 2) + 4 * hi; }
; __device__ __forceinline__ void diff_unit(KP Pk, Frame& F, int l, int b, int h, int qrow0, int nkt) {
;     ...
;     if (m == 0) {
;         const float* dl = Pk->in[I_DLAM] + l * 256; const float lam_init = __builtin_bit_cast(float, __builtin_amdgcn_readfirstlane(__builtin_bit_cast(int, l == 0 ? 0.2f : (0.8f - 0.6f * 0.74081822068f))));
;         const float lam = expf(wave_sum(dl[ln_] * dl[64 + ln_])) - expf(wave_sum(dl[128 + ln_] * dl[192 + ln_])) + lam_init;
;         float ssq[16];
; #pragma unroll
;         for (int r = 0; r < 16; ++r) { float a = 0.f;
; #pragma unroll
;             for (int nb = 0; nb < 4; ++nb) { const float v = O[nb][r] * rlr[r] - lam * ex[crow(r, hi) * 128 + nb * 32 + r32]; O[nb][r] = v; a += v * v; }
;             a += __shfl_xor(a, 1); a += __shfl_xor(a, 2); a += __shfl_xor(a, 4); a += __shfl_xor(a, 8); a += __shfl_xor(a, 16);
;             ssq[r] = rsqrtf(a * (1.f / 128.f) + NORM_EPS) * (1.f - lam_init); }
.LBB0_637:
	v_readlane_b32 s26, v253, 17
	v_readlane_b32 s27, v253, 18
	s_andn2_b64 vcc, exec, s[26:27]
	s_waitcnt lgkmcnt(0)
	s_barrier
	s_cbranch_vccnz .LBB0_639
	s_load_dwordx4 s[44:47], s[8:9], 0xd8
	s_lshl_b32 s8, s4, 8
	s_ashr_i32 s9, s8, 31
	s_lshl_b64 s[8:9], s[8:9], 2
	v_ashrrev_i32_e32 v101, 31, v100
	s_waitcnt lgkmcnt(0)
	s_add_u32 s8, s44, s8
	s_addc_u32 s9, s45, s9
	v_lshl_add_u64 v[100:101], v[100:101], 2, s[8:9]
	global_load_dword v69, v[100:101], off
	global_load_dword v71, v[100:101], off offset:256
	global_load_dword v250, v[100:101], off offset:512
	global_load_dword v251, v[100:101], off offset:768
	s_cmp_eq_u32 s4, 0
	s_mov_b32 s5, 0x3e4ccccd
	s_cselect_b32 s5, s5, 0x3eb60549
	v_mov_b32_e32 v102, v2
	v_mov_b32_e32 v103, v18
	v_mov_b32_e32 v146, v50
	v_mov_b32_e32 v147, v34
	v_mov_b32_e32 v18, v3
	v_mov_b32_e32 v50, v35
	s_mov_b32 s8, 0x358637bd
	v_mov_b32_e32 v106, s46
	v_mov_b32_e32 v107, s47
	s_ashr_i32 s41, s40, 31
	v_mov_b32_e32 v105, v0
	v_ashrrev_i32_e32 v93, 31, v92
	v_lshlrev_b64 v[92:93], 11, v[92:93]
	v_ashrrev_i32_e32 v91, 31, v90
	v_lshlrev_b64 v[90:91], 11, v[90:91]
	v_ashrrev_i32_e32 v89, 31, v88
	v_lshlrev_b64 v[88:89], 11, v[88:89]
	v_ashrrev_i32_e32 v87, 31, v86
	v_lshlrev_b64 v[86:87], 11, v[86:87]
	v_ashrrev_i32_e32 v85, 31, v84
	v_lshlrev_b64 v[84:85], 11, v[84:85]
	v_ashrrev_i32_e32 v83, 31, v82
	v_lshlrev_b64 v[82:83], 11, v[82:83]
	v_ashrrev_i32_e32 v81, 31, v80
	v_lshlrev_b64 v[80:81], 11, v[80:81]
	v_ashrrev_i32_e32 v79, 31, v78
	v_lshlrev_b64 v[78:79], 11, v[78:79]
	v_ashrrev_i32_e32 v99, 31, v98
	v_ashrrev_i32_e32 v97, 31, v96
	v_ashrrev_i32_e32 v95, 31, v94
	v_lshlrev_b64 v[94:95], 11, v[94:95]
	s_waitcnt vmcnt(0)
	v_mul_f32_e32 v73, v69, v71
	ds_bpermute_b32 v73, v142, v73
	s_waitcnt lgkmcnt(0)
	v_fmac_f32_e32 v73, v69, v71
	ds_bpermute_b32 v69, v141, v73
	s_waitcnt lgkmcnt(0)
	v_add_f32_e32 v69, v73, v69
	ds_bpermute_b32 v71, v140, v69
	s_waitcnt lgkmcnt(0)
	v_add_f32_e32 v69, v69, v71
	ds_bpermute_b32 v71, v139, v69
	s_waitcnt lgkmcnt(0)
	v_add_f32_e32 v69, v69, v71
	ds_bpermute_b32 v71, v1, v69
	s_waitcnt lgkmcnt(0)
	v_add_f32_e32 v69, v69, v71
	ds_bpermute_b32 v71, v143, v69
	s_waitcnt lgkmcnt(0)
	v_add_f32_e32 v69, v69, v71
	v_mul_f32_e32 v71, 0x3fb8aa3b, v69
	v_fma_f32 v73, v69, s10, -v71
	v_rndne_f32_e32 v75, v71
	v_fmac_f32_e32 v73, 0x32a5705f, v69
	v_sub_f32_e32 v71, v71, v75
	v_add_f32_e32 v71, v71, v73
	v_exp_f32_e32 v71, v71
	v_cvt_i32_f32_e32 v73, v75
	v_cmp_ngt_f32_e32 vcc, s11, v69
	v_ldexp_f32 v71, v71, v73
	s_nop 0
	v_cndmask_b32_e32 v71, 0, v71, vcc
	v_cmp_nlt_f32_e32 vcc, s12, v69
	s_nop 1
	v_cndmask_b32_e32 v69, v237, v71, vcc
	v_mov_b32_e32 v71, v250
	v_mov_b32_e32 v73, v251
	ds_read2_b32 v[100:101], v67 offset1:32
	v_mul_f32_e32 v75, v71, v73
	ds_bpermute_b32 v75, v142, v75
	s_waitcnt lgkmcnt(0)
	v_fmac_f32_e32 v75, v71, v73
	ds_bpermute_b32 v71, v141, v75
	s_waitcnt lgkmcnt(0)
	v_add_f32_e32 v71, v75, v71
	ds_bpermute_b32 v73, v140, v71
	s_waitcnt lgkmcnt(0)
	v_add_f32_e32 v71, v71, v73
	ds_bpermute_b32 v73, v139, v71
	s_waitcnt lgkmcnt(0)
	v_add_f32_e32 v71, v71, v73
	ds_bpermute_b32 v73, v1, v71
	s_waitcnt lgkmcnt(0)
	v_add_f32_e32 v71, v71, v73
	ds_bpermute_b32 v73, v143, v71
	s_waitcnt lgkmcnt(0)
	v_add_f32_e32 v71, v71, v73
	v_mul_f32_e32 v73, 0x3fb8aa3b, v71
	v_fma_f32 v75, v71, s10, -v73
	v_rndne_f32_e32 v77, v73
	v_fmac_f32_e32 v75, 0x32a5705f, v71
	v_sub_f32_e32 v73, v73, v77
	v_add_f32_e32 v73, v73, v75
	v_exp_f32_e32 v73, v73
	v_cvt_i32_f32_e32 v75, v77
	v_cmp_ngt_f32_e32 vcc, s11, v71
	v_ldexp_f32 v73, v73, v75
	s_nop 0
	v_cndmask_b32_e32 v73, 0, v73, vcc
	v_cmp_nlt_f32_e32 vcc, s12, v71
	v_ashrrev_i32_e32 v75, 31, v74
	v_lshlrev_b64 v[74:75], 11, v[74:75]
	v_cndmask_b32_e32 v71, v237, v73, vcc
	v_sub_f32_e32 v69, v69, v71
	v_add_f32_e32 v116, s5, v69
	v_pk_mul_f32 v[100:101], v[100:101], v[116:117] op_sel_hi:[1,0]
	v_sub_f32_e64 v69, 1.0, s5
	v_pk_fma_f32 v[100:101], v[102:103], v[76:77], v[100:101] op_sel_hi:[1,0,1] neg_lo:[0,0,1] neg_hi:[0,0,1]
	ds_read2_b32 v[102:103], v67 offset0:64 offset1:96
	v_pk_mul_f32 v[144:145], v[100:101], v[100:101]
	v_add_u32_e32 v71, 0x400, v67
	v_readlane_b32 s5, v254, 61
	v_ashrrev_i32_e32 v73, 31, v72
	s_waitcnt lgkmcnt(0)
	v_mov_b32_e32 v148, v103
	v_mov_b32_e32 v149, v102
	v_pk_mul_f32 v[102:103], v[116:117], v[148:149] op_sel_hi:[0,1]
	v_pk_fma_f32 v[76:77], v[146:147], v[76:77], v[102:103] op_sel_hi:[1,0,1] neg_lo:[0,0,1] neg_hi:[0,0,1]
	ds_read2_b32 v[102:103], v67 offset0:128 offset1:160
	v_pk_mul_f32 v[146:147], v[76:77], v[76:77]
	v_lshlrev_b64 v[72:73], 11, v[72:73]
	s_waitcnt lgkmcnt(0)
	v_pk_mul_f32 v[2:3], v[116:117], v[102:103] op_sel_hi:[0,1]
	v_pk_fma_f32 v[102:103], v[18:19], v[122:123], v[2:3] op_sel_hi:[1,0,1] neg_lo:[0,0,1] neg_hi:[0,0,1]
	ds_read2_b32 v[2:3], v67 offset0:192 offset1:224
	v_pk_mul_f32 v[18:19], v[102:103], v[102:103]
	s_waitcnt lgkmcnt(0)
	v_pk_mul_f32 v[2:3], v[116:117], v[2:3] op_sel_hi:[0,1]
	v_pk_fma_f32 v[2:3], v[50:51], v[122:123], v[2:3] op_sel_hi:[1,0,1] neg_lo:[0,0,1] neg_hi:[0,0,1]
	v_mov_b32_e32 v50, v18
	v_pk_mul_f32 v[34:35], v[2:3], v[2:3]
	v_mov_b32_e32 v51, v144
	v_mov_b32_e32 v144, v19
	v_pk_add_f32 v[18:19], v[50:51], v[144:145]
	v_mov_b32_e32 v50, v34
	v_mov_b32_e32 v51, v147
	v_pk_add_f32 v[18:19], v[18:19], v[50:51]
	v_pk_mov_b32 v[34:35], v[34:35], v[146:147] op_sel:[1,0]
	v_mov_b64_e32 v[122:123], s[8:9]
	v_pk_add_f32 v[18:19], v[18:19], v[34:35]
	ds_bpermute_b32 v35, v142, v19
	ds_bpermute_b32 v34, v142, v18
	s_brev_b32 s8, 60
	ds_read2_b32 v[146:147], v71 offset0:128 offset1:160
	v_mov_b32_e32 v144, v36
	v_mov_b32_e32 v145, v52
	s_waitcnt lgkmcnt(1)
; __device__ __forceinline__ int crow(int r, int hi) { return (r & 3) + 8 * (r >> 2) + 4 * hi; }
; __device__ __forceinline__ void diff_unit(KP Pk, Frame& F, int l, int b, int h, int qrow0, int nkt) {
;     ...
;         for (int r = 0; r < 16; ++r) { float a = 0.f;
; #pragma unroll
;             for (int nb = 0; nb < 4; ++nb) { const float v = O[nb][r] * rlr[r] - lam * ex[crow(r, hi) * 128 + nb * 32 + r32]; O[nb][r] = v; a += v * v; }
;             a += __shfl_xor(a, 1); a += __shfl_xor(a, 2); a += __shfl_xor(a, 4); a += __shfl_xor(a, 8); a += __shfl_xor(a, 16);
;             ssq[r] = rsqrtf(a * (1.f / 128.f) + NORM_EPS) * (1.f - lam_init); }
	v_pk_add_f32 v[18:19], v[18:19], v[34:35]
	ds_bpermute_b32 v35, v141, v19
	ds_bpermute_b32 v34, v141, v18
	v_mov_b32_e32 v52, v37
	s_waitcnt lgkmcnt(0)
	v_pk_add_f32 v[18:19], v[18:19], v[34:35]
	ds_bpermute_b32 v35, v140, v19
	ds_bpermute_b32 v34, v140, v18
	s_waitcnt lgkmcnt(0)
	v_pk_add_f32 v[18:19], v[18:19], v[34:35]
	ds_bpermute_b32 v35, v139, v19
	ds_bpermute_b32 v34, v139, v18
	s_waitcnt lgkmcnt(0)
	v_pk_add_f32 v[18:19], v[18:19], v[34:35]
	ds_bpermute_b32 v35, v1, v19
	ds_bpermute_b32 v34, v1, v18
	s_waitcnt lgkmcnt(0)
	v_pk_add_f32 v[18:19], v[18:19], v[34:35]
	s_nop 0
	v_pk_fma_f32 v[18:19], v[18:19], s[8:9], v[122:123] op_sel_hi:[1,0,0]
	v_mov_b32_e32 v35, v20
	v_mul_f32_e32 v34, 0x4b800000, v19
	v_cmp_gt_f32_e64 s[38:39], s66, v19
	v_cmp_gt_f32_e32 vcc, s66, v18
	v_mov_b32_e32 v20, v5
	v_cndmask_b32_e64 v19, v19, v34, s[38:39]
	v_rsq_f32_e32 v19, v19
	s_nop 0
	v_mul_f32_e32 v34, 0x45800000, v19
	v_cndmask_b32_e64 v19, v19, v34, s[38:39]
	v_mul_f32_e32 v111, v69, v19
	v_mul_f32_e32 v19, 0x4b800000, v18
	v_cndmask_b32_e32 v18, v18, v19, vcc
	v_rsq_f32_e32 v18, v18
	v_mov_b32_e32 v34, v4
	v_pk_mul_f32 v[4:5], v[116:117], v[146:147] op_sel_hi:[0,1]
	v_pk_fma_f32 v[20:21], v[20:21], v[136:137], v[4:5] op_sel_hi:[1,0,1] neg_lo:[0,0,1] neg_hi:[0,0,1]
	v_mul_f32_e32 v19, 0x45800000, v18
	v_cndmask_b32_e32 v18, v18, v19, vcc
	v_mul_f32_e32 v109, v69, v18
	ds_read2_b32 v[18:19], v71 offset1:32
	ds_read2_b32 v[4:5], v71 offset0:192 offset1:224
	v_pk_mul_f32 v[146:147], v[20:21], v[20:21]
	v_mul_f32_e32 v2, v2, v109
	v_mul_f32_e32 v3, v3, v109
	s_waitcnt lgkmcnt(1)
	v_pk_mul_f32 v[18:19], v[116:117], v[18:19] op_sel_hi:[0,1]
	v_pk_fma_f32 v[34:35], v[34:35], v[138:139], v[18:19] op_sel_hi:[1,0,1] neg_lo:[0,0,1] neg_hi:[0,0,1]
	ds_read2_b32 v[18:19], v71 offset0:64 offset1:96
	s_waitcnt lgkmcnt(1)
	v_pk_mul_f32 v[4:5], v[116:117], v[4:5] op_sel_hi:[0,1]
	v_pk_mul_f32 v[50:51], v[34:35], v[34:35]
	v_pk_fma_f32 v[4:5], v[52:53], v[136:137], v[4:5] op_sel_hi:[1,0,1] neg_lo:[0,0,1] neg_hi:[0,0,1]
	v_mov_b32_e32 v52, v146
	s_waitcnt lgkmcnt(0)
	v_pk_mul_f32 v[18:19], v[116:117], v[18:19] op_sel_hi:[0,1]
	v_pk_fma_f32 v[18:19], v[144:145], v[138:139], v[18:19] op_sel_hi:[1,0,1] neg_lo:[0,0,1] neg_hi:[0,0,1]
	v_pk_mul_f32 v[36:37], v[4:5], v[4:5]
	v_pk_mul_f32 v[144:145], v[18:19], v[18:19]
	v_mov_b32_e32 v53, v50
	v_mov_b32_e32 v50, v147
	v_pk_add_f32 v[50:51], v[52:53], v[50:51]
	v_mov_b32_e32 v52, v36
	v_mov_b32_e32 v53, v144
	v_pk_add_f32 v[50:51], v[50:51], v[52:53]
	v_mov_b32_e32 v144, v37
	v_pk_add_f32 v[36:37], v[50:51], v[144:145]
	ds_bpermute_b32 v51, v142, v37
	ds_bpermute_b32 v50, v142, v36
	v_add_u32_e32 v71, 0x1000, v67
	v_mov_b32_e32 v52, v38
	v_mov_b32_e32 v53, v54
	v_mov_b32_e32 v54, v39
	s_waitcnt lgkmcnt(0)
	v_pk_add_f32 v[36:37], v[36:37], v[50:51]
	ds_bpermute_b32 v51, v141, v37
	ds_bpermute_b32 v50, v141, v36
	s_waitcnt lgkmcnt(0)
	v_pk_add_f32 v[36:37], v[36:37], v[50:51]
	ds_bpermute_b32 v51, v140, v37
	ds_bpermute_b32 v50, v140, v36
	s_waitcnt lgkmcnt(0)
	v_pk_add_f32 v[36:37], v[36:37], v[50:51]
	ds_bpermute_b32 v51, v139, v37
	ds_bpermute_b32 v50, v139, v36
	s_waitcnt lgkmcnt(0)
	v_pk_add_f32 v[36:37], v[36:37], v[50:51]
	ds_bpermute_b32 v51, v1, v37
	ds_bpermute_b32 v50, v1, v36
	s_waitcnt lgkmcnt(0)
	v_pk_add_f32 v[36:37], v[36:37], v[50:51]
	s_nop 0
	v_pk_fma_f32 v[36:37], v[36:37], s[8:9], v[122:123] op_sel_hi:[1,0,0]
	v_mov_b32_e32 v51, v22
	v_mul_f32_e32 v50, 0x4b800000, v37
	v_cmp_gt_f32_e64 s[38:39], s66, v37
	v_cmp_gt_f32_e32 vcc, s66, v36
	v_mov_b32_e32 v22, v7
	v_cndmask_b32_e64 v37, v37, v50, s[38:39]
	v_rsq_f32_e32 v37, v37
	s_nop 0
	v_mul_f32_e32 v50, 0x45800000, v37
	v_cndmask_b32_e64 v37, v37, v50, s[38:39]
	v_mul_f32_e32 v115, v69, v37
	v_mul_f32_e32 v37, 0x4b800000, v36
	v_cndmask_b32_e32 v36, v36, v37, vcc
	v_rsq_f32_e32 v36, v36
	v_mov_b32_e32 v50, v6
	v_mul_f32_e32 v34, v34, v115
	v_mul_f32_e32 v37, 0x45800000, v36
	v_cndmask_b32_e32 v36, v36, v37, vcc
	v_mul_f32_e32 v113, v69, v36
	ds_read2_b32 v[36:37], v71 offset1:32
	v_mul_f32_e32 v20, v20, v113
	v_mul_f32_e32 v21, v21, v113
	s_waitcnt lgkmcnt(0)
	v_pk_mul_f32 v[36:37], v[116:117], v[36:37] op_sel_hi:[0,1]
	v_pk_fma_f32 v[36:37], v[50:51], v[134:135], v[36:37] op_sel_hi:[1,0,1] neg_lo:[0,0,1] neg_hi:[0,0,1]
	ds_read2_b32 v[50:51], v71 offset0:64 offset1:96
	v_pk_mul_f32 v[136:137], v[36:37], v[36:37]
	s_waitcnt lgkmcnt(0)
	v_pk_mul_f32 v[50:51], v[116:117], v[50:51] op_sel_hi:[0,1]
	v_pk_fma_f32 v[50:51], v[52:53], v[134:135], v[50:51] op_sel_hi:[1,0,1] neg_lo:[0,0,1] neg_hi:[0,0,1]
	ds_read2_b32 v[52:53], v71 offset0:128 offset1:160
	v_pk_mul_f32 v[134:135], v[50:51], v[50:51]
	s_waitcnt lgkmcnt(0)
	v_pk_mul_f32 v[6:7], v[116:117], v[52:53] op_sel_hi:[0,1]
	v_pk_fma_f32 v[52:53], v[22:23], v[132:133], v[6:7] op_sel_hi:[1,0,1] neg_lo:[0,0,1] neg_hi:[0,0,1]
	ds_read2_b32 v[6:7], v71 offset0:192 offset1:224
	v_pk_mul_f32 v[22:23], v[52:53], v[52:53]
	v_add_u32_e32 v71, 0x1400, v67
	s_waitcnt lgkmcnt(0)
	v_pk_mul_f32 v[6:7], v[116:117], v[6:7] op_sel_hi:[0,1]
	v_pk_fma_f32 v[6:7], v[54:55], v[132:133], v[6:7] op_sel_hi:[1,0,1] neg_lo:[0,0,1] neg_hi:[0,0,1]
	v_mov_b32_e32 v54, v22
	v_pk_mul_f32 v[38:39], v[6:7], v[6:7]
	v_mov_b32_e32 v55, v136
	v_mov_b32_e32 v136, v23
	v_pk_add_f32 v[22:23], v[54:55], v[136:137]
	v_mov_b32_e32 v54, v38
	v_mov_b32_e32 v55, v134
	v_pk_add_f32 v[22:23], v[22:23], v[54:55]
	v_mov_b32_e32 v134, v39
	v_pk_add_f32 v[22:23], v[22:23], v[134:135]
	ds_bpermute_b32 v39, v142, v23
	ds_bpermute_b32 v38, v142, v22
	v_mov_b32_e32 v54, v40
	v_mov_b32_e32 v55, v56
	v_mov_b32_e32 v56, v41
	s_waitcnt lgkmcnt(0)
; __device__ __forceinline__ int crow(int r, int hi) { return (r & 3) + 8 * (r >> 2) + 4 * hi; }
; __device__ __forceinline__ void diff_unit(KP Pk, Frame& F, int l, int b, int h, int qrow0, int nkt) {
;     ...
;         for (int r = 0; r < 16; ++r) { float a = 0.f;
; #pragma unroll
;             for (int nb = 0; nb < 4; ++nb) { const float v = O[nb][r] * rlr[r] - lam * ex[crow(r, hi) * 128 + nb * 32 + r32]; O[nb][r] = v; a += v * v; }
;             a += __shfl_xor(a, 1); a += __shfl_xor(a, 2); a += __shfl_xor(a, 4); a += __shfl_xor(a, 8); a += __shfl_xor(a, 16);
;             ssq[r] = rsqrtf(a * (1.f / 128.f) + NORM_EPS) * (1.f - lam_init); }
	v_pk_add_f32 v[22:23], v[22:23], v[38:39]
	ds_bpermute_b32 v39, v141, v23
	ds_bpermute_b32 v38, v141, v22
	s_waitcnt lgkmcnt(0)
	v_pk_add_f32 v[22:23], v[22:23], v[38:39]
	ds_bpermute_b32 v39, v140, v23
	ds_bpermute_b32 v38, v140, v22
	s_waitcnt lgkmcnt(0)
	v_pk_add_f32 v[22:23], v[22:23], v[38:39]
	ds_bpermute_b32 v39, v139, v23
	ds_bpermute_b32 v38, v139, v22
	s_waitcnt lgkmcnt(0)
	v_pk_add_f32 v[22:23], v[22:23], v[38:39]
	ds_bpermute_b32 v39, v1, v23
	ds_bpermute_b32 v38, v1, v22
	s_waitcnt lgkmcnt(0)
	v_pk_add_f32 v[22:23], v[22:23], v[38:39]
	s_nop 0
	v_pk_fma_f32 v[22:23], v[22:23], s[8:9], v[122:123] op_sel_hi:[1,0,0]
	v_mov_b32_e32 v39, v24
	v_mul_f32_e32 v38, 0x4b800000, v23
	v_cmp_gt_f32_e64 s[38:39], s66, v23
	v_cmp_gt_f32_e32 vcc, s66, v22
	v_mov_b32_e32 v24, v9
	v_cndmask_b32_e64 v23, v23, v38, s[38:39]
	v_rsq_f32_e32 v23, v23
	s_nop 0
	v_mul_f32_e32 v38, 0x45800000, v23
	v_cndmask_b32_e64 v23, v23, v38, s[38:39]
	v_mul_f32_e32 v119, v69, v23
	v_mul_f32_e32 v23, 0x4b800000, v22
	v_cndmask_b32_e32 v22, v22, v23, vcc
	v_rsq_f32_e32 v22, v22
	v_mov_b32_e32 v38, v8
	v_mul_f32_e32 v23, 0x45800000, v22
	v_cndmask_b32_e32 v22, v22, v23, vcc
	v_mul_f32_e32 v117, v69, v22
	ds_read2_b32 v[22:23], v71 offset1:32
	s_waitcnt lgkmcnt(0)
	v_pk_mul_f32 v[22:23], v[116:117], v[22:23] op_sel_hi:[0,1]
	v_pk_fma_f32 v[38:39], v[38:39], v[130:131], v[22:23] op_sel_hi:[1,0,1] neg_lo:[0,0,1] neg_hi:[0,0,1]
	ds_read2_b32 v[22:23], v71 offset0:64 offset1:96
	v_pk_mul_f32 v[132:133], v[38:39], v[38:39]
	s_waitcnt lgkmcnt(0)
	v_pk_mul_f32 v[22:23], v[116:117], v[22:23] op_sel_hi:[0,1]
	v_pk_fma_f32 v[22:23], v[54:55], v[130:131], v[22:23] op_sel_hi:[1,0,1] neg_lo:[0,0,1] neg_hi:[0,0,1]
	ds_read2_b32 v[54:55], v71 offset0:128 offset1:160
	v_pk_mul_f32 v[130:131], v[22:23], v[22:23]
	s_waitcnt lgkmcnt(0)
	v_pk_mul_f32 v[8:9], v[116:117], v[54:55] op_sel_hi:[0,1]
	v_pk_fma_f32 v[54:55], v[24:25], v[128:129], v[8:9] op_sel_hi:[1,0,1] neg_lo:[0,0,1] neg_hi:[0,0,1]
	ds_read2_b32 v[8:9], v71 offset0:192 offset1:224
	v_pk_mul_f32 v[24:25], v[54:55], v[54:55]
	v_add_u32_e32 v71, 0x2000, v67
	s_waitcnt lgkmcnt(0)
	v_pk_mul_f32 v[8:9], v[116:117], v[8:9] op_sel_hi:[0,1]
	v_pk_fma_f32 v[8:9], v[56:57], v[128:129], v[8:9] op_sel_hi:[1,0,1] neg_lo:[0,0,1] neg_hi:[0,0,1]
	v_mov_b32_e32 v56, v24
	v_pk_mul_f32 v[40:41], v[8:9], v[8:9]
	v_mov_b32_e32 v57, v132
	v_mov_b32_e32 v132, v25
	v_pk_add_f32 v[24:25], v[56:57], v[132:133]
	v_mov_b32_e32 v56, v40
	v_mov_b32_e32 v57, v130
	v_pk_add_f32 v[24:25], v[24:25], v[56:57]
	v_mov_b32_e32 v130, v41
	v_pk_add_f32 v[24:25], v[24:25], v[130:131]
	ds_bpermute_b32 v41, v142, v25
	ds_bpermute_b32 v40, v142, v24
	v_mov_b32_e32 v56, v42
	v_mov_b32_e32 v57, v58
	v_mov_b32_e32 v58, v43
	s_waitcnt lgkmcnt(0)
	v_pk_add_f32 v[24:25], v[24:25], v[40:41]
	ds_bpermute_b32 v41, v141, v25
	ds_bpermute_b32 v40, v141, v24
	s_waitcnt lgkmcnt(0)
	v_pk_add_f32 v[24:25], v[24:25], v[40:41]
	ds_bpermute_b32 v41, v140, v25
	ds_bpermute_b32 v40, v140, v24
	s_waitcnt lgkmcnt(0)
	v_pk_add_f32 v[24:25], v[24:25], v[40:41]
	ds_bpermute_b32 v41, v139, v25
	ds_bpermute_b32 v40, v139, v24
	s_waitcnt lgkmcnt(0)
	v_pk_add_f32 v[24:25], v[24:25], v[40:41]
	ds_bpermute_b32 v41, v1, v25
	ds_bpermute_b32 v40, v1, v24
	s_waitcnt lgkmcnt(0)
	v_pk_add_f32 v[24:25], v[24:25], v[40:41]
	s_nop 0
	v_pk_fma_f32 v[24:25], v[24:25], s[8:9], v[122:123] op_sel_hi:[1,0,0]
	v_mov_b32_e32 v41, v26
	v_mul_f32_e32 v40, 0x4b800000, v25
	v_cmp_gt_f32_e64 s[38:39], s66, v25
	v_cmp_gt_f32_e32 vcc, s66, v24
	v_mov_b32_e32 v26, v11
	v_cndmask_b32_e64 v25, v25, v40, s[38:39]
	v_rsq_f32_e32 v25, v25
	s_nop 0
	v_mul_f32_e32 v40, 0x45800000, v25
	v_cndmask_b32_e64 v25, v25, v40, s[38:39]
	v_mul_f32_e32 v125, v69, v25
	v_mul_f32_e32 v25, 0x4b800000, v24
	v_cndmask_b32_e32 v24, v24, v25, vcc
	v_rsq_f32_e32 v24, v24
	v_mov_b32_e32 v40, v10
	v_mul_f32_e32 v25, 0x45800000, v24
	v_cndmask_b32_e32 v24, v24, v25, vcc
	v_mul_f32_e32 v121, v69, v24
	ds_read2_b32 v[24:25], v71 offset1:32
	s_waitcnt lgkmcnt(0)
	v_pk_mul_f32 v[24:25], v[116:117], v[24:25] op_sel_hi:[0,1]
	v_pk_fma_f32 v[40:41], v[40:41], v[126:127], v[24:25] op_sel_hi:[1,0,1] neg_lo:[0,0,1] neg_hi:[0,0,1]
	ds_read2_b32 v[24:25], v71 offset0:64 offset1:96
	v_pk_mul_f32 v[128:129], v[40:41], v[40:41]
	s_waitcnt lgkmcnt(0)
	v_pk_mul_f32 v[24:25], v[116:117], v[24:25] op_sel_hi:[0,1]
	v_pk_fma_f32 v[24:25], v[56:57], v[126:127], v[24:25] op_sel_hi:[1,0,1] neg_lo:[0,0,1] neg_hi:[0,0,1]
	ds_read2_b32 v[56:57], v71 offset0:128 offset1:160
	v_pk_mul_f32 v[126:127], v[24:25], v[24:25]
	s_waitcnt lgkmcnt(0)
	v_pk_mul_f32 v[10:11], v[116:117], v[56:57] op_sel_hi:[0,1]
	v_pk_fma_f32 v[56:57], v[26:27], v[124:125], v[10:11] op_sel_hi:[1,0,1] neg_lo:[0,0,1] neg_hi:[0,0,1]
	ds_read2_b32 v[10:11], v71 offset0:192 offset1:224
	v_pk_mul_f32 v[26:27], v[56:57], v[56:57]
	v_add_u32_e32 v71, 0x2400, v67
	s_waitcnt lgkmcnt(0)
	v_pk_mul_f32 v[10:11], v[116:117], v[10:11] op_sel_hi:[0,1]
	v_pk_fma_f32 v[10:11], v[58:59], v[124:125], v[10:11] op_sel_hi:[1,0,1] neg_lo:[0,0,1] neg_hi:[0,0,1]
	v_mov_b32_e32 v58, v26
	v_pk_mul_f32 v[42:43], v[10:11], v[10:11]
	v_mov_b32_e32 v59, v128
	v_mov_b32_e32 v128, v27
	v_pk_add_f32 v[26:27], v[58:59], v[128:129]
	v_mov_b32_e32 v58, v42
	v_mov_b32_e32 v59, v126
	v_pk_add_f32 v[26:27], v[26:27], v[58:59]
	v_mov_b32_e32 v126, v43
	v_pk_add_f32 v[26:27], v[26:27], v[126:127]
	ds_bpermute_b32 v43, v142, v27
	ds_bpermute_b32 v42, v142, v26
	v_mov_b32_e32 v58, v44
	v_mov_b32_e32 v59, v60
	v_mov_b32_e32 v60, v45
	s_waitcnt lgkmcnt(0)
	v_pk_add_f32 v[26:27], v[26:27], v[42:43]
	ds_bpermute_b32 v43, v141, v27
	ds_bpermute_b32 v42, v141, v26
	s_waitcnt lgkmcnt(0)
; __device__ __forceinline__ int crow(int r, int hi) { return (r & 3) + 8 * (r >> 2) + 4 * hi; }
; __device__ __forceinline__ void diff_unit(KP Pk, Frame& F, int l, int b, int h, int qrow0, int nkt) {
;     ...
;         for (int r = 0; r < 16; ++r) { float a = 0.f;
; #pragma unroll
;             for (int nb = 0; nb < 4; ++nb) { const float v = O[nb][r] * rlr[r] - lam * ex[crow(r, hi) * 128 + nb * 32 + r32]; O[nb][r] = v; a += v * v; }
;             a += __shfl_xor(a, 1); a += __shfl_xor(a, 2); a += __shfl_xor(a, 4); a += __shfl_xor(a, 8); a += __shfl_xor(a, 16);
;             ssq[r] = rsqrtf(a * (1.f / 128.f) + NORM_EPS) * (1.f - lam_init); }
	v_pk_add_f32 v[26:27], v[26:27], v[42:43]
	ds_bpermute_b32 v43, v140, v27
	ds_bpermute_b32 v42, v140, v26
	s_waitcnt lgkmcnt(0)
	v_pk_add_f32 v[26:27], v[26:27], v[42:43]
	ds_bpermute_b32 v43, v139, v27
	ds_bpermute_b32 v42, v139, v26
	s_waitcnt lgkmcnt(0)
	v_pk_add_f32 v[26:27], v[26:27], v[42:43]
	ds_bpermute_b32 v43, v1, v27
	ds_bpermute_b32 v42, v1, v26
	s_waitcnt lgkmcnt(0)
	v_pk_add_f32 v[26:27], v[26:27], v[42:43]
	s_nop 0
	v_pk_fma_f32 v[26:27], v[26:27], s[8:9], v[122:123] op_sel_hi:[1,0,0]
	v_mov_b32_e32 v43, v28
	v_mul_f32_e32 v42, 0x4b800000, v27
	v_cmp_gt_f32_e64 s[38:39], s66, v27
	v_cmp_gt_f32_e32 vcc, s66, v26
	v_mov_b32_e32 v28, v13
	v_cndmask_b32_e64 v27, v27, v42, s[38:39]
	v_rsq_f32_e32 v27, v27
	s_nop 0
	v_mul_f32_e32 v42, 0x45800000, v27
	v_cndmask_b32_e64 v27, v27, v42, s[38:39]
	v_mul_f32_e32 v126, v69, v27
	v_mul_f32_e32 v27, 0x4b800000, v26
	v_cndmask_b32_e32 v26, v26, v27, vcc
	v_rsq_f32_e32 v26, v26
	v_mov_b32_e32 v42, v12
	v_mul_f32_e32 v27, 0x45800000, v26
	v_cndmask_b32_e32 v26, v26, v27, vcc
	v_mul_f32_e32 v124, v69, v26
	ds_read2_b32 v[26:27], v71 offset1:32
	s_waitcnt lgkmcnt(0)
	v_pk_mul_f32 v[26:27], v[116:117], v[26:27] op_sel_hi:[0,1]
	v_pk_fma_f32 v[42:43], v[42:43], v[120:121], v[26:27] op_sel_hi:[1,0,1] neg_lo:[0,0,1] neg_hi:[0,0,1]
	ds_read2_b32 v[26:27], v71 offset0:64 offset1:96
	v_pk_mul_f32 v[128:129], v[42:43], v[42:43]
	s_waitcnt lgkmcnt(0)
	v_pk_mul_f32 v[26:27], v[116:117], v[26:27] op_sel_hi:[0,1]
	v_pk_fma_f32 v[26:27], v[58:59], v[120:121], v[26:27] op_sel_hi:[1,0,1] neg_lo:[0,0,1] neg_hi:[0,0,1]
	ds_read2_b32 v[58:59], v71 offset0:128 offset1:160
	v_pk_mul_f32 v[130:131], v[26:27], v[26:27]
	s_waitcnt lgkmcnt(0)
	v_pk_mul_f32 v[12:13], v[116:117], v[58:59] op_sel_hi:[0,1]
	v_pk_fma_f32 v[58:59], v[28:29], v[118:119], v[12:13] op_sel_hi:[1,0,1] neg_lo:[0,0,1] neg_hi:[0,0,1]
	ds_read2_b32 v[12:13], v71 offset0:192 offset1:224
	v_pk_mul_f32 v[28:29], v[58:59], v[58:59]
	v_add_u32_e32 v71, 0x3000, v67
	v_add_u32_e32 v67, 0x3400, v67
	s_waitcnt lgkmcnt(0)
	v_pk_mul_f32 v[12:13], v[116:117], v[12:13] op_sel_hi:[0,1]
	v_pk_fma_f32 v[12:13], v[60:61], v[118:119], v[12:13] op_sel_hi:[1,0,1] neg_lo:[0,0,1] neg_hi:[0,0,1]
	v_mov_b32_e32 v60, v28
	v_pk_mul_f32 v[44:45], v[12:13], v[12:13]
	v_mov_b32_e32 v61, v128
	v_mov_b32_e32 v128, v29
	v_pk_add_f32 v[28:29], v[60:61], v[128:129]
	v_mov_b32_e32 v60, v44
	v_mov_b32_e32 v61, v130
	v_pk_add_f32 v[28:29], v[28:29], v[60:61]
	v_mov_b32_e32 v130, v45
	v_pk_add_f32 v[28:29], v[28:29], v[130:131]
	ds_bpermute_b32 v45, v142, v29
	ds_bpermute_b32 v44, v142, v28
	v_mov_b32_e32 v60, v46
	v_mov_b32_e32 v61, v62
	v_mov_b32_e32 v62, v47
	s_waitcnt lgkmcnt(0)
	v_pk_add_f32 v[28:29], v[28:29], v[44:45]
	ds_bpermute_b32 v45, v141, v29
	ds_bpermute_b32 v44, v141, v28
	s_waitcnt lgkmcnt(0)
	v_pk_add_f32 v[28:29], v[28:29], v[44:45]
	ds_bpermute_b32 v45, v140, v29
	ds_bpermute_b32 v44, v140, v28
	s_waitcnt lgkmcnt(0)
	v_pk_add_f32 v[28:29], v[28:29], v[44:45]
	ds_bpermute_b32 v45, v139, v29
	ds_bpermute_b32 v44, v139, v28
	s_waitcnt lgkmcnt(0)
	v_pk_add_f32 v[28:29], v[28:29], v[44:45]
	ds_bpermute_b32 v45, v1, v29
	ds_bpermute_b32 v44, v1, v28
	s_waitcnt lgkmcnt(0)
	v_pk_add_f32 v[28:29], v[28:29], v[44:45]
	s_nop 0
	v_pk_fma_f32 v[28:29], v[28:29], s[8:9], v[122:123] op_sel_hi:[1,0,0]
	v_mov_b32_e32 v45, v30
	v_mul_f32_e32 v44, 0x4b800000, v29
	v_cmp_gt_f32_e64 s[38:39], s66, v29
	v_cmp_gt_f32_e32 vcc, s66, v28
	v_mov_b32_e32 v30, v15
	v_cndmask_b32_e64 v29, v29, v44, s[38:39]
	v_rsq_f32_e32 v29, v29
	s_nop 0
	v_mul_f32_e32 v44, 0x45800000, v29
	v_cndmask_b32_e64 v29, v29, v44, s[38:39]
	v_mul_f32_e32 v120, v69, v29
	v_mul_f32_e32 v29, 0x4b800000, v28
	v_cndmask_b32_e32 v28, v28, v29, vcc
	v_rsq_f32_e32 v28, v28
	v_mov_b32_e32 v44, v14
	v_mul_f32_e32 v29, 0x45800000, v28
	v_cndmask_b32_e32 v28, v28, v29, vcc
	v_mul_f32_e32 v118, v69, v28
	ds_read2_b32 v[28:29], v71 offset1:32
	s_waitcnt lgkmcnt(0)
	v_pk_mul_f32 v[28:29], v[116:117], v[28:29] op_sel_hi:[0,1]
	v_pk_fma_f32 v[44:45], v[44:45], v[114:115], v[28:29] op_sel_hi:[1,0,1] neg_lo:[0,0,1] neg_hi:[0,0,1]
	ds_read2_b32 v[28:29], v71 offset0:64 offset1:96
	v_pk_mul_f32 v[128:129], v[44:45], v[44:45]
	s_waitcnt lgkmcnt(0)
	v_pk_mul_f32 v[28:29], v[116:117], v[28:29] op_sel_hi:[0,1]
	v_pk_fma_f32 v[28:29], v[60:61], v[114:115], v[28:29] op_sel_hi:[1,0,1] neg_lo:[0,0,1] neg_hi:[0,0,1]
	ds_read2_b32 v[60:61], v71 offset0:128 offset1:160
	v_pk_mul_f32 v[130:131], v[28:29], v[28:29]
	s_waitcnt lgkmcnt(0)
	v_pk_mul_f32 v[14:15], v[116:117], v[60:61] op_sel_hi:[0,1]
	v_pk_fma_f32 v[60:61], v[30:31], v[112:113], v[14:15] op_sel_hi:[1,0,1] neg_lo:[0,0,1] neg_hi:[0,0,1]
	ds_read2_b32 v[14:15], v71 offset0:192 offset1:224
	v_pk_mul_f32 v[30:31], v[60:61], v[60:61]
	v_mov_b32_e32 v71, v0
	s_waitcnt lgkmcnt(0)
	v_pk_mul_f32 v[14:15], v[116:117], v[14:15] op_sel_hi:[0,1]
	v_pk_fma_f32 v[14:15], v[62:63], v[112:113], v[14:15] op_sel_hi:[1,0,1] neg_lo:[0,0,1] neg_hi:[0,0,1]
	v_mov_b32_e32 v62, v30
	v_pk_mul_f32 v[46:47], v[14:15], v[14:15]
	v_mov_b32_e32 v63, v128
	v_mov_b32_e32 v128, v31
	v_pk_add_f32 v[30:31], v[62:63], v[128:129]
	v_mov_b32_e32 v62, v46
	v_mov_b32_e32 v63, v130
	v_pk_add_f32 v[30:31], v[30:31], v[62:63]
	v_mov_b32_e32 v130, v47
	v_pk_add_f32 v[30:31], v[30:31], v[130:131]
	ds_bpermute_b32 v47, v142, v31
	ds_bpermute_b32 v46, v142, v30
	ds_read2_b32 v[130:131], v67 offset0:128 offset1:160
	v_mov_b32_e32 v128, v48
	v_mov_b32_e32 v129, v64
	v_mov_b32_e32 v64, v49
	s_waitcnt lgkmcnt(1)
	v_pk_add_f32 v[30:31], v[30:31], v[46:47]
	ds_bpermute_b32 v47, v141, v31
	ds_bpermute_b32 v46, v141, v30
	s_waitcnt lgkmcnt(0)
; __device__ __forceinline__ int crow(int r, int hi) { return (r & 3) + 8 * (r >> 2) + 4 * hi; }
; __device__ __forceinline__ void diff_unit(KP Pk, Frame& F, int l, int b, int h, int qrow0, int nkt) {
;     ...
;         for (int r = 0; r < 16; ++r) { float a = 0.f;
; #pragma unroll
;             for (int nb = 0; nb < 4; ++nb) { const float v = O[nb][r] * rlr[r] - lam * ex[crow(r, hi) * 128 + nb * 32 + r32]; O[nb][r] = v; a += v * v; }
;             a += __shfl_xor(a, 1); a += __shfl_xor(a, 2); a += __shfl_xor(a, 4); a += __shfl_xor(a, 8); a += __shfl_xor(a, 16);
;             ssq[r] = rsqrtf(a * (1.f / 128.f) + NORM_EPS) * (1.f - lam_init); }
;         unsigned char* mix = ws + WS_H + ((size_t)(qrow0 + 32 * rb) * D + 1536 + h * 128) * MIXB;
; #pragma unroll
;         for (int nb = 0; nb < 4; ++nb) { const float w = Pk->in[I_DSUB][l * 128 + nb * 32 + r32];
	v_pk_add_f32 v[30:31], v[30:31], v[46:47]
	ds_bpermute_b32 v47, v140, v31
	ds_bpermute_b32 v46, v140, v30
	s_waitcnt lgkmcnt(0)
	v_pk_add_f32 v[30:31], v[30:31], v[46:47]
	ds_bpermute_b32 v47, v139, v31
	ds_bpermute_b32 v46, v139, v30
	s_waitcnt lgkmcnt(0)
	v_pk_add_f32 v[30:31], v[30:31], v[46:47]
	ds_bpermute_b32 v47, v1, v31
	ds_bpermute_b32 v46, v1, v30
	s_waitcnt lgkmcnt(0)
	v_pk_add_f32 v[30:31], v[30:31], v[46:47]
	s_nop 0
	v_pk_fma_f32 v[30:31], v[30:31], s[8:9], v[122:123] op_sel_hi:[1,0,0]
	v_mov_b32_e32 v47, v32
	v_mul_f32_e32 v46, 0x4b800000, v31
	v_cmp_gt_f32_e64 s[38:39], s66, v31
	v_cmp_gt_f32_e32 vcc, s66, v30
	v_mov_b32_e32 v32, v17
	v_cndmask_b32_e64 v31, v31, v46, s[38:39]
	v_rsq_f32_e32 v31, v31
	s_nop 0
	v_mul_f32_e32 v46, 0x45800000, v31
	v_cndmask_b32_e64 v31, v31, v46, s[38:39]
	v_mul_f32_e32 v114, v69, v31
	v_mul_f32_e32 v31, 0x4b800000, v30
	v_cndmask_b32_e32 v30, v30, v31, vcc
	v_rsq_f32_e32 v30, v30
	v_mov_b32_e32 v46, v16
	v_pk_mul_f32 v[16:17], v[116:117], v[130:131] op_sel_hi:[0,1]
	v_pk_fma_f32 v[32:33], v[32:33], v[108:109], v[16:17] op_sel_hi:[1,0,1] neg_lo:[0,0,1] neg_hi:[0,0,1]
	v_mul_f32_e32 v31, 0x45800000, v30
	v_cndmask_b32_e32 v30, v30, v31, vcc
	v_mul_f32_e32 v112, v69, v30
	ds_read2_b32 v[30:31], v67 offset1:32
	ds_read2_b32 v[16:17], v67 offset0:192 offset1:224
	v_pk_mul_f32 v[130:131], v[32:33], v[32:33]
	s_waitcnt lgkmcnt(1)
	v_pk_mul_f32 v[30:31], v[116:117], v[30:31] op_sel_hi:[0,1]
	v_pk_fma_f32 v[46:47], v[46:47], v[110:111], v[30:31] op_sel_hi:[1,0,1] neg_lo:[0,0,1] neg_hi:[0,0,1]
	ds_read2_b32 v[30:31], v67 offset0:64 offset1:96
	s_waitcnt lgkmcnt(1)
	v_pk_mul_f32 v[16:17], v[116:117], v[16:17] op_sel_hi:[0,1]
	v_pk_mul_f32 v[62:63], v[46:47], v[46:47]
	v_pk_fma_f32 v[16:17], v[64:65], v[108:109], v[16:17] op_sel_hi:[1,0,1] neg_lo:[0,0,1] neg_hi:[0,0,1]
	v_mov_b32_e32 v64, v130
	s_waitcnt lgkmcnt(0)
	v_pk_mul_f32 v[30:31], v[116:117], v[30:31] op_sel_hi:[0,1]
	v_pk_fma_f32 v[30:31], v[128:129], v[110:111], v[30:31] op_sel_hi:[1,0,1] neg_lo:[0,0,1] neg_hi:[0,0,1]
	v_pk_mul_f32 v[48:49], v[16:17], v[16:17]
	v_pk_mul_f32 v[128:129], v[30:31], v[30:31]
	v_mov_b32_e32 v65, v62
	v_mov_b32_e32 v62, v131
	v_pk_add_f32 v[62:63], v[64:65], v[62:63]
	v_mov_b32_e32 v64, v48
	v_mov_b32_e32 v65, v128
	v_pk_add_f32 v[62:63], v[62:63], v[64:65]
	v_mov_b32_e32 v128, v49
	v_pk_add_f32 v[48:49], v[62:63], v[128:129]
	ds_bpermute_b32 v63, v142, v49
	ds_bpermute_b32 v62, v142, v48
	v_mov_b32_e32 v65, v0
	s_waitcnt lgkmcnt(0)
	v_pk_add_f32 v[48:49], v[48:49], v[62:63]
	ds_bpermute_b32 v63, v141, v49
	ds_bpermute_b32 v62, v141, v48
	s_waitcnt lgkmcnt(0)
	v_pk_add_f32 v[48:49], v[48:49], v[62:63]
	ds_bpermute_b32 v63, v140, v49
	ds_bpermute_b32 v62, v140, v48
	s_waitcnt lgkmcnt(0)
	v_pk_add_f32 v[48:49], v[48:49], v[62:63]
	ds_bpermute_b32 v63, v139, v49
	ds_bpermute_b32 v62, v139, v48
	s_waitcnt lgkmcnt(0)
	v_pk_add_f32 v[48:49], v[48:49], v[62:63]
	ds_bpermute_b32 v63, v1, v49
	ds_bpermute_b32 v62, v1, v48
	s_waitcnt lgkmcnt(0)
	v_pk_add_f32 v[48:49], v[48:49], v[62:63]
	s_nop 0
	v_pk_fma_f32 v[48:49], v[48:49], s[8:9], v[122:123] op_sel_hi:[1,0,0]
	v_mul_f32_e32 v62, v100, v111
	v_mul_f32_e32 v1, 0x4b800000, v49
	v_cmp_gt_f32_e64 s[38:39], s66, v49
	v_cmp_gt_f32_e32 vcc, s66, v48
	s_lshl_b64 s[8:9], s[40:41], 11
	v_cndmask_b32_e64 v1, v49, v1, s[38:39]
	v_rsq_f32_e32 v1, v1
	s_add_u32 s5, s5, s8
	v_readlane_b32 s8, v254, 62
	s_addc_u32 s9, s8, s9
	v_mul_f32_e32 v49, 0x45800000, v1
	v_cndmask_b32_e64 v1, v1, v49, s[38:39]
	v_mul_f32_e32 v108, v69, v1
	v_mul_f32_e32 v1, 0x4b800000, v48
	v_cndmask_b32_e32 v1, v48, v1, vcc
	v_rsq_f32_e32 v1, v1
	s_add_u32 s8, s5, s18
	s_addc_u32 s9, s9, 0
	v_mul_f32_e32 v48, 0x45800000, v1
	v_cndmask_b32_e32 v1, v1, v48, vcc
	v_lshl_or_b32 v48, s4, 7, v104
	v_ashrrev_i32_e32 v49, 31, v48
	v_lshl_add_u64 v[48:49], v[48:49], 2, v[106:107]
	global_load_dword v67, v[48:49], off
	global_load_dword v236, v[48:49], off offset:128
	global_load_dword v250, v[48:49], off offset:256
	global_load_dword v251, v[48:49], off offset:384
	v_mul_f32_e32 v1, v69, v1
	v_lshl_add_u64 v[104:105], s[8:9], 0, v[104:105]
	v_lshl_add_u64 v[92:93], v[104:105], 0, v[92:93]
	v_lshl_add_u64 v[90:91], v[104:105], 0, v[90:91]
	v_lshl_add_u64 v[88:89], v[104:105], 0, v[88:89]
	v_lshl_add_u64 v[86:87], v[104:105], 0, v[86:87]
	v_lshl_add_u64 v[84:85], v[104:105], 0, v[84:85]
	v_lshl_add_u64 v[82:83], v[104:105], 0, v[82:83]
	v_lshl_add_u64 v[80:81], v[104:105], 0, v[80:81]
	v_lshl_add_u64 v[78:79], v[104:105], 0, v[78:79]
	v_lshl_add_u64 v[74:75], v[104:105], 0, v[74:75]
	v_lshl_add_u64 v[72:73], v[104:105], 0, v[72:73]
	v_lshl_add_u64 v[94:95], v[104:105], 0, v[94:95]
	s_waitcnt vmcnt(0)
; __device__ __forceinline__ unsigned f2bf(float f) { unsigned u = __builtin_bit_cast(unsigned, f); return (u + 0x7fffu + ((u >> 16) & 1u)) >> 16; }
; __device__ __forceinline__ int crow(int r, int hi) { return (r & 3) + 8 * (r >> 2) + 4 * hi; }
; __device__ __forceinline__ unsigned char f8_1(float a) { a = fminf(fmaxf(a, -448.f), 448.f); return (unsigned char)(__builtin_amdgcn_cvt_pk_fp8_f32(a, a, 0, false) & 0xff); }
; __device__ __forceinline__ void diff_unit(KP Pk, Frame& F, int l, int b, int h, int qrow0, int nkt) {
;     ...
;         unsigned char* mix = ws + WS_H + ((size_t)(qrow0 + 32 * rb) * D + 1536 + h * 128) * MIXB;
; #pragma unroll
;         for (int nb = 0; nb < 4; ++nb) { const float w = Pk->in[I_DSUB][l * 128 + nb * 32 + r32];
; #pragma unroll
;             for (int r = 0; r < 16; ++r) { const float y = O[nb][r] * ssq[r] * w; const size_t e = (size_t)crow(r, hi) * D + nb * 32 + r32; if (WOUT_F8) mix[e] = f8_1(y); else ((bf16_t*)mix)[e] = (bf16_t)f2bf(y); } }
	v_mul_f32_e32 v64, v62, v67
	v_med3_f32 v64, v64, s83, v238
	v_cvt_pk_fp8_f32 v65, v64, v64
	v_mul_f32_e32 v64, v102, v109
	v_mul_f32_e32 v69, v64, v67
	v_med3_f32 v69, v69, s83, v238
	v_mul_f32_e32 v34, v34, v67
	v_cvt_pk_fp8_f32 v71, v69, v69
	v_med3_f32 v34, v34, s83, v238
	v_mov_b32_e32 v69, v0
	v_mul_f32_e32 v20, v20, v67
	v_cvt_pk_fp8_f32 v69, v34, v34
	v_med3_f32 v20, v20, s83, v238
	v_mov_b32_e32 v34, v0
	v_cvt_pk_fp8_f32 v34, v20, v20
	v_mul_f32_e32 v20, v36, v119
	v_mul_f32_e32 v20, v20, v67
	v_med3_f32 v20, v20, s83, v238
	global_store_byte v[92:93], v34, off
	v_mov_b32_e32 v34, v0
	v_cvt_pk_fp8_f32 v34, v20, v20
	v_mul_f32_e32 v20, v52, v117
	v_mul_f32_e32 v20, v20, v67
	v_med3_f32 v20, v20, s83, v238
	global_store_byte v[90:91], v34, off
	v_mov_b32_e32 v34, v0
	v_cvt_pk_fp8_f32 v34, v20, v20
	v_mul_f32_e32 v20, v38, v125
	v_mul_f32_e32 v20, v20, v67
	v_med3_f32 v20, v20, s83, v238
	global_store_byte v[88:89], v34, off
	v_mov_b32_e32 v34, v0
	v_cvt_pk_fp8_f32 v34, v20, v20
	v_mul_f32_e32 v20, v54, v121
	v_mul_f32_e32 v20, v20, v67
	v_med3_f32 v20, v20, s83, v238
	global_store_byte v[86:87], v34, off
	v_mov_b32_e32 v34, v0
	v_cvt_pk_fp8_f32 v34, v20, v20
	v_mul_f32_e32 v20, v40, v126
	v_mul_f32_e32 v20, v20, v67
	v_med3_f32 v20, v20, s83, v238
	global_store_byte v[84:85], v34, off
	v_mov_b32_e32 v34, v0
	v_cvt_pk_fp8_f32 v34, v20, v20
	v_mul_f32_e32 v20, v56, v124
	v_mul_f32_e32 v20, v20, v67
	v_med3_f32 v20, v20, s83, v238
	global_store_byte v[82:83], v34, off
	v_mov_b32_e32 v34, v0
	v_cvt_pk_fp8_f32 v34, v20, v20
	v_mul_f32_e32 v20, v42, v120
	v_mul_f32_e32 v20, v20, v67
	v_med3_f32 v20, v20, s83, v238
	global_store_byte v[80:81], v34, off
	v_mov_b32_e32 v34, v0
	v_cvt_pk_fp8_f32 v34, v20, v20
	v_mul_f32_e32 v20, v58, v118
	v_mul_f32_e32 v20, v20, v67
	v_med3_f32 v20, v20, s83, v238
	global_store_byte v[78:79], v34, off
	v_mov_b32_e32 v34, v0
	v_cvt_pk_fp8_f32 v34, v20, v20
	v_mul_f32_e32 v20, v44, v114
	v_mul_f32_e32 v20, v20, v67
	v_med3_f32 v20, v20, s83, v238
	global_store_byte v[74:75], v34, off
	v_mov_b32_e32 v34, v0
	v_cvt_pk_fp8_f32 v34, v20, v20
	v_lshlrev_b64 v[62:63], 11, v[98:99]
	v_mul_f32_e32 v20, v60, v112
	v_lshl_add_u64 v[62:63], v[104:105], 0, v[62:63]
	v_mul_f32_e32 v20, v20, v67
	global_store_byte v[62:63], v65, off
	v_lshlrev_b64 v[64:65], 11, v[96:97]
	global_store_byte v[72:73], v34, off
	v_med3_f32 v20, v20, s83, v238
	v_mov_b32_e32 v34, v0
	v_lshl_add_u64 v[64:65], v[104:105], 0, v[64:65]
	v_cvt_pk_fp8_f32 v34, v20, v20
	global_store_byte v[64:65], v71, off
	v_ashrrev_i32_e32 v71, 31, v70
	v_lshlrev_b64 v[70:71], 11, v[70:71]
	v_mul_f32_e32 v20, v46, v108
	v_lshl_add_u64 v[70:71], v[104:105], 0, v[70:71]
	v_mul_f32_e32 v20, v67, v20
	global_store_byte v[70:71], v34, off
	v_med3_f32 v20, v20, s83, v238
	v_mov_b32_e32 v34, v0
	v_cvt_pk_fp8_f32 v34, v20, v20
	v_mul_f32_e32 v20, v32, v1
	v_mul_f32_e32 v20, v67, v20
	v_med3_f32 v20, v20, s83, v238
	v_mov_b32_e32 v32, v0
	v_cvt_pk_fp8_f32 v32, v20, v20
	global_store_byte v[94:95], v69, off
	v_ashrrev_i32_e32 v69, 31, v68
	v_ashrrev_i32_e32 v67, 31, v66
	v_lshlrev_b64 v[68:69], 11, v[68:69]
	v_lshlrev_b64 v[66:67], 11, v[66:67]
	v_lshl_add_u64 v[68:69], v[104:105], 0, v[68:69]
	v_lshl_add_u64 v[66:67], v[104:105], 0, v[66:67]
	global_store_byte v[68:69], v34, off
	global_store_byte v[66:67], v32, off
	v_mov_b32_e32 v20, v236
	v_mul_f32_e32 v32, v101, v111
	v_mov_b32_e32 v34, v0
	v_mul_f32_e32 v32, v32, v20
	v_med3_f32 v32, v32, s83, v238
	v_cvt_pk_fp8_f32 v34, v32, v32
	v_mul_f32_e32 v32, v103, v109
	v_mul_f32_e32 v32, v32, v20
	v_med3_f32 v32, v32, s83, v238
	global_store_byte v[62:63], v34, off offset:32
	v_mov_b32_e32 v34, v0
	v_cvt_pk_fp8_f32 v34, v32, v32
	v_mul_f32_e32 v32, v35, v115
	v_mul_f32_e32 v32, v32, v20
	v_med3_f32 v32, v32, s83, v238
	global_store_byte v[64:65], v34, off offset:32
	v_mov_b32_e32 v34, v0
	v_mul_f32_e32 v21, v21, v20
	v_cvt_pk_fp8_f32 v34, v32, v32
	v_med3_f32 v21, v21, s83, v238
	v_mov_b32_e32 v32, v0
	v_cvt_pk_fp8_f32 v32, v21, v21
	v_mul_f32_e32 v21, v37, v119
	v_mul_f32_e32 v21, v21, v20
	v_med3_f32 v21, v21, s83, v238
	global_store_byte v[92:93], v32, off offset:32
	v_mov_b32_e32 v32, v0
	v_cvt_pk_fp8_f32 v32, v21, v21
	v_mul_f32_e32 v21, v53, v117
	v_mul_f32_e32 v21, v21, v20
	v_med3_f32 v21, v21, s83, v238
	global_store_byte v[90:91], v32, off offset:32
	v_mov_b32_e32 v32, v0
	v_cvt_pk_fp8_f32 v32, v21, v21
	v_mul_f32_e32 v21, v39, v125
	v_mul_f32_e32 v21, v21, v20
	v_med3_f32 v21, v21, s83, v238
	global_store_byte v[88:89], v32, off offset:32
	v_mov_b32_e32 v32, v0
	v_cvt_pk_fp8_f32 v32, v21, v21
	v_mul_f32_e32 v21, v55, v121
	v_mul_f32_e32 v21, v21, v20
	v_med3_f32 v21, v21, s83, v238
	global_store_byte v[86:87], v32, off offset:32
	v_mov_b32_e32 v32, v0
	v_cvt_pk_fp8_f32 v32, v21, v21
	v_mul_f32_e32 v21, v41, v126
	v_mul_f32_e32 v21, v21, v20
	v_med3_f32 v21, v21, s83, v238
	global_store_byte v[84:85], v32, off offset:32
	v_mov_b32_e32 v32, v0
	v_cvt_pk_fp8_f32 v32, v21, v21
	v_mul_f32_e32 v21, v57, v124
	v_mul_f32_e32 v21, v21, v20
	v_med3_f32 v21, v21, s83, v238
	global_store_byte v[82:83], v32, off offset:32
	v_mov_b32_e32 v32, v0
	v_cvt_pk_fp8_f32 v32, v21, v21
	v_mul_f32_e32 v21, v43, v120
	v_mul_f32_e32 v21, v21, v20
	v_med3_f32 v21, v21, s83, v238
	global_store_byte v[80:81], v32, off offset:32
	v_mov_b32_e32 v32, v0
	v_cvt_pk_fp8_f32 v32, v21, v21
	v_mul_f32_e32 v21, v59, v118
	v_mul_f32_e32 v21, v21, v20
	v_med3_f32 v21, v21, s83, v238
	global_store_byte v[78:79], v32, off offset:32
	v_mov_b32_e32 v32, v0
	v_cvt_pk_fp8_f32 v32, v21, v21
	v_mul_f32_e32 v21, v45, v114
	v_mul_f32_e32 v21, v21, v20
; __device__ __forceinline__ unsigned f2bf(float f) { unsigned u = __builtin_bit_cast(unsigned, f); return (u + 0x7fffu + ((u >> 16) & 1u)) >> 16; }
; __device__ __forceinline__ unsigned char f8_1(float a) { a = fminf(fmaxf(a, -448.f), 448.f); return (unsigned char)(__builtin_amdgcn_cvt_pk_fp8_f32(a, a, 0, false) & 0xff); }
; __device__ __forceinline__ int crow(int r, int hi) { return (r & 3) + 8 * (r >> 2) + 4 * hi; }
; __device__ __forceinline__ void diff_unit(KP Pk, Frame& F, int l, int b, int h, int qrow0, int nkt) {
;     ...
;         for (int nb = 0; nb < 4; ++nb) { const float w = Pk->in[I_DSUB][l * 128 + nb * 32 + r32];
; #pragma unroll
;             for (int r = 0; r < 16; ++r) { const float y = O[nb][r] * ssq[r] * w; const size_t e = (size_t)crow(r, hi) * D + nb * 32 + r32; if (WOUT_F8) mix[e] = f8_1(y); else ((bf16_t*)mix)[e] = (bf16_t)f2bf(y); } }
	v_med3_f32 v21, v21, s83, v238
	global_store_byte v[74:75], v32, off offset:32
	v_mov_b32_e32 v32, v0
	v_cvt_pk_fp8_f32 v32, v21, v21
	v_mul_f32_e32 v21, v61, v112
	v_mul_f32_e32 v21, v21, v20
	v_med3_f32 v21, v21, s83, v238
	global_store_byte v[72:73], v32, off offset:32
	v_mov_b32_e32 v32, v0
	v_cvt_pk_fp8_f32 v32, v21, v21
	v_mul_f32_e32 v21, v47, v108
	v_mul_f32_e32 v21, v21, v20
	v_med3_f32 v21, v21, s83, v238
	global_store_byte v[70:71], v32, off offset:32
	v_mov_b32_e32 v32, v0
	v_cvt_pk_fp8_f32 v32, v21, v21
	v_mul_f32_e32 v21, v33, v1
	v_mul_f32_e32 v20, v21, v20
	v_med3_f32 v20, v20, s83, v238
	v_mov_b32_e32 v21, v0
	v_cvt_pk_fp8_f32 v21, v20, v20
	global_store_byte v[94:95], v34, off offset:32
	global_store_byte v[68:69], v32, off offset:32
	v_mov_b32_e32 v32, v0
	global_store_byte v[66:67], v21, off offset:32
	v_mov_b32_e32 v20, v250
	v_mul_f32_e32 v21, v77, v111
	v_mul_f32_e32 v21, v21, v20
	v_med3_f32 v21, v21, s83, v238
	v_mul_f32_e32 v2, v2, v20
	v_cvt_pk_fp8_f32 v32, v21, v21
	v_med3_f32 v2, v2, s83, v238
	v_mov_b32_e32 v21, v0
	v_cvt_pk_fp8_f32 v21, v2, v2
	v_mul_f32_e32 v2, v18, v115
	v_mul_f32_e32 v2, v2, v20
	v_med3_f32 v2, v2, s83, v238
	v_mov_b32_e32 v18, v0
	v_cvt_pk_fp8_f32 v18, v2, v2
	v_mul_f32_e32 v2, v4, v113
	v_mul_f32_e32 v2, v2, v20
	v_med3_f32 v2, v2, s83, v238
	v_mov_b32_e32 v4, v0
	v_cvt_pk_fp8_f32 v4, v2, v2
	v_mul_f32_e32 v2, v50, v119
	v_mul_f32_e32 v2, v2, v20
	v_med3_f32 v2, v2, s83, v238
	global_store_byte v[92:93], v4, off offset:64
	v_mov_b32_e32 v4, v0
	v_cvt_pk_fp8_f32 v4, v2, v2
	v_mul_f32_e32 v2, v6, v117
	v_mul_f32_e32 v2, v2, v20
	v_med3_f32 v2, v2, s83, v238
	global_store_byte v[90:91], v4, off offset:64
	v_mov_b32_e32 v4, v0
	v_cvt_pk_fp8_f32 v4, v2, v2
	v_mul_f32_e32 v2, v22, v125
	v_mul_f32_e32 v2, v2, v20
	v_med3_f32 v2, v2, s83, v238
	global_store_byte v[88:89], v4, off offset:64
	v_mov_b32_e32 v4, v0
	v_cvt_pk_fp8_f32 v4, v2, v2
	v_mul_f32_e32 v2, v8, v121
	v_mul_f32_e32 v2, v2, v20
	v_med3_f32 v2, v2, s83, v238
	global_store_byte v[86:87], v4, off offset:64
	v_mov_b32_e32 v4, v0
	v_cvt_pk_fp8_f32 v4, v2, v2
	v_mul_f32_e32 v2, v24, v126
	v_mul_f32_e32 v2, v2, v20
	v_med3_f32 v2, v2, s83, v238
	global_store_byte v[84:85], v4, off offset:64
	v_mov_b32_e32 v4, v0
	v_cvt_pk_fp8_f32 v4, v2, v2
	v_mul_f32_e32 v2, v10, v124
	v_mul_f32_e32 v2, v2, v20
	v_med3_f32 v2, v2, s83, v238
	global_store_byte v[82:83], v4, off offset:64
	v_mov_b32_e32 v4, v0
	v_cvt_pk_fp8_f32 v4, v2, v2
	v_mul_f32_e32 v2, v26, v120
	v_mul_f32_e32 v2, v2, v20
	v_med3_f32 v2, v2, s83, v238
	global_store_byte v[80:81], v4, off offset:64
	v_mov_b32_e32 v4, v0
	v_cvt_pk_fp8_f32 v4, v2, v2
	v_mul_f32_e32 v2, v12, v118
	v_mul_f32_e32 v2, v2, v20
	v_med3_f32 v2, v2, s83, v238
	global_store_byte v[78:79], v4, off offset:64
	v_mov_b32_e32 v4, v0
	v_cvt_pk_fp8_f32 v4, v2, v2
	v_mul_f32_e32 v2, v28, v114
	v_mul_f32_e32 v2, v2, v20
	v_med3_f32 v2, v2, s83, v238
	global_store_byte v[74:75], v4, off offset:64
	v_mov_b32_e32 v4, v0
	v_cvt_pk_fp8_f32 v4, v2, v2
	v_mul_f32_e32 v2, v14, v112
	v_mul_f32_e32 v2, v2, v20
	v_med3_f32 v2, v2, s83, v238
	global_store_byte v[72:73], v4, off offset:64
	v_mov_b32_e32 v4, v0
	v_cvt_pk_fp8_f32 v4, v2, v2
	v_mul_f32_e32 v2, v30, v108
	v_mul_f32_e32 v2, v2, v20
	v_med3_f32 v2, v2, s83, v238
	global_store_byte v[70:71], v4, off offset:64
	v_mov_b32_e32 v4, v0
	v_cvt_pk_fp8_f32 v4, v2, v2
	v_mul_f32_e32 v2, v16, v1
	v_mul_f32_e32 v2, v2, v20
	v_med3_f32 v2, v2, s83, v238
	global_store_byte v[68:69], v4, off offset:64
	v_mov_b32_e32 v4, v0
	v_cvt_pk_fp8_f32 v4, v2, v2
	global_store_byte v[62:63], v32, off offset:64
	global_store_byte v[64:65], v21, off offset:64
	global_store_byte v[94:95], v18, off offset:64
	global_store_byte v[66:67], v4, off offset:64
	v_mov_b32_e32 v2, v251
	v_mul_f32_e32 v4, v76, v111
	v_mov_b32_e32 v6, v0
	v_mul_f32_e32 v1, v17, v1
	v_mul_f32_e32 v4, v4, v2
	v_med3_f32 v4, v4, s83, v238
	v_mul_f32_e32 v3, v3, v2
	v_cvt_pk_fp8_f32 v6, v4, v4
	v_med3_f32 v3, v3, s83, v238
	v_mov_b32_e32 v4, v0
	v_cvt_pk_fp8_f32 v4, v3, v3
	v_mul_f32_e32 v3, v19, v115
	v_mul_f32_e32 v3, v3, v2
	v_med3_f32 v3, v3, s83, v238
	global_store_byte v[64:65], v4, off offset:96
	v_mov_b32_e32 v4, v0
	v_cvt_pk_fp8_f32 v4, v3, v3
	v_mul_f32_e32 v3, v5, v113
	v_mul_f32_e32 v3, v3, v2
	v_med3_f32 v3, v3, s83, v238
	global_store_byte v[94:95], v4, off offset:96
	v_mov_b32_e32 v4, v0
	v_cvt_pk_fp8_f32 v4, v3, v3
	v_mul_f32_e32 v3, v51, v119
	v_mul_f32_e32 v3, v3, v2
	v_med3_f32 v3, v3, s83, v238
	global_store_byte v[92:93], v4, off offset:96
	v_mov_b32_e32 v4, v0
	v_cvt_pk_fp8_f32 v4, v3, v3
	v_mul_f32_e32 v3, v7, v117
	v_mul_f32_e32 v3, v3, v2
	v_med3_f32 v3, v3, s83, v238
	global_store_byte v[90:91], v4, off offset:96
	v_mov_b32_e32 v4, v0
	v_cvt_pk_fp8_f32 v4, v3, v3
	v_mul_f32_e32 v3, v23, v125
	v_mul_f32_e32 v3, v3, v2
	v_med3_f32 v3, v3, s83, v238
	global_store_byte v[88:89], v4, off offset:96
	v_mov_b32_e32 v4, v0
	v_cvt_pk_fp8_f32 v4, v3, v3
	v_mul_f32_e32 v3, v9, v121
	v_mul_f32_e32 v3, v3, v2
	v_med3_f32 v3, v3, s83, v238
	global_store_byte v[86:87], v4, off offset:96
	v_mov_b32_e32 v4, v0
	v_cvt_pk_fp8_f32 v4, v3, v3
	v_mul_f32_e32 v3, v25, v126
	v_mul_f32_e32 v3, v3, v2
	v_med3_f32 v3, v3, s83, v238
	global_store_byte v[84:85], v4, off offset:96
	v_mov_b32_e32 v4, v0
	v_cvt_pk_fp8_f32 v4, v3, v3
	v_mul_f32_e32 v3, v11, v124
	v_mul_f32_e32 v3, v3, v2
	v_med3_f32 v3, v3, s83, v238
	global_store_byte v[82:83], v4, off offset:96
	v_mov_b32_e32 v4, v0
	v_cvt_pk_fp8_f32 v4, v3, v3
	v_mul_f32_e32 v3, v27, v120
	v_mul_f32_e32 v3, v3, v2
	v_med3_f32 v3, v3, s83, v238
	global_store_byte v[80:81], v4, off offset:96
	v_mov_b32_e32 v4, v0
	v_cvt_pk_fp8_f32 v4, v3, v3
	v_mul_f32_e32 v3, v13, v118
	v_mul_f32_e32 v3, v3, v2
	v_med3_f32 v3, v3, s83, v238
	global_store_byte v[78:79], v4, off offset:96
	v_mov_b32_e32 v4, v0
	v_cvt_pk_fp8_f32 v4, v3, v3
	v_mul_f32_e32 v3, v29, v114
	v_mul_f32_e32 v3, v3, v2
	v_med3_f32 v3, v3, s83, v238
	global_store_byte v[74:75], v4, off offset:96
	v_mov_b32_e32 v4, v0
	v_cvt_pk_fp8_f32 v4, v3, v3
	v_mul_f32_e32 v3, v15, v112
	v_mul_f32_e32 v3, v3, v2
	v_med3_f32 v3, v3, s83, v238
	global_store_byte v[72:73], v4, off offset:96
	v_mov_b32_e32 v4, v0
	v_cvt_pk_fp8_f32 v4, v3, v3
	v_mul_f32_e32 v3, v31, v108
	v_mul_f32_e32 v3, v3, v2
	v_mul_f32_e32 v1, v1, v2
	global_store_byte v[70:71], v4, off offset:96
	v_med3_f32 v3, v3, s83, v238
	v_mov_b32_e32 v4, v0
	v_med3_f32 v1, v1, s83, v238
	v_mov_b32_e32 v2, v0
	v_cvt_pk_fp8_f32 v4, v3, v3
	v_cvt_pk_fp8_f32 v2, v1, v1
	global_store_byte v[62:63], v6, off offset:96
	global_store_byte v[68:69], v4, off offset:96
	global_store_byte v[66:67], v2, off offset:96

; #define LAS __attribute__((address_space(3)))
; #define LDS_WAIT() asm volatile("s_waitcnt lgkmcnt(0)" ::: "memory")
; __device__ __forceinline__ void p0_transpose_item8(const float* W, int ldw, int srccol0, int k0, unsigned char* dst, int K, LAS float* scr, int lane) {
;     { f32x4 v[8];
; #pragma unroll
;       for (int i = 0; i < 8; ++i) v[i] = *(const f32x4*)(W + (size_t)(k0 + 8 * i + (lane >> 3)) * ldw + srccol0 + 4 * (lane & 7));
; #pragma unroll
;       for (int i = 0; i < 8; ++i) { LAS float* p = scr + (8 * i + (lane >> 3)) * 33 + 4 * (lane & 7); p[0] = v[i][0]; p[1] = v[i][1]; p[2] = v[i][2]; p[3] = v[i][3]; } }
;     LDS_WAIT(); asm volatile("" ::: "memory");
; __device__ __forceinline__ void p0_item(KP Pk, Frame& F, int it, LAS float* scr) {
;     ...
;     { const int le = it / TI_DN, r = it % TI_DN, kb = r / 64, nb = r % 64;
;         p0_transpose_item8(Pk->in[I_ED] + (size_t)le * DE * D, D, 32 * nb, 64 * kb, ws + WS_WD + ((size_t)le * D + 32 * nb) * DE, DE, scr, F.lane); }
.Lcv_dn:
	s_load_dwordx2 s[8:9], s[48:49], 0x108
	s_add_i32 s5, s4, 0xfffec5c0
	s_lshr_b32 s60, s5, 10
	s_and_b32 s5, s5, 0x3c0
	s_lshl_b64 s[18:19], s[60:61], 23
	s_waitcnt lgkmcnt(0)
	s_add_u32 s18, s8, s18
	s_addc_u32 s19, s9, s19
	s_lshl_b32 s8, s4, 5
	s_and_b32 s26, s8, 0x7e0
	s_lshl_b64 s[8:9], s[60:61], 21
	s_lshl_b32 s27, s26, 10
	v_readlane_b32 s34, v255, 7
	s_add_u32 s8, s34, s8
	v_readlane_b32 s34, v255, 8
	s_addc_u32 s9, s34, s9
	s_add_u32 s8, s8, s27
	s_addc_u32 s9, s9, 0
	s_add_u32 s8, s8, s5
	s_addc_u32 s9, s9, 0
	s_lshl_b32 s26, s26, 2
	s_add_u32 s18, s18, s26
	s_addc_u32 s19, s19, 0
	v_add_u32_e32 v32, s5, v2
	v_lshlrev_b32_e32 v32, 13, v32
	v_lshl_add_u32 v68, v4, 2, v32
	v_add_u32_e32 v69, 0x10000, v68
	v_add_u32_e32 v70, 0x20000, v68
	v_add_u32_e32 v71, 0x30000, v68
	v_add_u32_e32 v72, 0x40000, v68
	v_add_u32_e32 v73, 0x50000, v68
	v_add_u32_e32 v74, 0x60000, v68
	v_add_u32_e32 v75, 0x70000, v68
	global_load_dwordx4 v[84:87], v68, s[18:19]
	global_load_dwordx4 v[88:91], v69, s[18:19]
	global_load_dwordx4 v[92:95], v70, s[18:19]
	global_load_dwordx4 v[96:99], v71, s[18:19]
	global_load_dwordx4 v[100:103], v72, s[18:19]
	global_load_dwordx4 v[104:107], v73, s[18:19]
	global_load_dwordx4 v[108:111], v74, s[18:19]
	global_load_dwordx4 v[112:115], v75, s[18:19]
	global_load_dwordx4 v[116:119], v68, s[18:19] offset:128
	global_load_dwordx4 v[120:123], v69, s[18:19] offset:128
	global_load_dwordx4 v[124:127], v70, s[18:19] offset:128
	global_load_dwordx4 v[128:131], v71, s[18:19] offset:128
	global_load_dwordx4 v[132:135], v72, s[18:19] offset:128
	global_load_dwordx4 v[136:139], v73, s[18:19] offset:128
	global_load_dwordx4 v[140:143], v74, s[18:19] offset:128
	global_load_dwordx4 v[144:147], v75, s[18:19] offset:128
	global_load_dwordx4 v[148:151], v68, s[18:19] offset:256
	global_load_dwordx4 v[152:155], v69, s[18:19] offset:256
	global_load_dwordx4 v[156:159], v70, s[18:19] offset:256
	global_load_dwordx4 v[160:163], v71, s[18:19] offset:256
	global_load_dwordx4 v[164:167], v72, s[18:19] offset:256
	global_load_dwordx4 v[168:171], v73, s[18:19] offset:256
	global_load_dwordx4 v[178:181], v74, s[18:19] offset:256
	global_load_dwordx4 v[182:185], v75, s[18:19] offset:256
	global_load_dwordx4 v[196:199], v68, s[18:19] offset:384
	global_load_dwordx4 v[200:203], v69, s[18:19] offset:384
	global_load_dwordx4 v[204:207], v70, s[18:19] offset:384
	global_load_dwordx4 v[208:211], v71, s[18:19] offset:384
	global_load_dwordx4 v[212:215], v72, s[18:19] offset:384
	global_load_dwordx4 v[216:219], v73, s[18:19] offset:384
	global_load_dwordx4 v[220:223], v74, s[18:19] offset:384
	global_load_dwordx4 v[186:189], v75, s[18:19] offset:384
	s_add_u32 s18, s18, 0x200
	s_addc_u32 s19, s19, 0
	s_mov_b32 s43, 0
.Lcv_dn_loop:
	s_cmp_eq_u32 s43, 0
	s_cbranch_scc1 .Lcv_dn_0_f
	s_cmp_eq_u32 s43, 12
	s_cbranch_scc1 .Lcv_dn_0_l
	s_waitcnt vmcnt(40)
	s_branch .Lcv_dn_0_d
.Lcv_dn_0_f:
	s_waitcnt vmcnt(24)
	s_branch .Lcv_dn_0_d
.Lcv_dn_0_l:
	s_waitcnt vmcnt(40)
.Lcv_dn_0_d:
	v_add_u32_e32 v3, v1, v5
	ds_write2_b32 v3, v84, v85 offset1:1
	ds_write2_b32 v3, v86, v87 offset0:2 offset1:3
	v_add_u32_e32 v32, 0x420, v3
	ds_write2_b32 v32, v88, v89 offset1:1
	v_add_u32_e32 v33, 0x428, v3
	ds_write2_b32 v33, v90, v91 offset1:1
	v_add_u32_e32 v32, 0x840, v3
	ds_write2_b32 v32, v92, v93 offset1:1
	v_add_u32_e32 v33, 0x848, v3
	ds_write2_b32 v33, v94, v95 offset1:1
	v_add_u32_e32 v32, 0xc60, v3
	ds_write2_b32 v32, v96, v97 offset1:1
	v_add_u32_e32 v33, 0xc68, v3
	ds_write2_b32 v33, v98, v99 offset1:1
	v_add_u32_e32 v32, 0x1080, v3
	ds_write2_b32 v32, v100, v101 offset1:1
	v_add_u32_e32 v33, 0x1088, v3
	ds_write2_b32 v33, v102, v103 offset1:1
	v_add_u32_e32 v32, 0x14a0, v3
	ds_write2_b32 v32, v104, v105 offset1:1
	v_add_u32_e32 v33, 0x14a8, v3
	ds_write2_b32 v33, v106, v107 offset1:1
	v_add_u32_e32 v32, 0x18c0, v3
	ds_write2_b32 v32, v108, v109 offset1:1
	v_add_u32_e32 v33, 0x18c8, v3
	ds_write2_b32 v33, v110, v111 offset1:1
	v_add_u32_e32 v32, 0x1ce0, v3
	ds_write2_b32 v32, v112, v113 offset1:1
	v_add_u32_e32 v33, 0x1ce8, v3
	ds_write2_b32 v33, v114, v115 offset1:1
	v_mov_b32_e32 v42, v0
	v_mov_b32_e32 v43, v0
	s_waitcnt lgkmcnt(0)
	s_cmp_lt_u32 s43, 12
	s_cbranch_scc0 .Lcv_dn_0_n
	global_load_dwordx4 v[84:87], v68, s[18:19]
	global_load_dwordx4 v[88:91], v69, s[18:19]
	global_load_dwordx4 v[92:95], v70, s[18:19]
	global_load_dwordx4 v[96:99], v71, s[18:19]
	global_load_dwordx4 v[100:103], v72, s[18:19]
	global_load_dwordx4 v[104:107], v73, s[18:19]
	global_load_dwordx4 v[108:111], v74, s[18:19]
	global_load_dwordx4 v[112:115], v75, s[18:19]
; #define LAS __attribute__((address_space(3)))
; #define LDS_WAIT() asm volatile("s_waitcnt lgkmcnt(0)" ::: "memory")
; __device__ __forceinline__ void p0_transpose_item8(const float* W, int ldw, int srccol0, int k0, unsigned char* dst, int K, LAS float* scr, int lane) {
;     ...
;     LDS_WAIT(); asm volatile("" ::: "memory");
;     const int c = lane & 7;
; #pragma unroll
;     for (int j = 0; j < 4; ++j) { const int n = (lane >> 3) + 8 * j; const LAS float* s = scr + (8 * c) * 33 + n;
;         u32x2 o; o.x = pk4_f8(s[0 * 33] * 32.f, s[1 * 33] * 32.f, s[2 * 33] * 32.f, s[3 * 33] * 32.f); o.y = pk4_f8(s[4 * 33] * 32.f, s[5 * 33] * 32.f, s[6 * 33] * 32.f, s[7 * 33] * 32.f);
;         *(u32x2*)(dst + (size_t)n * K + k0 + 8 * c) = o; }
;     LDS_WAIT(); asm volatile("" ::: "memory");
.Lcv_dn_0_n:
	ds_read2_b32 v[34:35], v50 offset1:8
	ds_read2_b32 v[36:37], v50 offset0:33 offset1:41
	ds_read2_b32 v[44:45], v50 offset0:132 offset1:140
	ds_read2_b32 v[46:47], v50 offset0:165 offset1:173
	ds_read2_b32 v[38:39], v50 offset0:66 offset1:74
	ds_read2_b32 v[40:41], v50 offset0:99 offset1:107
	s_waitcnt lgkmcnt(5)
	v_mul_f32_e32 v3, 0x42000000, v34
	s_waitcnt lgkmcnt(4)
	v_mul_f32_e32 v34, 0x42000000, v36
	v_med3_f32 v3, v3, s83, v238
	v_med3_f32 v34, v34, s83, v238
	ds_read2_b32 v[48:49], v50 offset0:198 offset1:206
	ds_read2_b32 v[52:53], v50 offset0:231 offset1:239
	v_cvt_pk_fp8_f32 v42, v3, v34
	s_waitcnt lgkmcnt(5)
	v_mul_f32_e32 v3, 0x42000000, v44
	s_waitcnt lgkmcnt(4)
	v_mul_f32_e32 v34, 0x42000000, v46
	v_med3_f32 v3, v3, s83, v238
	v_med3_f32 v34, v34, s83, v238
	s_waitcnt lgkmcnt(3)
	v_mul_f32_e32 v36, 0x42000000, v38
	s_waitcnt lgkmcnt(2)
	v_mul_f32_e32 v38, 0x42000000, v40
	v_cvt_pk_fp8_f32 v43, v3, v34
	v_mul_f32_e32 v3, 0x42000000, v35
	v_mul_f32_e32 v34, 0x42000000, v37
	v_med3_f32 v36, v36, s83, v238
	v_med3_f32 v38, v38, s83, v238
	v_med3_f32 v3, v3, s83, v238
	v_med3_f32 v37, v34, s83, v238
	v_mov_b32_e32 v34, v0
	v_cvt_pk_fp8_f32 v42, v36, v38 op_sel:[0,0,1]
	s_waitcnt lgkmcnt(1)
	v_mul_f32_e32 v36, 0x42000000, v48
	s_waitcnt lgkmcnt(0)
	v_mul_f32_e32 v38, 0x42000000, v52
	v_cvt_pk_fp8_f32 v34, v3, v37
	v_med3_f32 v36, v36, s83, v238
	v_med3_f32 v38, v38, s83, v238
	v_cvt_pk_fp8_f32 v43, v36, v38 op_sel:[0,0,1]
	v_mul_f32_e32 v35, 0x42000000, v39
	v_mul_f32_e32 v36, 0x42000000, v41
	v_med3_f32 v35, v35, s83, v238
	v_med3_f32 v36, v36, s83, v238
	v_cvt_pk_fp8_f32 v34, v35, v36 op_sel:[0,0,1]
	v_mul_f32_e32 v3, 0x42000000, v45
	v_mul_f32_e32 v35, 0x42000000, v47
	v_med3_f32 v3, v3, s83, v238
	v_med3_f32 v38, v35, s83, v238
	v_mov_b32_e32 v35, v0
	v_cvt_pk_fp8_f32 v35, v3, v38
	v_mul_f32_e32 v36, 0x42000000, v49
	v_mul_f32_e32 v37, 0x42000000, v53
	v_med3_f32 v36, v36, s83, v238
	v_med3_f32 v37, v37, s83, v238
	v_cvt_pk_fp8_f32 v35, v36, v37 op_sel:[0,0,1]
	v_lshl_add_u64 v[32:33], s[8:9], 0, v[6:7]
	v_lshl_add_u64 v[36:37], v[32:33], 0, v[10:11]
	ds_read2_b32 v[44:45], v50 offset0:148 offset1:156
	global_store_dwordx2 v[36:37], v[34:35], off
	ds_read2_b32 v[34:35], v50 offset0:16 offset1:24
	ds_read2_b32 v[36:37], v50 offset0:49 offset1:57
	ds_read2_b32 v[46:47], v50 offset0:181 offset1:189
	ds_read2_b32 v[38:39], v50 offset0:82 offset1:90
	ds_read2_b32 v[40:41], v50 offset0:115 offset1:123
	v_lshl_add_u64 v[54:55], v[32:33], 0, v[8:9]
	s_waitcnt lgkmcnt(4)
	v_mul_f32_e32 v3, 0x42000000, v34
	s_waitcnt lgkmcnt(3)
	v_mul_f32_e32 v34, 0x42000000, v36
	global_store_dwordx2 v[54:55], v[42:43], off
	v_med3_f32 v3, v3, s83, v238
	v_med3_f32 v34, v34, s83, v238
	v_mov_b32_e32 v42, v0
	ds_read2_b32 v[48:49], v50 offset0:214 offset1:222
	ds_read2_b32 v[52:53], v50 offset0:247 offset1:255
	v_cvt_pk_fp8_f32 v42, v3, v34
	v_mul_f32_e32 v3, 0x42000000, v44
	s_waitcnt lgkmcnt(4)
	v_mul_f32_e32 v34, 0x42000000, v46
	v_med3_f32 v3, v3, s83, v238
	v_med3_f32 v34, v34, s83, v238
	v_mov_b32_e32 v43, v0
	s_waitcnt lgkmcnt(3)
	v_mul_f32_e32 v36, 0x42000000, v38
	s_waitcnt lgkmcnt(2)
	v_mul_f32_e32 v38, 0x42000000, v40
	v_cvt_pk_fp8_f32 v43, v3, v34
	v_mul_f32_e32 v3, 0x42000000, v35
	v_mul_f32_e32 v34, 0x42000000, v37
	v_med3_f32 v36, v36, s83, v238
	v_med3_f32 v38, v38, s83, v238
	v_med3_f32 v3, v3, s83, v238
	v_med3_f32 v37, v34, s83, v238
	v_mov_b32_e32 v34, v0
	v_cvt_pk_fp8_f32 v42, v36, v38 op_sel:[0,0,1]
	s_waitcnt lgkmcnt(1)
	v_mul_f32_e32 v36, 0x42000000, v48
	s_waitcnt lgkmcnt(0)
	v_mul_f32_e32 v38, 0x42000000, v52
	v_cvt_pk_fp8_f32 v34, v3, v37
	v_med3_f32 v36, v36, s83, v238
	v_med3_f32 v38, v38, s83, v238
	v_cvt_pk_fp8_f32 v43, v36, v38 op_sel:[0,0,1]
	v_mul_f32_e32 v35, 0x42000000, v39
	v_mul_f32_e32 v36, 0x42000000, v41
	v_med3_f32 v35, v35, s83, v238
	v_med3_f32 v36, v36, s83, v238
	v_cvt_pk_fp8_f32 v34, v35, v36 op_sel:[0,0,1]
	v_mul_f32_e32 v3, 0x42000000, v45
	v_mul_f32_e32 v35, 0x42000000, v47
	v_med3_f32 v3, v3, s83, v238
	v_med3_f32 v38, v35, s83, v238
	v_mov_b32_e32 v35, v0
	v_cvt_pk_fp8_f32 v35, v3, v38
	v_mul_f32_e32 v36, 0x42000000, v49
	v_mul_f32_e32 v37, 0x42000000, v53
	v_med3_f32 v36, v36, s83, v238
	v_med3_f32 v37, v37, s83, v238
	v_cvt_pk_fp8_f32 v35, v36, v37 op_sel:[0,0,1]
	v_lshl_add_u64 v[54:55], v[32:33], 0, v[12:13]
	v_lshl_add_u64 v[32:33], v[32:33], 0, v[14:15]
	global_store_dwordx2 v[54:55], v[42:43], off
	global_store_dwordx2 v[32:33], v[34:35], off
	s_waitcnt lgkmcnt(0)
	s_add_u32 s8, s8, 0x8000
	s_addc_u32 s9, s9, 0
	s_cmp_eq_u32 s43, 0
	s_cbranch_scc1 .Lcv_dn_1_f
	s_cmp_eq_u32 s43, 12
	s_cbranch_scc1 .Lcv_dn_1_l
	s_waitcnt vmcnt(40)
	s_branch .Lcv_dn_1_d
.Lcv_dn_1_f:
	s_waitcnt vmcnt(28)
	s_branch .Lcv_dn_1_d
.Lcv_dn_1_l:
	s_waitcnt vmcnt(32)
.Lcv_dn_1_d:
	v_add_u32_e32 v3, v1, v5
	ds_write2_b32 v3, v116, v117 offset1:1
	ds_write2_b32 v3, v118, v119 offset0:2 offset1:3
	v_add_u32_e32 v32, 0x420, v3
	ds_write2_b32 v32, v120, v121 offset1:1
	v_add_u32_e32 v33, 0x428, v3
	ds_write2_b32 v33, v122, v123 offset1:1
	v_add_u32_e32 v32, 0x840, v3
	ds_write2_b32 v32, v124, v125 offset1:1
	v_add_u32_e32 v33, 0x848, v3
	ds_write2_b32 v33, v126, v127 offset1:1
	v_add_u32_e32 v32, 0xc60, v3
	ds_write2_b32 v32, v128, v129 offset1:1
	v_add_u32_e32 v33, 0xc68, v3
	ds_write2_b32 v33, v130, v131 offset1:1
	v_add_u32_e32 v32, 0x1080, v3
	ds_write2_b32 v32, v132, v133 offset1:1
	v_add_u32_e32 v33, 0x1088, v3
	ds_write2_b32 v33, v134, v135 offset1:1
	v_add_u32_e32 v32, 0x14a0, v3
	ds_write2_b32 v32, v136, v137 offset1:1
	v_add_u32_e32 v33, 0x14a8, v3
	ds_write2_b32 v33, v138, v139 offset1:1
	v_add_u32_e32 v32, 0x18c0, v3
	ds_write2_b32 v32, v140, v141 offset1:1
	v_add_u32_e32 v33, 0x18c8, v3
	ds_write2_b32 v33, v142, v143 offset1:1
	v_add_u32_e32 v32, 0x1ce0, v3
	ds_write2_b32 v32, v144, v145 offset1:1
	v_add_u32_e32 v33, 0x1ce8, v3
	ds_write2_b32 v33, v146, v147 offset1:1
	v_mov_b32_e32 v42, v0
	v_mov_b32_e32 v43, v0
	s_waitcnt lgkmcnt(0)
	s_cmp_lt_u32 s43, 12
	s_cbranch_scc0 .Lcv_dn_1_n
	global_load_dwordx4 v[116:119], v68, s[18:19] offset:128
	global_load_dwordx4 v[120:123], v69, s[18:19] offset:128
	global_load_dwordx4 v[124:127], v70, s[18:19] offset:128
	global_load_dwordx4 v[128:131], v71, s[18:19] offset:128
	global_load_dwordx4 v[132:135], v72, s[18:19] offset:128
	global_load_dwordx4 v[136:139], v73, s[18:19] offset:128
	global_load_dwordx4 v[140:143], v74, s[18:19] offset:128
	global_load_dwordx4 v[144:147], v75, s[18:19] offset:128

; #define LAS __attribute__((address_space(3)))
; #define LDS_WAIT() asm volatile("s_waitcnt lgkmcnt(0)" ::: "memory")
; __device__ __forceinline__ void p0_transpose_item8(const float* W, int ldw, int srccol0, int k0, unsigned char* dst, int K, LAS float* scr, int lane) {
;     { f32x4 v[8];
; #pragma unroll
;       for (int i = 0; i < 8; ++i) v[i] = *(const f32x4*)(W + (size_t)(k0 + 8 * i + (lane >> 3)) * ldw + srccol0 + 4 * (lane & 7));
; #pragma unroll
;       for (int i = 0; i < 8; ++i) { LAS float* p = scr + (8 * i + (lane >> 3)) * 33 + 4 * (lane & 7); p[0] = v[i][0]; p[1] = v[i][1]; p[2] = v[i][2]; p[3] = v[i][3]; } }
;     LDS_WAIT(); asm volatile("" ::: "memory");
.Lcv_dn_2_f:
	s_waitcnt vmcnt(32)
	s_branch .Lcv_dn_2_d
.Lcv_dn_2_l:
	s_waitcnt vmcnt(24)
.Lcv_dn_2_d:
	v_add_u32_e32 v3, v1, v5
	ds_write2_b32 v3, v148, v149 offset1:1
	ds_write2_b32 v3, v150, v151 offset0:2 offset1:3
	v_add_u32_e32 v32, 0x420, v3
	ds_write2_b32 v32, v152, v153 offset1:1
	v_add_u32_e32 v33, 0x428, v3
	ds_write2_b32 v33, v154, v155 offset1:1
	v_add_u32_e32 v32, 0x840, v3
	ds_write2_b32 v32, v156, v157 offset1:1
	v_add_u32_e32 v33, 0x848, v3
	ds_write2_b32 v33, v158, v159 offset1:1
	v_add_u32_e32 v32, 0xc60, v3
	ds_write2_b32 v32, v160, v161 offset1:1
	v_add_u32_e32 v33, 0xc68, v3
	ds_write2_b32 v33, v162, v163 offset1:1
	v_add_u32_e32 v32, 0x1080, v3
	ds_write2_b32 v32, v164, v165 offset1:1
	v_add_u32_e32 v33, 0x1088, v3
	ds_write2_b32 v33, v166, v167 offset1:1
	v_add_u32_e32 v32, 0x14a0, v3
	ds_write2_b32 v32, v168, v169 offset1:1
	v_add_u32_e32 v33, 0x14a8, v3
	ds_write2_b32 v33, v170, v171 offset1:1
	v_add_u32_e32 v32, 0x18c0, v3
	ds_write2_b32 v32, v178, v179 offset1:1
	v_add_u32_e32 v33, 0x18c8, v3
	ds_write2_b32 v33, v180, v181 offset1:1
	v_add_u32_e32 v32, 0x1ce0, v3
	ds_write2_b32 v32, v182, v183 offset1:1
	v_add_u32_e32 v33, 0x1ce8, v3
	ds_write2_b32 v33, v184, v185 offset1:1
	v_mov_b32_e32 v42, v0
	v_mov_b32_e32 v43, v0
	s_waitcnt lgkmcnt(0)
	s_cmp_lt_u32 s43, 12
	s_cbranch_scc0 .Lcv_dn_2_n
	global_load_dwordx4 v[148:151], v68, s[18:19] offset:256
	global_load_dwordx4 v[152:155], v69, s[18:19] offset:256
	global_load_dwordx4 v[156:159], v70, s[18:19] offset:256
	global_load_dwordx4 v[160:163], v71, s[18:19] offset:256
	global_load_dwordx4 v[164:167], v72, s[18:19] offset:256
	global_load_dwordx4 v[168:171], v73, s[18:19] offset:256
	global_load_dwordx4 v[178:181], v74, s[18:19] offset:256
	global_load_dwordx4 v[182:185], v75, s[18:19] offset:256

; #define LAS __attribute__((address_space(3)))
; #define LDS_WAIT() asm volatile("s_waitcnt lgkmcnt(0)" ::: "memory")
; __device__ __forceinline__ void p0_transpose_item8(const float* W, int ldw, int srccol0, int k0, unsigned char* dst, int K, LAS float* scr, int lane) {
;     { f32x4 v[8];
; #pragma unroll
;       for (int i = 0; i < 8; ++i) v[i] = *(const f32x4*)(W + (size_t)(k0 + 8 * i + (lane >> 3)) * ldw + srccol0 + 4 * (lane & 7));
; #pragma unroll
;       for (int i = 0; i < 8; ++i) { LAS float* p = scr + (8 * i + (lane >> 3)) * 33 + 4 * (lane & 7); p[0] = v[i][0]; p[1] = v[i][1]; p[2] = v[i][2]; p[3] = v[i][3]; } }
;     LDS_WAIT(); asm volatile("" ::: "memory");
;     const int c = lane & 7;
; #pragma unroll
;     for (int j = 0; j < 4; ++j) { const int n = (lane >> 3) + 8 * j; const LAS float* s = scr + (8 * c) * 33 + n;
;         u32x2 o; o.x = pk4_f8(s[0 * 33] * 32.f, s[1 * 33] * 32.f, s[2 * 33] * 32.f, s[3 * 33] * 32.f); o.y = pk4_f8(s[4 * 33] * 32.f, s[5 * 33] * 32.f, s[6 * 33] * 32.f, s[7 * 33] * 32.f);
;         *(u32x2*)(dst + (size_t)n * K + k0 + 8 * c) = o; }
;     LDS_WAIT(); asm volatile("" ::: "memory");
.Lcv_dn_3_f:
	s_waitcnt vmcnt(36)
	s_branch .Lcv_dn_3_d
.Lcv_dn_3_l:
	s_waitcnt vmcnt(16)
.Lcv_dn_3_d:
	v_add_u32_e32 v3, v1, v5
	ds_write2_b32 v3, v196, v197 offset1:1
	ds_write2_b32 v3, v198, v199 offset0:2 offset1:3
	v_add_u32_e32 v32, 0x420, v3
	ds_write2_b32 v32, v200, v201 offset1:1
	v_add_u32_e32 v33, 0x428, v3
	ds_write2_b32 v33, v202, v203 offset1:1
	v_add_u32_e32 v32, 0x840, v3
	ds_write2_b32 v32, v204, v205 offset1:1
	v_add_u32_e32 v33, 0x848, v3
	ds_write2_b32 v33, v206, v207 offset1:1
	v_add_u32_e32 v32, 0xc60, v3
	ds_write2_b32 v32, v208, v209 offset1:1
	v_add_u32_e32 v33, 0xc68, v3
	ds_write2_b32 v33, v210, v211 offset1:1
	v_add_u32_e32 v32, 0x1080, v3
	ds_write2_b32 v32, v212, v213 offset1:1
	v_add_u32_e32 v33, 0x1088, v3
	ds_write2_b32 v33, v214, v215 offset1:1
	v_add_u32_e32 v32, 0x14a0, v3
	ds_write2_b32 v32, v216, v217 offset1:1
	v_add_u32_e32 v33, 0x14a8, v3
	ds_write2_b32 v33, v218, v219 offset1:1
	v_add_u32_e32 v32, 0x18c0, v3
	ds_write2_b32 v32, v220, v221 offset1:1
	v_add_u32_e32 v33, 0x18c8, v3
	ds_write2_b32 v33, v222, v223 offset1:1
	v_add_u32_e32 v32, 0x1ce0, v3
	ds_write2_b32 v32, v186, v187 offset1:1
	v_add_u32_e32 v33, 0x1ce8, v3
	ds_write2_b32 v33, v188, v189 offset1:1
	v_mov_b32_e32 v42, v0
	v_mov_b32_e32 v43, v0
	s_waitcnt lgkmcnt(0)
	s_cmp_lt_u32 s43, 12
	s_cbranch_scc0 .Lcv_dn_3_n
	global_load_dwordx4 v[196:199], v68, s[18:19] offset:384
	global_load_dwordx4 v[200:203], v69, s[18:19] offset:384
	global_load_dwordx4 v[204:207], v70, s[18:19] offset:384
	global_load_dwordx4 v[208:211], v71, s[18:19] offset:384
	global_load_dwordx4 v[212:215], v72, s[18:19] offset:384
	global_load_dwordx4 v[216:219], v73, s[18:19] offset:384
	global_load_dwordx4 v[220:223], v74, s[18:19] offset:384
	global_load_dwordx4 v[186:189], v75, s[18:19] offset:384
.Lcv_dn_3_n:
	ds_read2_b32 v[34:35], v50 offset1:8
	ds_read2_b32 v[36:37], v50 offset0:33 offset1:41
	ds_read2_b32 v[44:45], v50 offset0:132 offset1:140
	ds_read2_b32 v[46:47], v50 offset0:165 offset1:173
	ds_read2_b32 v[38:39], v50 offset0:66 offset1:74
	ds_read2_b32 v[40:41], v50 offset0:99 offset1:107
	s_waitcnt lgkmcnt(5)
	v_mul_f32_e32 v3, 0x42000000, v34
	s_waitcnt lgkmcnt(4)
	v_mul_f32_e32 v34, 0x42000000, v36
	v_med3_f32 v3, v3, s83, v238
	v_med3_f32 v34, v34, s83, v238
	ds_read2_b32 v[48:49], v50 offset0:198 offset1:206
	ds_read2_b32 v[52:53], v50 offset0:231 offset1:239
	v_cvt_pk_fp8_f32 v42, v3, v34
	s_waitcnt lgkmcnt(5)
	v_mul_f32_e32 v3, 0x42000000, v44
	s_waitcnt lgkmcnt(4)
	v_mul_f32_e32 v34, 0x42000000, v46
	v_med3_f32 v3, v3, s83, v238
	v_med3_f32 v34, v34, s83, v238
	s_waitcnt lgkmcnt(3)
	v_mul_f32_e32 v36, 0x42000000, v38
	s_waitcnt lgkmcnt(2)
	v_mul_f32_e32 v38, 0x42000000, v40
	v_cvt_pk_fp8_f32 v43, v3, v34
	v_mul_f32_e32 v3, 0x42000000, v35
	v_mul_f32_e32 v34, 0x42000000, v37
	v_med3_f32 v36, v36, s83, v238
	v_med3_f32 v38, v38, s83, v238
	v_med3_f32 v3, v3, s83, v238
	v_med3_f32 v37, v34, s83, v238
	v_mov_b32_e32 v34, v0
	v_cvt_pk_fp8_f32 v42, v36, v38 op_sel:[0,0,1]
	s_waitcnt lgkmcnt(1)
	v_mul_f32_e32 v36, 0x42000000, v48
	s_waitcnt lgkmcnt(0)
	v_mul_f32_e32 v38, 0x42000000, v52
	v_cvt_pk_fp8_f32 v34, v3, v37
	v_med3_f32 v36, v36, s83, v238
	v_med3_f32 v38, v38, s83, v238
	v_cvt_pk_fp8_f32 v43, v36, v38 op_sel:[0,0,1]
	v_mul_f32_e32 v35, 0x42000000, v39
	v_mul_f32_e32 v36, 0x42000000, v41
	v_med3_f32 v35, v35, s83, v238
	v_med3_f32 v36, v36, s83, v238
	v_cvt_pk_fp8_f32 v34, v35, v36 op_sel:[0,0,1]
	v_mul_f32_e32 v3, 0x42000000, v45
	v_mul_f32_e32 v35, 0x42000000, v47
	v_med3_f32 v3, v3, s83, v238
	v_med3_f32 v38, v35, s83, v238
	v_mov_b32_e32 v35, v0
	v_cvt_pk_fp8_f32 v35, v3, v38
	v_mul_f32_e32 v36, 0x42000000, v49
	v_mul_f32_e32 v37, 0x42000000, v53
	v_med3_f32 v36, v36, s83, v238
	v_med3_f32 v37, v37, s83, v238
	v_cvt_pk_fp8_f32 v35, v36, v37 op_sel:[0,0,1]
	v_lshl_add_u64 v[32:33], s[8:9], 0, v[6:7]
	v_lshl_add_u64 v[36:37], v[32:33], 0, v[10:11]
	ds_read2_b32 v[44:45], v50 offset0:148 offset1:156
	global_store_dwordx2 v[36:37], v[34:35], off
	ds_read2_b32 v[34:35], v50 offset0:16 offset1:24
	ds_read2_b32 v[36:37], v50 offset0:49 offset1:57
	ds_read2_b32 v[46:47], v50 offset0:181 offset1:189
	ds_read2_b32 v[38:39], v50 offset0:82 offset1:90
	ds_read2_b32 v[40:41], v50 offset0:115 offset1:123
	v_lshl_add_u64 v[54:55], v[32:33], 0, v[8:9]
	s_waitcnt lgkmcnt(4)
	v_mul_f32_e32 v3, 0x42000000, v34
	s_waitcnt lgkmcnt(3)
	v_mul_f32_e32 v34, 0x42000000, v36
	global_store_dwordx2 v[54:55], v[42:43], off
	v_med3_f32 v3, v3, s83, v238
	v_med3_f32 v34, v34, s83, v238
	v_mov_b32_e32 v42, v0
	ds_read2_b32 v[48:49], v50 offset0:214 offset1:222
	ds_read2_b32 v[52:53], v50 offset0:247 offset1:255
	v_cvt_pk_fp8_f32 v42, v3, v34
	v_mul_f32_e32 v3, 0x42000000, v44
	s_waitcnt lgkmcnt(4)
	v_mul_f32_e32 v34, 0x42000000, v46
	v_med3_f32 v3, v3, s83, v238
	v_med3_f32 v34, v34, s83, v238
	v_mov_b32_e32 v43, v0
	s_waitcnt lgkmcnt(3)
	v_mul_f32_e32 v36, 0x42000000, v38
	s_waitcnt lgkmcnt(2)
	v_mul_f32_e32 v38, 0x42000000, v40
	v_cvt_pk_fp8_f32 v43, v3, v34
	v_mul_f32_e32 v3, 0x42000000, v35
	v_mul_f32_e32 v34, 0x42000000, v37
	v_med3_f32 v36, v36, s83, v238
	v_med3_f32 v38, v38, s83, v238
	v_med3_f32 v3, v3, s83, v238
	v_med3_f32 v37, v34, s83, v238
	v_mov_b32_e32 v34, v0
	v_cvt_pk_fp8_f32 v42, v36, v38 op_sel:[0,0,1]
	s_waitcnt lgkmcnt(1)
	v_mul_f32_e32 v36, 0x42000000, v48
	s_waitcnt lgkmcnt(0)
	v_mul_f32_e32 v38, 0x42000000, v52
	v_cvt_pk_fp8_f32 v34, v3, v37
	v_med3_f32 v36, v36, s83, v238
	v_med3_f32 v38, v38, s83, v238
	v_cvt_pk_fp8_f32 v43, v36, v38 op_sel:[0,0,1]
	v_mul_f32_e32 v35, 0x42000000, v39
	v_mul_f32_e32 v36, 0x42000000, v41
	v_med3_f32 v35, v35, s83, v238
	v_med3_f32 v36, v36, s83, v238
	v_cvt_pk_fp8_f32 v34, v35, v36 op_sel:[0,0,1]
	v_mul_f32_e32 v3, 0x42000000, v45
	v_mul_f32_e32 v35, 0x42000000, v47
	v_med3_f32 v3, v3, s83, v238
	v_med3_f32 v38, v35, s83, v238
	v_mov_b32_e32 v35, v0
	v_cvt_pk_fp8_f32 v35, v3, v38
	v_mul_f32_e32 v36, 0x42000000, v49
	v_mul_f32_e32 v37, 0x42000000, v53
	v_med3_f32 v36, v36, s83, v238
	v_med3_f32 v37, v37, s83, v238
	v_cvt_pk_fp8_f32 v35, v36, v37 op_sel:[0,0,1]
	v_lshl_add_u64 v[54:55], v[32:33], 0, v[12:13]
	v_lshl_add_u64 v[32:33], v[32:33], 0, v[14:15]
	global_store_dwordx2 v[54:55], v[42:43], off
	global_store_dwordx2 v[32:33], v[34:35], off
	s_waitcnt lgkmcnt(0)
	s_add_u32 s8, s8, 0x8000
	s_addc_u32 s9, s9, 0
	s_add_u32 s18, s18, 0x200
	s_addc_u32 s19, s19, 0
	s_add_i32 s43, s43, 4
	s_cmp_lt_u32 s43, 16
	s_cbranch_scc1 .Lcv_dn_loop
	s_mov_b32 s43, 15
	s_branch .LBB0_819
; #define LAS __attribute__((address_space(3)))
; __device__ __forceinline__ void p0_transpose_item8(const float* W, int ldw, int srccol0, int k0, unsigned char* dst, int K, LAS float* scr, int lane) {
;     { f32x4 v[8];
; #pragma unroll
;       for (int i = 0; i < 8; ++i) v[i] = *(const f32x4*)(W + (size_t)(k0 + 8 * i + (lane >> 3)) * ldw + srccol0 + 4 * (lane & 7));
; #pragma unroll
;       for (int i = 0; i < 8; ++i) { LAS float* p = scr + (8 * i + (lane >> 3)) * 33 + 4 * (lane & 7); p[0] = v[i][0]; p[1] = v[i][1]; p[2] = v[i][2]; p[3] = v[i][3]; } }
; __device__ __forceinline__ void p0_item(KP Pk, Frame& F, int it, LAS float* scr) {
;     ...
;     if (it < 32 * TI_GU) { const int le = it / TI_GU, r = it % TI_GU, kb = r / 64, nb = r % 64, n0 = 32 * nb, j = n0 >> 8, half = (n0 >> 7) & 1, c0 = 128 * j + (n0 & 127);
;         p0_transpose_item8((half ? Pk->in[I_EU] : Pk->in[I_EG]) + (size_t)le * D * DE, DE, c0, 64 * kb, ws + WS_WGU + ((size_t)le * 2048 + n0) * D, D, scr, F.lane); return; }
.Lcv_gu:
	s_load_dwordx2 s[18:19], s[48:49], 0xf8
	s_load_dwordx2 s[26:27], s[48:49], 0x100
	s_add_i32 s5, s4, 0xffffc5c0
	s_and_b32 s60, s5, 0xfffff800
	s_and_b32 s34, s5, 0x7c0
	s_lshl_b32 s8, s4, 5
	s_and_b32 s8, s8, 0x7e0
	s_lshl_b32 s9, s4, 4
	s_and_b32 s9, s9, 0x380
	s_lshl_b32 s5, s4, 5
	s_and_b32 s5, s5, 0x60
	s_or_b32 s5, s9, s5
	s_lshl_b32 s5, s5, 2
	s_or_b32 s8, s60, s8
	s_mov_b32 s9, 0
	s_lshl_b64 s[8:9], s[8:9], 11
	v_readlane_b32 s4, v255, 9
	s_add_u32 s8, s4, s8
	v_readlane_b32 s4, v255, 10
	s_addc_u32 s9, s4, s9
	s_add_u32 s8, s8, s34
	s_addc_u32 s9, s9, 0
	s_lshl_b32 s60, s60, 12
	s_add_u32 s60, s60, s5
	s_waitcnt lgkmcnt(0)
	s_add_u32 s18, s18, s60
	s_addc_u32 s19, s19, 0
	s_add_u32 s26, s26, s60
	s_addc_u32 s27, s27, 0
	v_add_u32_e32 v32, s34, v2
	v_lshlrev_b32_e32 v32, 12, v32
	v_lshl_add_u32 v68, v4, 2, v32
	v_add_u32_e32 v69, 0x8000, v68
	v_add_u32_e32 v70, 0x10000, v68
	v_add_u32_e32 v71, 0x18000, v68
	v_add_u32_e32 v72, 0x20000, v68
	v_add_u32_e32 v73, 0x28000, v68
	v_add_u32_e32 v74, 0x30000, v68
	v_add_u32_e32 v75, 0x38000, v68
	global_load_dwordx4 v[84:87], v68, s[18:19]
	global_load_dwordx4 v[88:91], v69, s[18:19]
	global_load_dwordx4 v[92:95], v70, s[18:19]
	global_load_dwordx4 v[96:99], v71, s[18:19]
	global_load_dwordx4 v[100:103], v72, s[18:19]
	global_load_dwordx4 v[104:107], v73, s[18:19]
	global_load_dwordx4 v[108:111], v74, s[18:19]
	global_load_dwordx4 v[112:115], v75, s[18:19]
	global_load_dwordx4 v[116:119], v68, s[18:19] offset:128
	global_load_dwordx4 v[120:123], v69, s[18:19] offset:128
	global_load_dwordx4 v[124:127], v70, s[18:19] offset:128
	global_load_dwordx4 v[128:131], v71, s[18:19] offset:128
	global_load_dwordx4 v[132:135], v72, s[18:19] offset:128
	global_load_dwordx4 v[136:139], v73, s[18:19] offset:128
	global_load_dwordx4 v[140:143], v74, s[18:19] offset:128
	global_load_dwordx4 v[144:147], v75, s[18:19] offset:128
	global_load_dwordx4 v[148:151], v68, s[18:19] offset:256
	global_load_dwordx4 v[152:155], v69, s[18:19] offset:256
	global_load_dwordx4 v[156:159], v70, s[18:19] offset:256
	global_load_dwordx4 v[160:163], v71, s[18:19] offset:256
	global_load_dwordx4 v[164:167], v72, s[18:19] offset:256
	global_load_dwordx4 v[168:171], v73, s[18:19] offset:256
	global_load_dwordx4 v[178:181], v74, s[18:19] offset:256
	global_load_dwordx4 v[182:185], v75, s[18:19] offset:256
	global_load_dwordx4 v[196:199], v68, s[18:19] offset:384
	global_load_dwordx4 v[200:203], v69, s[18:19] offset:384
	global_load_dwordx4 v[204:207], v70, s[18:19] offset:384
	global_load_dwordx4 v[208:211], v71, s[18:19] offset:384
	global_load_dwordx4 v[212:215], v72, s[18:19] offset:384
	global_load_dwordx4 v[216:219], v73, s[18:19] offset:384
	global_load_dwordx4 v[220:223], v74, s[18:19] offset:384
	global_load_dwordx4 v[186:189], v75, s[18:19] offset:384
	s_mov_b32 s4, s18
	s_mov_b32 s5, s19
	s_mov_b32 s18, s26
	s_mov_b32 s19, s27
	s_add_u32 s26, s4, 0x200
	s_addc_u32 s27, s5, 0
	s_mov_b32 s43, 0

; #define LAS __attribute__((address_space(3)))
; #define LDS_WAIT() asm volatile("s_waitcnt lgkmcnt(0)" ::: "memory")
; __device__ __forceinline__ void p0_transpose_item8(const float* W, int ldw, int srccol0, int k0, unsigned char* dst, int K, LAS float* scr, int lane) {
;     ...
;     LDS_WAIT(); asm volatile("" ::: "memory");
;     const int c = lane & 7;
; #pragma unroll
;     for (int j = 0; j < 4; ++j) { const int n = (lane >> 3) + 8 * j; const LAS float* s = scr + (8 * c) * 33 + n;
;         u32x2 o; o.x = pk4_f8(s[0 * 33] * 32.f, s[1 * 33] * 32.f, s[2 * 33] * 32.f, s[3 * 33] * 32.f); o.y = pk4_f8(s[4 * 33] * 32.f, s[5 * 33] * 32.f, s[6 * 33] * 32.f, s[7 * 33] * 32.f);
;         *(u32x2*)(dst + (size_t)n * K + k0 + 8 * c) = o; }
;     LDS_WAIT(); asm volatile("" ::: "memory");
.Lcv_gu_0_n:
	ds_read2_b32 v[34:35], v50 offset1:8
	ds_read2_b32 v[36:37], v50 offset0:33 offset1:41
	ds_read2_b32 v[44:45], v50 offset0:132 offset1:140
	ds_read2_b32 v[46:47], v50 offset0:165 offset1:173
	ds_read2_b32 v[38:39], v50 offset0:66 offset1:74
	ds_read2_b32 v[40:41], v50 offset0:99 offset1:107
	s_waitcnt lgkmcnt(5)
	v_mul_f32_e32 v3, 0x42000000, v34
	s_waitcnt lgkmcnt(4)
	v_mul_f32_e32 v34, 0x42000000, v36
	v_med3_f32 v3, v3, s83, v238
	v_med3_f32 v34, v34, s83, v238
	ds_read2_b32 v[48:49], v50 offset0:198 offset1:206
	ds_read2_b32 v[52:53], v50 offset0:231 offset1:239
	v_cvt_pk_fp8_f32 v42, v3, v34
	s_waitcnt lgkmcnt(5)
	v_mul_f32_e32 v3, 0x42000000, v44
	s_waitcnt lgkmcnt(4)
	v_mul_f32_e32 v34, 0x42000000, v46
	v_med3_f32 v3, v3, s83, v238
	v_med3_f32 v34, v34, s83, v238
	s_waitcnt lgkmcnt(3)
	v_mul_f32_e32 v36, 0x42000000, v38
	s_waitcnt lgkmcnt(2)
	v_mul_f32_e32 v38, 0x42000000, v40
	v_cvt_pk_fp8_f32 v43, v3, v34
	v_mul_f32_e32 v3, 0x42000000, v35
	v_mul_f32_e32 v34, 0x42000000, v37
	v_med3_f32 v36, v36, s83, v238
	v_med3_f32 v38, v38, s83, v238
	v_med3_f32 v3, v3, s83, v238
	v_med3_f32 v37, v34, s83, v238
	v_mov_b32_e32 v34, v0
	v_cvt_pk_fp8_f32 v42, v36, v38 op_sel:[0,0,1]
	s_waitcnt lgkmcnt(1)
	v_mul_f32_e32 v36, 0x42000000, v48
	s_waitcnt lgkmcnt(0)
	v_mul_f32_e32 v38, 0x42000000, v52
	v_cvt_pk_fp8_f32 v34, v3, v37
	v_med3_f32 v36, v36, s83, v238
	v_med3_f32 v38, v38, s83, v238
	v_cvt_pk_fp8_f32 v43, v36, v38 op_sel:[0,0,1]
	v_mul_f32_e32 v35, 0x42000000, v39
	v_mul_f32_e32 v36, 0x42000000, v41
	v_med3_f32 v35, v35, s83, v238
	v_med3_f32 v36, v36, s83, v238
	v_cvt_pk_fp8_f32 v34, v35, v36 op_sel:[0,0,1]
	v_mul_f32_e32 v3, 0x42000000, v45
	v_mul_f32_e32 v35, 0x42000000, v47
	v_med3_f32 v3, v3, s83, v238
	v_med3_f32 v38, v35, s83, v238
	v_mov_b32_e32 v35, v0
	v_cvt_pk_fp8_f32 v35, v3, v38
	v_mul_f32_e32 v36, 0x42000000, v49
	v_mul_f32_e32 v37, 0x42000000, v53
	v_med3_f32 v36, v36, s83, v238
	v_med3_f32 v37, v37, s83, v238
	v_cvt_pk_fp8_f32 v35, v36, v37 op_sel:[0,0,1]
	v_lshl_add_u64 v[32:33], s[8:9], 0, v[6:7]
	v_lshl_add_u64 v[36:37], v[32:33], 0, v[18:19]
	ds_read2_b32 v[44:45], v50 offset0:148 offset1:156
	global_store_dwordx2 v[36:37], v[34:35], off
	ds_read2_b32 v[34:35], v50 offset0:16 offset1:24
	ds_read2_b32 v[36:37], v50 offset0:49 offset1:57
	ds_read2_b32 v[46:47], v50 offset0:181 offset1:189
	ds_read2_b32 v[38:39], v50 offset0:82 offset1:90
	ds_read2_b32 v[40:41], v50 offset0:115 offset1:123
	v_lshl_add_u64 v[54:55], v[32:33], 0, v[16:17]
	s_waitcnt lgkmcnt(4)
	v_mul_f32_e32 v3, 0x42000000, v34
	s_waitcnt lgkmcnt(3)
	v_mul_f32_e32 v34, 0x42000000, v36
	global_store_dwordx2 v[54:55], v[42:43], off
	v_med3_f32 v3, v3, s83, v238
	v_med3_f32 v34, v34, s83, v238
	v_mov_b32_e32 v42, v0
	ds_read2_b32 v[48:49], v50 offset0:214 offset1:222
	ds_read2_b32 v[52:53], v50 offset0:247 offset1:255
	v_cvt_pk_fp8_f32 v42, v3, v34
	v_mul_f32_e32 v3, 0x42000000, v44
	s_waitcnt lgkmcnt(4)
	v_mul_f32_e32 v34, 0x42000000, v46
	v_med3_f32 v3, v3, s83, v238
	v_med3_f32 v34, v34, s83, v238
	v_mov_b32_e32 v43, v0
	s_waitcnt lgkmcnt(3)
	v_mul_f32_e32 v36, 0x42000000, v38
	s_waitcnt lgkmcnt(2)
	v_mul_f32_e32 v38, 0x42000000, v40
	v_cvt_pk_fp8_f32 v43, v3, v34
	v_mul_f32_e32 v3, 0x42000000, v35
	v_mul_f32_e32 v34, 0x42000000, v37
	v_med3_f32 v36, v36, s83, v238
	v_med3_f32 v38, v38, s83, v238
	v_med3_f32 v3, v3, s83, v238
	v_med3_f32 v37, v34, s83, v238
	v_mov_b32_e32 v34, v0
	v_cvt_pk_fp8_f32 v42, v36, v38 op_sel:[0,0,1]
	s_waitcnt lgkmcnt(1)
	v_mul_f32_e32 v36, 0x42000000, v48
	s_waitcnt lgkmcnt(0)
	v_mul_f32_e32 v38, 0x42000000, v52
	v_cvt_pk_fp8_f32 v34, v3, v37
	v_med3_f32 v36, v36, s83, v238
	v_med3_f32 v38, v38, s83, v238
	v_cvt_pk_fp8_f32 v43, v36, v38 op_sel:[0,0,1]
	v_mul_f32_e32 v35, 0x42000000, v39
	v_mul_f32_e32 v36, 0x42000000, v41
	v_med3_f32 v35, v35, s83, v238
	v_med3_f32 v36, v36, s83, v238
	v_cvt_pk_fp8_f32 v34, v35, v36 op_sel:[0,0,1]
	v_mul_f32_e32 v3, 0x42000000, v45
	v_mul_f32_e32 v35, 0x42000000, v47
	v_med3_f32 v3, v3, s83, v238
	v_med3_f32 v38, v35, s83, v238
	v_mov_b32_e32 v35, v0
	v_cvt_pk_fp8_f32 v35, v3, v38
	v_mul_f32_e32 v36, 0x42000000, v49
	v_mul_f32_e32 v37, 0x42000000, v53
	v_med3_f32 v36, v36, s83, v238
	v_med3_f32 v37, v37, s83, v238
	v_cvt_pk_fp8_f32 v35, v36, v37 op_sel:[0,0,1]
	v_lshl_add_u64 v[54:55], v[32:33], 0, v[20:21]
	v_lshl_add_u64 v[32:33], v[32:33], 0, v[22:23]
	global_store_dwordx2 v[54:55], v[42:43], off
	global_store_dwordx2 v[32:33], v[34:35], off
	s_waitcnt lgkmcnt(0)
	s_add_u32 s8, s8, 0x10000
	s_addc_u32 s9, s9, 0
	s_cmp_eq_u32 s43, 0
	s_cbranch_scc1 .Lcv_gu_1_f
	s_cmp_eq_u32 s43, 12
	s_cbranch_scc1 .Lcv_gu_1_l
	s_waitcnt vmcnt(40)
	s_branch .Lcv_gu_1_d

; #define LAS __attribute__((address_space(3)))
; #define LDS_WAIT() asm volatile("s_waitcnt lgkmcnt(0)" ::: "memory")
; __device__ __forceinline__ void p0_transpose_item8(const float* W, int ldw, int srccol0, int k0, unsigned char* dst, int K, LAS float* scr, int lane) {
;     ...
;     LDS_WAIT(); asm volatile("" ::: "memory");
;     const int c = lane & 7;
; #pragma unroll
;     for (int j = 0; j < 4; ++j) { const int n = (lane >> 3) + 8 * j; const LAS float* s = scr + (8 * c) * 33 + n;
;         u32x2 o; o.x = pk4_f8(s[0 * 33] * 32.f, s[1 * 33] * 32.f, s[2 * 33] * 32.f, s[3 * 33] * 32.f); o.y = pk4_f8(s[4 * 33] * 32.f, s[5 * 33] * 32.f, s[6 * 33] * 32.f, s[7 * 33] * 32.f);
;         *(u32x2*)(dst + (size_t)n * K + k0 + 8 * c) = o; }
;     LDS_WAIT(); asm volatile("" ::: "memory");
; __device__ __forceinline__ void ph_mixers(KP Pk, Frame& F, int l, int qid) {
;     ...
;             for (int j = 0; j < 16; ++j) { int x = tu * 128 + F.wave * 16 + j; if (x >= n_titems) break;
;                 int it;
;                 if (x < 16 * TI_GU) it = 2 * TI_L + l * 16 * TI_GU + x;
;                 else if ((x -= 16 * TI_GU) < 16 * TI_DN) it = 2 * TI_L + 32 * TI_GU + l * 16 * TI_DN + x;
;                 else if ((x -= 16 * TI_DN) < TI_WOUT) it = l * TI_L + TI_WIN + TI_WA + x;
;                 else it = TI_L + (x - TI_WOUT);
;                 p0_item(Pk, F, it, scr); }
.Lcv_gu_3_n:
	ds_read2_b32 v[34:35], v50 offset1:8
	ds_read2_b32 v[36:37], v50 offset0:33 offset1:41
	ds_read2_b32 v[44:45], v50 offset0:132 offset1:140
	ds_read2_b32 v[46:47], v50 offset0:165 offset1:173
	ds_read2_b32 v[38:39], v50 offset0:66 offset1:74
	ds_read2_b32 v[40:41], v50 offset0:99 offset1:107
	s_waitcnt lgkmcnt(5)
	v_mul_f32_e32 v3, 0x42000000, v34
	s_waitcnt lgkmcnt(4)
	v_mul_f32_e32 v34, 0x42000000, v36
	v_med3_f32 v3, v3, s83, v238
	v_med3_f32 v34, v34, s83, v238
	ds_read2_b32 v[48:49], v50 offset0:198 offset1:206
	ds_read2_b32 v[52:53], v50 offset0:231 offset1:239
	v_cvt_pk_fp8_f32 v42, v3, v34
	s_waitcnt lgkmcnt(5)
	v_mul_f32_e32 v3, 0x42000000, v44
	s_waitcnt lgkmcnt(4)
	v_mul_f32_e32 v34, 0x42000000, v46
	v_med3_f32 v3, v3, s83, v238
	v_med3_f32 v34, v34, s83, v238
	s_waitcnt lgkmcnt(3)
	v_mul_f32_e32 v36, 0x42000000, v38
	s_waitcnt lgkmcnt(2)
	v_mul_f32_e32 v38, 0x42000000, v40
	v_cvt_pk_fp8_f32 v43, v3, v34
	v_mul_f32_e32 v3, 0x42000000, v35
	v_mul_f32_e32 v34, 0x42000000, v37
	v_med3_f32 v36, v36, s83, v238
	v_med3_f32 v38, v38, s83, v238
	v_med3_f32 v3, v3, s83, v238
	v_med3_f32 v37, v34, s83, v238
	v_mov_b32_e32 v34, v0
	v_cvt_pk_fp8_f32 v42, v36, v38 op_sel:[0,0,1]
	s_waitcnt lgkmcnt(1)
	v_mul_f32_e32 v36, 0x42000000, v48
	s_waitcnt lgkmcnt(0)
	v_mul_f32_e32 v38, 0x42000000, v52
	v_cvt_pk_fp8_f32 v34, v3, v37
	v_med3_f32 v36, v36, s83, v238
	v_med3_f32 v38, v38, s83, v238
	v_cvt_pk_fp8_f32 v43, v36, v38 op_sel:[0,0,1]
	v_mul_f32_e32 v35, 0x42000000, v39
	v_mul_f32_e32 v36, 0x42000000, v41
	v_med3_f32 v35, v35, s83, v238
	v_med3_f32 v36, v36, s83, v238
	v_cvt_pk_fp8_f32 v34, v35, v36 op_sel:[0,0,1]
	v_mul_f32_e32 v3, 0x42000000, v45
	v_mul_f32_e32 v35, 0x42000000, v47
	v_med3_f32 v3, v3, s83, v238
	v_med3_f32 v38, v35, s83, v238
	v_mov_b32_e32 v35, v0
	v_cvt_pk_fp8_f32 v35, v3, v38
	v_mul_f32_e32 v36, 0x42000000, v49
	v_mul_f32_e32 v37, 0x42000000, v53
	v_med3_f32 v36, v36, s83, v238
	v_med3_f32 v37, v37, s83, v238
	v_cvt_pk_fp8_f32 v35, v36, v37 op_sel:[0,0,1]
	v_lshl_add_u64 v[32:33], s[8:9], 0, v[6:7]
	v_lshl_add_u64 v[36:37], v[32:33], 0, v[18:19]
	ds_read2_b32 v[44:45], v50 offset0:148 offset1:156
	global_store_dwordx2 v[36:37], v[34:35], off
	ds_read2_b32 v[34:35], v50 offset0:16 offset1:24
	ds_read2_b32 v[36:37], v50 offset0:49 offset1:57
	ds_read2_b32 v[46:47], v50 offset0:181 offset1:189
	ds_read2_b32 v[38:39], v50 offset0:82 offset1:90
	ds_read2_b32 v[40:41], v50 offset0:115 offset1:123
	v_lshl_add_u64 v[54:55], v[32:33], 0, v[16:17]
	s_waitcnt lgkmcnt(4)
	v_mul_f32_e32 v3, 0x42000000, v34
	s_waitcnt lgkmcnt(3)
	v_mul_f32_e32 v34, 0x42000000, v36
	global_store_dwordx2 v[54:55], v[42:43], off
	v_med3_f32 v3, v3, s83, v238
	v_med3_f32 v34, v34, s83, v238
	v_mov_b32_e32 v42, v0
	ds_read2_b32 v[48:49], v50 offset0:214 offset1:222
	ds_read2_b32 v[52:53], v50 offset0:247 offset1:255
	v_cvt_pk_fp8_f32 v42, v3, v34
	v_mul_f32_e32 v3, 0x42000000, v44
	s_waitcnt lgkmcnt(4)
	v_mul_f32_e32 v34, 0x42000000, v46
	v_med3_f32 v3, v3, s83, v238
	v_med3_f32 v34, v34, s83, v238
	v_mov_b32_e32 v43, v0
	s_waitcnt lgkmcnt(3)
	v_mul_f32_e32 v36, 0x42000000, v38
	s_waitcnt lgkmcnt(2)
	v_mul_f32_e32 v38, 0x42000000, v40
	v_cvt_pk_fp8_f32 v43, v3, v34
	v_mul_f32_e32 v3, 0x42000000, v35
	v_mul_f32_e32 v34, 0x42000000, v37
	v_med3_f32 v36, v36, s83, v238
	v_med3_f32 v38, v38, s83, v238
	v_med3_f32 v3, v3, s83, v238
	v_med3_f32 v37, v34, s83, v238
	v_mov_b32_e32 v34, v0
	v_cvt_pk_fp8_f32 v42, v36, v38 op_sel:[0,0,1]
	s_waitcnt lgkmcnt(1)
	v_mul_f32_e32 v36, 0x42000000, v48
	s_waitcnt lgkmcnt(0)
	v_mul_f32_e32 v38, 0x42000000, v52
	v_cvt_pk_fp8_f32 v34, v3, v37
	v_med3_f32 v36, v36, s83, v238
	v_med3_f32 v38, v38, s83, v238
	v_cvt_pk_fp8_f32 v43, v36, v38 op_sel:[0,0,1]
	v_mul_f32_e32 v35, 0x42000000, v39
	v_mul_f32_e32 v36, 0x42000000, v41
	v_med3_f32 v35, v35, s83, v238
	v_med3_f32 v36, v36, s83, v238
	v_cvt_pk_fp8_f32 v34, v35, v36 op_sel:[0,0,1]
	v_mul_f32_e32 v3, 0x42000000, v45
	v_mul_f32_e32 v35, 0x42000000, v47
	v_med3_f32 v3, v3, s83, v238
	v_med3_f32 v38, v35, s83, v238
	v_mov_b32_e32 v35, v0
	v_cvt_pk_fp8_f32 v35, v3, v38
	v_mul_f32_e32 v36, 0x42000000, v49
	v_mul_f32_e32 v37, 0x42000000, v53
	v_med3_f32 v36, v36, s83, v238
	v_med3_f32 v37, v37, s83, v238
	v_cvt_pk_fp8_f32 v35, v36, v37 op_sel:[0,0,1]
	v_lshl_add_u64 v[54:55], v[32:33], 0, v[20:21]
	v_lshl_add_u64 v[32:33], v[32:33], 0, v[22:23]
	global_store_dwordx2 v[54:55], v[42:43], off
	global_store_dwordx2 v[32:33], v[34:35], off
	s_waitcnt lgkmcnt(0)
	s_add_u32 s8, s8, 0x10000
	s_addc_u32 s9, s9, 0
	s_mov_b32 s4, s18
	s_mov_b32 s5, s19
	s_mov_b32 s18, s26
	s_mov_b32 s19, s27
	s_add_u32 s26, s4, 0x200
	s_addc_u32 s27, s5, 0
	s_add_i32 s43, s43, 4
	s_cmp_lt_u32 s43, 16
	s_cbranch_scc1 .Lcv_gu_loop
	s_mov_b32 s43, 15
	s_branch .LBB0_819

; #define LAS __attribute__((address_space(3)))
; #define LDS_WAIT() asm volatile("s_waitcnt lgkmcnt(0)" ::: "memory")
; __device__ __forceinline__ void p0_transpose_item8(const float* W, int ldw, int srccol0, int k0, unsigned char* dst, int K, LAS float* scr, int lane) {
;     { f32x4 v[8];
; #pragma unroll
;       for (int i = 0; i < 8; ++i) v[i] = *(const f32x4*)(W + (size_t)(k0 + 8 * i + (lane >> 3)) * ldw + srccol0 + 4 * (lane & 7));
; #pragma unroll
;       for (int i = 0; i < 8; ++i) { LAS float* p = scr + (8 * i + (lane >> 3)) * 33 + 4 * (lane & 7); p[0] = v[i][0]; p[1] = v[i][1]; p[2] = v[i][2]; p[3] = v[i][3]; } }
;     LDS_WAIT(); asm volatile("" ::: "memory");
;     const int c = lane & 7;
; #pragma unroll
;     for (int j = 0; j < 4; ++j) { const int n = (lane >> 3) + 8 * j; const LAS float* s = scr + (8 * c) * 33 + n;
;         u32x2 o; o.x = pk4_f8(s[0 * 33] * 32.f, s[1 * 33] * 32.f, s[2 * 33] * 32.f, s[3 * 33] * 32.f); o.y = pk4_f8(s[4 * 33] * 32.f, s[5 * 33] * 32.f, s[6 * 33] * 32.f, s[7 * 33] * 32.f);
;         *(u32x2*)(dst + (size_t)n * K + k0 + 8 * c) = o; }
;     LDS_WAIT(); asm volatile("" ::: "memory");
; __device__ __forceinline__ void p0_item(KP Pk, Frame& F, int it, LAS float* scr) {
;     ...
;     { const int le = it / TI_DN, r = it % TI_DN, kb = r / 64, nb = r % 64;
;         p0_transpose_item8(Pk->in[I_ED] + (size_t)le * DE * D, D, 32 * nb, 64 * kb, ws + WS_WD + ((size_t)le * D + 32 * nb) * DE, DE, scr, F.lane); }
.LBB0_836:
	s_cmp_gt_u32 s4, 0x13a3f
	s_cbranch_scc0 .LBB0_838
	s_cmp_eq_u32 s43, 0
	s_cbranch_scc1 .Lcv_dn
	s_load_dwordx2 s[8:9], s[48:49], 0x108
	s_add_i32 s5, s4, 0xfffec5c0
	s_lshr_b32 s60, s5, 10
	s_and_b32 s5, s5, 0x3c0
	s_lshl_b64 s[18:19], s[60:61], 23
	s_waitcnt lgkmcnt(0)
	s_add_u32 s18, s8, s18
	s_addc_u32 s19, s9, s19
	s_lshl_b32 s8, s4, 5
	s_and_b32 s26, s8, 0x7e0
	s_lshl_b64 s[8:9], s[60:61], 21
	s_lshl_b32 s27, s26, 10
	v_readlane_b32 s34, v255, 7
	s_add_u32 s8, s34, s8
	v_readlane_b32 s34, v255, 8
	s_addc_u32 s9, s34, s9
	s_add_u32 s27, s8, s27
	s_addc_u32 s34, s9, 0
	s_lshl_b32 s8, s26, 2
	v_add_u32_e32 v32, s5, v2
	s_add_u32 s8, s18, s8
	s_addc_u32 s9, s19, 0
	v_lshlrev_b32_e32 v34, 2, v4
	v_mov_b32_e32 v35, v0
	v_ashrrev_i32_e32 v33, 31, v32
	v_lshl_add_u64 v[34:35], s[8:9], 0, v[34:35]
	v_lshlrev_b64 v[32:33], 13, v[32:33]
	v_lshl_add_u64 v[48:49], v[34:35], 0, v[32:33]
	s_mov_b32 s8, 0x10000
	v_add_co_u32_e32 v36, vcc, s8, v48
	global_load_dwordx4 v[32:35], v[48:49], off
	s_nop 0
	v_addc_co_u32_e32 v37, vcc, 0, v49, vcc
	s_mov_b32 s8, 0x20000
	global_load_dwordx4 v[36:39], v[36:37], off
	v_add_co_u32_e32 v40, vcc, s8, v48
	s_mov_b32 s8, 0x30000
	s_nop 0
	v_addc_co_u32_e32 v41, vcc, 0, v49, vcc
	global_load_dwordx4 v[40:43], v[40:41], off
	v_add_co_u32_e32 v44, vcc, s8, v48
	s_mov_b32 s8, 0x40000
	s_nop 0
	v_addc_co_u32_e32 v45, vcc, 0, v49, vcc
	global_load_dwordx4 v[44:47], v[44:45], off
	v_add_co_u32_e32 v52, vcc, s8, v48
	s_mov_b32 s8, 0x50000
	s_nop 0
	v_addc_co_u32_e32 v53, vcc, 0, v49, vcc
	global_load_dwordx4 v[52:55], v[52:53], off
	v_add_co_u32_e32 v56, vcc, s8, v48
	s_mov_b32 s8, 0x60000
	s_nop 0
	v_addc_co_u32_e32 v57, vcc, 0, v49, vcc
	global_load_dwordx4 v[56:59], v[56:57], off
	v_add_co_u32_e32 v60, vcc, s8, v48
	s_mov_b32 s8, 0x70000
	s_nop 0
	v_addc_co_u32_e32 v61, vcc, 0, v49, vcc
	global_load_dwordx4 v[60:63], v[60:61], off
	v_add_co_u32_e32 v48, vcc, s8, v48
	v_add_u32_e32 v3, v1, v5
	s_nop 0
	v_addc_co_u32_e32 v49, vcc, 0, v49, vcc
	global_load_dwordx4 v[64:67], v[48:49], off
	s_add_u32 s8, s27, s5
	s_addc_u32 s9, s34, 0
	s_waitcnt vmcnt(7)
	ds_write2_b32 v3, v32, v33 offset1:1
	ds_write2_b32 v3, v34, v35 offset0:2 offset1:3
	v_add_u32_e32 v32, 0x420, v3
	s_waitcnt vmcnt(6)
	ds_write2_b32 v32, v36, v37 offset1:1
	v_add_u32_e32 v32, 0x428, v3
	ds_write2_b32 v32, v38, v39 offset1:1
	v_add_u32_e32 v32, 0x840, v3
	s_waitcnt vmcnt(5)
	ds_write2_b32 v32, v40, v41 offset1:1
	v_add_u32_e32 v32, 0x848, v3
	ds_write2_b32 v32, v42, v43 offset1:1
	v_add_u32_e32 v32, 0xc60, v3
	v_mov_b32_e32 v42, v0
	v_mov_b32_e32 v43, v0
	s_waitcnt vmcnt(4)
	ds_write2_b32 v32, v44, v45 offset1:1
	v_add_u32_e32 v32, 0xc68, v3
	ds_write2_b32 v32, v46, v47 offset1:1
	v_add_u32_e32 v32, 0x1080, v3
	s_waitcnt vmcnt(3)
	ds_write2_b32 v32, v52, v53 offset1:1
	v_add_u32_e32 v32, 0x1088, v3
	ds_write2_b32 v32, v54, v55 offset1:1
	v_add_u32_e32 v32, 0x14a0, v3
	s_waitcnt vmcnt(2)
	ds_write2_b32 v32, v56, v57 offset1:1
	v_add_u32_e32 v32, 0x14a8, v3
	ds_write2_b32 v32, v58, v59 offset1:1
	v_add_u32_e32 v32, 0x18c0, v3
	s_waitcnt vmcnt(1)
	ds_write2_b32 v32, v60, v61 offset1:1
	v_add_u32_e32 v32, 0x18c8, v3
	ds_write2_b32 v32, v62, v63 offset1:1
	v_add_u32_e32 v32, 0x1ce0, v3
	v_add_u32_e32 v3, 0x1ce8, v3
	s_waitcnt vmcnt(0)
	ds_write2_b32 v32, v64, v65 offset1:1
	ds_write2_b32 v3, v66, v67 offset1:1
	s_waitcnt lgkmcnt(0)
	ds_read2_b32 v[34:35], v50 offset1:8
	ds_read2_b32 v[36:37], v50 offset0:33 offset1:41
	ds_read2_b32 v[44:45], v50 offset0:132 offset1:140
	ds_read2_b32 v[46:47], v50 offset0:165 offset1:173
	ds_read2_b32 v[38:39], v50 offset0:66 offset1:74
	ds_read2_b32 v[40:41], v50 offset0:99 offset1:107
	s_waitcnt lgkmcnt(5)
	v_mul_f32_e32 v3, 0x42000000, v34
	s_waitcnt lgkmcnt(4)
	v_mul_f32_e32 v34, 0x42000000, v36
	v_med3_f32 v3, v3, s83, v238
	v_med3_f32 v34, v34, s83, v238
	ds_read2_b32 v[48:49], v50 offset0:198 offset1:206
	ds_read2_b32 v[52:53], v50 offset0:231 offset1:239
	v_cvt_pk_fp8_f32 v42, v3, v34
	s_waitcnt lgkmcnt(5)
	v_mul_f32_e32 v3, 0x42000000, v44
	s_waitcnt lgkmcnt(4)
	v_mul_f32_e32 v34, 0x42000000, v46
	v_med3_f32 v3, v3, s83, v238
	v_med3_f32 v34, v34, s83, v238
	s_waitcnt lgkmcnt(3)
	v_mul_f32_e32 v36, 0x42000000, v38
	s_waitcnt lgkmcnt(2)
	v_mul_f32_e32 v38, 0x42000000, v40
	v_cvt_pk_fp8_f32 v43, v3, v34
	v_mul_f32_e32 v3, 0x42000000, v35
	v_mul_f32_e32 v34, 0x42000000, v37
	v_med3_f32 v36, v36, s83, v238
	v_med3_f32 v38, v38, s83, v238
	v_med3_f32 v3, v3, s83, v238
	v_med3_f32 v37, v34, s83, v238
	v_mov_b32_e32 v34, v0
	v_cvt_pk_fp8_f32 v42, v36, v38 op_sel:[0,0,1]
	s_waitcnt lgkmcnt(1)
	v_mul_f32_e32 v36, 0x42000000, v48
	s_waitcnt lgkmcnt(0)
	v_mul_f32_e32 v38, 0x42000000, v52
	v_cvt_pk_fp8_f32 v34, v3, v37
	v_med3_f32 v36, v36, s83, v238
	v_med3_f32 v38, v38, s83, v238
	v_cvt_pk_fp8_f32 v43, v36, v38 op_sel:[0,0,1]
	v_mul_f32_e32 v35, 0x42000000, v39
	v_mul_f32_e32 v36, 0x42000000, v41
	v_med3_f32 v35, v35, s83, v238
	v_med3_f32 v36, v36, s83, v238
	v_cvt_pk_fp8_f32 v34, v35, v36 op_sel:[0,0,1]
	v_mul_f32_e32 v3, 0x42000000, v45
	v_mul_f32_e32 v35, 0x42000000, v47
	v_med3_f32 v3, v3, s83, v238
	v_med3_f32 v38, v35, s83, v238
	v_mov_b32_e32 v35, v0
	v_cvt_pk_fp8_f32 v35, v3, v38
	v_mul_f32_e32 v36, 0x42000000, v49
	v_mul_f32_e32 v37, 0x42000000, v53
	v_med3_f32 v36, v36, s83, v238
	v_med3_f32 v37, v37, s83, v238
	v_cvt_pk_fp8_f32 v35, v36, v37 op_sel:[0,0,1]
	v_lshl_add_u64 v[32:33], s[8:9], 0, v[6:7]
	v_lshl_add_u64 v[36:37], v[32:33], 0, v[10:11]
	ds_read2_b32 v[44:45], v50 offset0:148 offset1:156
	global_store_dwordx2 v[36:37], v[34:35], off
	ds_read2_b32 v[34:35], v50 offset0:16 offset1:24
	ds_read2_b32 v[36:37], v50 offset0:49 offset1:57
	ds_read2_b32 v[46:47], v50 offset0:181 offset1:189
	ds_read2_b32 v[38:39], v50 offset0:82 offset1:90
	ds_read2_b32 v[40:41], v50 offset0:115 offset1:123
	v_lshl_add_u64 v[54:55], v[32:33], 0, v[8:9]
	s_waitcnt lgkmcnt(4)
; #define LAS __attribute__((address_space(3)))
; #define LDS_WAIT() asm volatile("s_waitcnt lgkmcnt(0)" ::: "memory")
; __device__ __forceinline__ void p0_transpose_item8(const float* W, int ldw, int srccol0, int k0, unsigned char* dst, int K, LAS float* scr, int lane) {
;     ...
;     LDS_WAIT(); asm volatile("" ::: "memory");
;     const int c = lane & 7;
; #pragma unroll
;     for (int j = 0; j < 4; ++j) { const int n = (lane >> 3) + 8 * j; const LAS float* s = scr + (8 * c) * 33 + n;
;         u32x2 o; o.x = pk4_f8(s[0 * 33] * 32.f, s[1 * 33] * 32.f, s[2 * 33] * 32.f, s[3 * 33] * 32.f); o.y = pk4_f8(s[4 * 33] * 32.f, s[5 * 33] * 32.f, s[6 * 33] * 32.f, s[7 * 33] * 32.f);
;         *(u32x2*)(dst + (size_t)n * K + k0 + 8 * c) = o; }
;     LDS_WAIT(); asm volatile("" ::: "memory");
; __device__ __forceinline__ void p0_item(KP Pk, Frame& F, int it, LAS float* scr) {
;     ...
;     if (it < 32 * TI_GU) { const int le = it / TI_GU, r = it % TI_GU, kb = r / 64, nb = r % 64, n0 = 32 * nb, j = n0 >> 8, half = (n0 >> 7) & 1, c0 = 128 * j + (n0 & 127);
;         p0_transpose_item8((half ? Pk->in[I_EU] : Pk->in[I_EG]) + (size_t)le * D * DE, DE, c0, 64 * kb, ws + WS_WGU + ((size_t)le * 2048 + n0) * D, D, scr, F.lane); return; }
	v_mul_f32_e32 v3, 0x42000000, v34
	s_waitcnt lgkmcnt(3)
	v_mul_f32_e32 v34, 0x42000000, v36
	global_store_dwordx2 v[54:55], v[42:43], off
	v_med3_f32 v3, v3, s83, v238
	v_med3_f32 v34, v34, s83, v238
	v_mov_b32_e32 v42, v0
	ds_read2_b32 v[48:49], v50 offset0:214 offset1:222
	ds_read2_b32 v[52:53], v50 offset0:247 offset1:255
	v_cvt_pk_fp8_f32 v42, v3, v34
	v_mul_f32_e32 v3, 0x42000000, v44
	s_waitcnt lgkmcnt(4)
	v_mul_f32_e32 v34, 0x42000000, v46
	v_med3_f32 v3, v3, s83, v238
	v_med3_f32 v34, v34, s83, v238
	v_mov_b32_e32 v43, v0
	s_waitcnt lgkmcnt(3)
	v_mul_f32_e32 v36, 0x42000000, v38
	s_waitcnt lgkmcnt(2)
	v_mul_f32_e32 v38, 0x42000000, v40
	v_cvt_pk_fp8_f32 v43, v3, v34
	v_mul_f32_e32 v3, 0x42000000, v35
	v_mul_f32_e32 v34, 0x42000000, v37
	v_med3_f32 v36, v36, s83, v238
	v_med3_f32 v38, v38, s83, v238
	v_med3_f32 v3, v3, s83, v238
	v_med3_f32 v37, v34, s83, v238
	v_mov_b32_e32 v34, v0
	v_cvt_pk_fp8_f32 v42, v36, v38 op_sel:[0,0,1]
	s_waitcnt lgkmcnt(1)
	v_mul_f32_e32 v36, 0x42000000, v48
	s_waitcnt lgkmcnt(0)
	v_mul_f32_e32 v38, 0x42000000, v52
	v_cvt_pk_fp8_f32 v34, v3, v37
	v_med3_f32 v36, v36, s83, v238
	v_med3_f32 v38, v38, s83, v238
	v_cvt_pk_fp8_f32 v43, v36, v38 op_sel:[0,0,1]
	v_mul_f32_e32 v35, 0x42000000, v39
	v_mul_f32_e32 v36, 0x42000000, v41
	v_med3_f32 v35, v35, s83, v238
	v_med3_f32 v36, v36, s83, v238
	v_cvt_pk_fp8_f32 v34, v35, v36 op_sel:[0,0,1]
	v_mul_f32_e32 v3, 0x42000000, v45
	v_mul_f32_e32 v35, 0x42000000, v47
	v_med3_f32 v3, v3, s83, v238
	v_med3_f32 v38, v35, s83, v238
	v_mov_b32_e32 v35, v0
	v_cvt_pk_fp8_f32 v35, v3, v38
	v_mul_f32_e32 v36, 0x42000000, v49
	v_mul_f32_e32 v37, 0x42000000, v53
	v_med3_f32 v36, v36, s83, v238
	v_med3_f32 v37, v37, s83, v238
	v_cvt_pk_fp8_f32 v35, v36, v37 op_sel:[0,0,1]
	v_lshl_add_u64 v[54:55], v[32:33], 0, v[12:13]
	v_lshl_add_u64 v[32:33], v[32:33], 0, v[14:15]
	global_store_dwordx2 v[54:55], v[42:43], off
	global_store_dwordx2 v[32:33], v[34:35], off
	s_waitcnt lgkmcnt(0)
	s_mov_b64 s[8:9], 0
.LBB0_838:
	s_andn2_b64 vcc, exec, s[8:9]
	s_cbranch_vccnz .LBB0_840
	s_cmp_eq_u32 s43, 0
	s_cbranch_scc1 .Lcv_gu
	s_lshl_b32 s8, s4, 5
	s_lshl_b32 s9, s4, 4
	s_add_i32 s5, s4, 0xffffc5c0
	s_waitcnt lgkmcnt(0)
	s_and_b32 s26, s8, 0x7e0
	s_and_b32 s9, s9, 0x380
	s_and_b32 s8, s8, 0x60
	s_and_b32 s60, s5, 0xfffff800
	s_and_b32 s5, s5, 0x7c0
	s_or_b32 s27, s9, s8
	s_bitcmp0_b32 s4, 2
	s_movk_i32 s8, 0xf8
	s_cselect_b32 s8, s8, 0x100
	s_add_u32 s8, s48, s8
	s_addc_u32 s9, s49, 0
	s_load_dwordx2 s[8:9], s[8:9], 0x0
	s_lshl_b64 s[18:19], s[60:61], 12
	v_add_u32_e32 v32, s5, v2
	v_lshlrev_b32_e32 v34, 2, v4
	v_mov_b32_e32 v35, v0
	s_waitcnt lgkmcnt(0)
	s_add_u32 s18, s8, s18
	s_addc_u32 s19, s9, s19
	s_or_b32 s60, s60, s26
	s_lshl_b64 s[8:9], s[60:61], 11
	v_readlane_b32 s26, v255, 9
	s_add_u32 s26, s26, s8
	v_readlane_b32 s8, v255, 10
	s_addc_u32 s34, s8, s9
	s_lshl_b32 s8, s27, 2
	s_add_u32 s8, s18, s8
	s_addc_u32 s9, s19, 0
	v_ashrrev_i32_e32 v33, 31, v32
	v_lshl_add_u64 v[34:35], s[8:9], 0, v[34:35]
	v_lshlrev_b64 v[32:33], 12, v[32:33]
	v_lshl_add_u64 v[48:49], v[34:35], 0, v[32:33]
	s_mov_b32 s8, 0x8000
	v_add_co_u32_e32 v36, vcc, s8, v48
	global_load_dwordx4 v[32:35], v[48:49], off
	s_nop 0
	v_addc_co_u32_e32 v37, vcc, 0, v49, vcc
	s_mov_b32 s8, 0x10000
	global_load_dwordx4 v[36:39], v[36:37], off
	v_add_co_u32_e32 v40, vcc, s8, v48
	s_mov_b32 s8, 0x18000
	s_nop 0
	v_addc_co_u32_e32 v41, vcc, 0, v49, vcc
	global_load_dwordx4 v[40:43], v[40:41], off
	v_add_co_u32_e32 v44, vcc, s8, v48
	s_mov_b32 s8, 0x20000
	s_nop 0
	v_addc_co_u32_e32 v45, vcc, 0, v49, vcc
	global_load_dwordx4 v[44:47], v[44:45], off
	v_add_co_u32_e32 v52, vcc, s8, v48
	s_mov_b32 s8, 0x28000
	s_nop 0
	v_addc_co_u32_e32 v53, vcc, 0, v49, vcc
	global_load_dwordx4 v[52:55], v[52:53], off
	v_add_co_u32_e32 v56, vcc, s8, v48
	s_mov_b32 s8, 0x30000
	s_nop 0
	v_addc_co_u32_e32 v57, vcc, 0, v49, vcc
	global_load_dwordx4 v[56:59], v[56:57], off
	v_add_co_u32_e32 v60, vcc, s8, v48
	s_mov_b32 s8, 0x38000
	s_nop 0
	v_addc_co_u32_e32 v61, vcc, 0, v49, vcc
	global_load_dwordx4 v[60:63], v[60:61], off
	v_add_co_u32_e32 v48, vcc, s8, v48
	v_add_u32_e32 v3, v1, v5
	s_nop 0
	v_addc_co_u32_e32 v49, vcc, 0, v49, vcc
	global_load_dwordx4 v[64:67], v[48:49], off
	s_add_u32 s8, s26, s5
	s_addc_u32 s9, s34, 0
	s_waitcnt vmcnt(7)
	ds_write2_b32 v3, v32, v33 offset1:1
	ds_write2_b32 v3, v34, v35 offset0:2 offset1:3
	v_add_u32_e32 v32, 0x420, v3
	s_waitcnt vmcnt(6)
	ds_write2_b32 v32, v36, v37 offset1:1
	v_add_u32_e32 v32, 0x428, v3
	ds_write2_b32 v32, v38, v39 offset1:1
	v_add_u32_e32 v32, 0x840, v3
	s_waitcnt vmcnt(5)
	ds_write2_b32 v32, v40, v41 offset1:1
	v_add_u32_e32 v32, 0x848, v3
	ds_write2_b32 v32, v42, v43 offset1:1
	v_add_u32_e32 v32, 0xc60, v3
	v_mov_b32_e32 v42, v0
	v_mov_b32_e32 v43, v0
	s_waitcnt vmcnt(4)
	ds_write2_b32 v32, v44, v45 offset1:1
	v_add_u32_e32 v32, 0xc68, v3
	ds_write2_b32 v32, v46, v47 offset1:1
	v_add_u32_e32 v32, 0x1080, v3
	s_waitcnt vmcnt(3)
; #define LAS __attribute__((address_space(3)))
; #define LDS_WAIT() asm volatile("s_waitcnt lgkmcnt(0)" ::: "memory")
; __device__ __forceinline__ void p0_transpose_item8(const float* W, int ldw, int srccol0, int k0, unsigned char* dst, int K, LAS float* scr, int lane) {
;     { f32x4 v[8];
; #pragma unroll
;       for (int i = 0; i < 8; ++i) v[i] = *(const f32x4*)(W + (size_t)(k0 + 8 * i + (lane >> 3)) * ldw + srccol0 + 4 * (lane & 7));
; #pragma unroll
;       for (int i = 0; i < 8; ++i) { LAS float* p = scr + (8 * i + (lane >> 3)) * 33 + 4 * (lane & 7); p[0] = v[i][0]; p[1] = v[i][1]; p[2] = v[i][2]; p[3] = v[i][3]; } }
;     LDS_WAIT(); asm volatile("" ::: "memory");
;     const int c = lane & 7;
; #pragma unroll
;     for (int j = 0; j < 4; ++j) { const int n = (lane >> 3) + 8 * j; const LAS float* s = scr + (8 * c) * 33 + n;
;         u32x2 o; o.x = pk4_f8(s[0 * 33] * 32.f, s[1 * 33] * 32.f, s[2 * 33] * 32.f, s[3 * 33] * 32.f); o.y = pk4_f8(s[4 * 33] * 32.f, s[5 * 33] * 32.f, s[6 * 33] * 32.f, s[7 * 33] * 32.f);
;         *(u32x2*)(dst + (size_t)n * K + k0 + 8 * c) = o; }
;     LDS_WAIT(); asm volatile("" ::: "memory");
	ds_write2_b32 v32, v52, v53 offset1:1
	v_add_u32_e32 v32, 0x1088, v3
	ds_write2_b32 v32, v54, v55 offset1:1
	v_add_u32_e32 v32, 0x14a0, v3
	s_waitcnt vmcnt(2)
	ds_write2_b32 v32, v56, v57 offset1:1
	v_add_u32_e32 v32, 0x14a8, v3
	ds_write2_b32 v32, v58, v59 offset1:1
	v_add_u32_e32 v32, 0x18c0, v3
	s_waitcnt vmcnt(1)
	ds_write2_b32 v32, v60, v61 offset1:1
	v_add_u32_e32 v32, 0x18c8, v3
	ds_write2_b32 v32, v62, v63 offset1:1
	v_add_u32_e32 v32, 0x1ce0, v3
	v_add_u32_e32 v3, 0x1ce8, v3
	s_waitcnt vmcnt(0)
	ds_write2_b32 v32, v64, v65 offset1:1
	ds_write2_b32 v3, v66, v67 offset1:1
	s_waitcnt lgkmcnt(0)
	ds_read2_b32 v[34:35], v50 offset1:8
	ds_read2_b32 v[36:37], v50 offset0:33 offset1:41
	ds_read2_b32 v[44:45], v50 offset0:132 offset1:140
	ds_read2_b32 v[46:47], v50 offset0:165 offset1:173
	ds_read2_b32 v[38:39], v50 offset0:66 offset1:74
	ds_read2_b32 v[40:41], v50 offset0:99 offset1:107
	s_waitcnt lgkmcnt(5)
	v_mul_f32_e32 v3, 0x42000000, v34
	s_waitcnt lgkmcnt(4)
	v_mul_f32_e32 v34, 0x42000000, v36
	v_med3_f32 v3, v3, s83, v238
	v_med3_f32 v34, v34, s83, v238
	ds_read2_b32 v[48:49], v50 offset0:198 offset1:206
	ds_read2_b32 v[52:53], v50 offset0:231 offset1:239
	v_cvt_pk_fp8_f32 v42, v3, v34
	s_waitcnt lgkmcnt(5)
	v_mul_f32_e32 v3, 0x42000000, v44
	s_waitcnt lgkmcnt(4)
	v_mul_f32_e32 v34, 0x42000000, v46
	v_med3_f32 v3, v3, s83, v238
	v_med3_f32 v34, v34, s83, v238
	s_waitcnt lgkmcnt(3)
	v_mul_f32_e32 v36, 0x42000000, v38
	s_waitcnt lgkmcnt(2)
	v_mul_f32_e32 v38, 0x42000000, v40
	v_cvt_pk_fp8_f32 v43, v3, v34
	v_mul_f32_e32 v3, 0x42000000, v35
	v_mul_f32_e32 v34, 0x42000000, v37
	v_med3_f32 v36, v36, s83, v238
	v_med3_f32 v38, v38, s83, v238
	v_med3_f32 v3, v3, s83, v238
	v_med3_f32 v37, v34, s83, v238
	v_mov_b32_e32 v34, v0
	v_cvt_pk_fp8_f32 v42, v36, v38 op_sel:[0,0,1]
	s_waitcnt lgkmcnt(1)
	v_mul_f32_e32 v36, 0x42000000, v48
	s_waitcnt lgkmcnt(0)
	v_mul_f32_e32 v38, 0x42000000, v52
	v_cvt_pk_fp8_f32 v34, v3, v37
	v_med3_f32 v36, v36, s83, v238
	v_med3_f32 v38, v38, s83, v238
	v_cvt_pk_fp8_f32 v43, v36, v38 op_sel:[0,0,1]
	v_mul_f32_e32 v35, 0x42000000, v39
	v_mul_f32_e32 v36, 0x42000000, v41
	v_med3_f32 v35, v35, s83, v238
	v_med3_f32 v36, v36, s83, v238
	v_cvt_pk_fp8_f32 v34, v35, v36 op_sel:[0,0,1]
	v_mul_f32_e32 v3, 0x42000000, v45
	v_mul_f32_e32 v35, 0x42000000, v47
	v_med3_f32 v3, v3, s83, v238
	v_med3_f32 v38, v35, s83, v238
	v_mov_b32_e32 v35, v0
	v_cvt_pk_fp8_f32 v35, v3, v38
	v_mul_f32_e32 v36, 0x42000000, v49
	v_mul_f32_e32 v37, 0x42000000, v53
	v_med3_f32 v36, v36, s83, v238
	v_med3_f32 v37, v37, s83, v238
	v_cvt_pk_fp8_f32 v35, v36, v37 op_sel:[0,0,1]
	v_lshl_add_u64 v[32:33], s[8:9], 0, v[6:7]
	v_lshl_add_u64 v[36:37], v[32:33], 0, v[18:19]
	ds_read2_b32 v[44:45], v50 offset0:148 offset1:156
	global_store_dwordx2 v[36:37], v[34:35], off
	ds_read2_b32 v[34:35], v50 offset0:16 offset1:24
	ds_read2_b32 v[36:37], v50 offset0:49 offset1:57
	ds_read2_b32 v[46:47], v50 offset0:181 offset1:189
	ds_read2_b32 v[38:39], v50 offset0:82 offset1:90
	ds_read2_b32 v[40:41], v50 offset0:115 offset1:123
	v_lshl_add_u64 v[54:55], v[32:33], 0, v[16:17]
	s_waitcnt lgkmcnt(4)
	v_mul_f32_e32 v3, 0x42000000, v34
	s_waitcnt lgkmcnt(3)
	v_mul_f32_e32 v34, 0x42000000, v36
	global_store_dwordx2 v[54:55], v[42:43], off
	v_med3_f32 v3, v3, s83, v238
	v_med3_f32 v34, v34, s83, v238
	v_mov_b32_e32 v42, v0
	ds_read2_b32 v[48:49], v50 offset0:214 offset1:222
	ds_read2_b32 v[52:53], v50 offset0:247 offset1:255
	v_cvt_pk_fp8_f32 v42, v3, v34
	v_mul_f32_e32 v3, 0x42000000, v44
	s_waitcnt lgkmcnt(4)
	v_mul_f32_e32 v34, 0x42000000, v46
	v_med3_f32 v3, v3, s83, v238
	v_med3_f32 v34, v34, s83, v238
	v_mov_b32_e32 v43, v0
	s_waitcnt lgkmcnt(3)
	v_mul_f32_e32 v36, 0x42000000, v38
	s_waitcnt lgkmcnt(2)
	v_mul_f32_e32 v38, 0x42000000, v40
	v_cvt_pk_fp8_f32 v43, v3, v34
	v_mul_f32_e32 v3, 0x42000000, v35
	v_mul_f32_e32 v34, 0x42000000, v37
	v_med3_f32 v36, v36, s83, v238
	v_med3_f32 v38, v38, s83, v238
	v_med3_f32 v3, v3, s83, v238
	v_med3_f32 v37, v34, s83, v238
	v_mov_b32_e32 v34, v0
	v_cvt_pk_fp8_f32 v42, v36, v38 op_sel:[0,0,1]
	s_waitcnt lgkmcnt(1)
	v_mul_f32_e32 v36, 0x42000000, v48
	s_waitcnt lgkmcnt(0)
	v_mul_f32_e32 v38, 0x42000000, v52
	v_cvt_pk_fp8_f32 v34, v3, v37
	v_med3_f32 v36, v36, s83, v238
	v_med3_f32 v38, v38, s83, v238
	v_cvt_pk_fp8_f32 v43, v36, v38 op_sel:[0,0,1]
	v_mul_f32_e32 v35, 0x42000000, v39
	v_mul_f32_e32 v36, 0x42000000, v41
	v_med3_f32 v35, v35, s83, v238
	v_med3_f32 v36, v36, s83, v238
	v_cvt_pk_fp8_f32 v34, v35, v36 op_sel:[0,0,1]
	v_mul_f32_e32 v3, 0x42000000, v45
	v_mul_f32_e32 v35, 0x42000000, v47
	v_med3_f32 v3, v3, s83, v238
	v_med3_f32 v38, v35, s83, v238
	v_mov_b32_e32 v35, v0
	v_cvt_pk_fp8_f32 v35, v3, v38
	v_mul_f32_e32 v36, 0x42000000, v49
	v_mul_f32_e32 v37, 0x42000000, v53
	v_med3_f32 v36, v36, s83, v238
	v_med3_f32 v37, v37, s83, v238
	v_cvt_pk_fp8_f32 v35, v36, v37 op_sel:[0,0,1]
	v_lshl_add_u64 v[54:55], v[32:33], 0, v[20:21]
	v_lshl_add_u64 v[32:33], v[32:33], 0, v[22:23]
	global_store_dwordx2 v[54:55], v[42:43], off
	global_store_dwordx2 v[32:33], v[34:35], off
	s_waitcnt lgkmcnt(0)
